# LRU v3: gate loads requested at chunk top (registers remapped)
# baseline (speedup 1.0000x reference)
.Lmylru_nodma_1:
	v_mov_b32_e32 v163, v162
	ds_read_b128 v[96:99], v163
	ds_read_b128 v[100:103], v163 offset:8192
	ds_read_b128 v[104:107], v163 offset:16384
	ds_read_b128 v[108:111], v163 offset:24576
	v_xor_b32_e32 v164, 0x40, v163
	ds_read_b128 v[112:115], v164
	ds_read_b128 v[116:119], v164 offset:8192
	ds_read_b128 v[120:123], v164 offset:16384
	ds_read_b128 v[124:127], v164 offset:24576
	s_waitcnt lgkmcnt(7)
	v_mfma_f32_16x16x32_bf16 v[64:67], v[96:99], v[0:3], 0
	v_mfma_f32_16x16x32_bf16 v[68:71], v[96:99], v[32:35], 0
	v_xor_b32_e32 v164, 0x80, v163
	ds_read_b128 v[96:99], v164
	s_waitcnt lgkmcnt(7)
	v_mfma_f32_16x16x32_bf16 v[72:75], v[100:103], v[0:3], 0
	v_mfma_f32_16x16x32_bf16 v[76:79], v[100:103], v[32:35], 0
	ds_read_b128 v[100:103], v164 offset:8192
	s_waitcnt lgkmcnt(7)
	v_mfma_f32_16x16x32_bf16 v[80:83], v[104:107], v[0:3], 0
	v_mfma_f32_16x16x32_bf16 v[84:87], v[104:107], v[32:35], 0
	ds_read_b128 v[104:107], v164 offset:16384
	s_waitcnt lgkmcnt(7)
	v_mfma_f32_16x16x32_bf16 v[88:91], v[108:111], v[0:3], 0
	v_mfma_f32_16x16x32_bf16 v[92:95], v[108:111], v[32:35], 0
	ds_read_b128 v[108:111], v164 offset:24576
	s_waitcnt lgkmcnt(7)
	v_mfma_f32_16x16x32_bf16 v[64:67], v[112:115], v[4:7], v[64:67]
	v_mfma_f32_16x16x32_bf16 v[68:71], v[112:115], v[36:39], v[68:71]
	v_xor_b32_e32 v164, 0xc0, v163
	ds_read_b128 v[112:115], v164
	s_waitcnt lgkmcnt(7)
	v_mfma_f32_16x16x32_bf16 v[72:75], v[116:119], v[4:7], v[72:75]
	v_mfma_f32_16x16x32_bf16 v[76:79], v[116:119], v[36:39], v[76:79]
	ds_read_b128 v[116:119], v164 offset:8192
	s_waitcnt lgkmcnt(7)
	v_mfma_f32_16x16x32_bf16 v[80:83], v[120:123], v[4:7], v[80:83]
	v_mfma_f32_16x16x32_bf16 v[84:87], v[120:123], v[36:39], v[84:87]
	ds_read_b128 v[120:123], v164 offset:16384
	s_waitcnt lgkmcnt(7)
	v_mfma_f32_16x16x32_bf16 v[88:91], v[124:127], v[4:7], v[88:91]
	v_mfma_f32_16x16x32_bf16 v[92:95], v[124:127], v[36:39], v[92:95]
	ds_read_b128 v[124:127], v164 offset:24576
	s_waitcnt lgkmcnt(7)
	v_mfma_f32_16x16x32_bf16 v[64:67], v[96:99], v[8:11], v[64:67]
	v_mfma_f32_16x16x32_bf16 v[68:71], v[96:99], v[40:43], v[68:71]
	v_xor_b32_e32 v164, 0x100, v163
	ds_read_b128 v[96:99], v164
	s_waitcnt lgkmcnt(7)
	v_mfma_f32_16x16x32_bf16 v[72:75], v[100:103], v[8:11], v[72:75]
	v_mfma_f32_16x16x32_bf16 v[76:79], v[100:103], v[40:43], v[76:79]
	ds_read_b128 v[100:103], v164 offset:8192
	s_waitcnt lgkmcnt(7)
	v_mfma_f32_16x16x32_bf16 v[80:83], v[104:107], v[8:11], v[80:83]
	v_mfma_f32_16x16x32_bf16 v[84:87], v[104:107], v[40:43], v[84:87]
	ds_read_b128 v[104:107], v164 offset:16384
	s_waitcnt lgkmcnt(7)
	v_mfma_f32_16x16x32_bf16 v[88:91], v[108:111], v[8:11], v[88:91]
	v_mfma_f32_16x16x32_bf16 v[92:95], v[108:111], v[40:43], v[92:95]
	ds_read_b128 v[108:111], v164 offset:24576
	s_waitcnt lgkmcnt(7)
	v_mfma_f32_16x16x32_bf16 v[64:67], v[112:115], v[12:15], v[64:67]
	v_mfma_f32_16x16x32_bf16 v[68:71], v[112:115], v[44:47], v[68:71]
	v_xor_b32_e32 v164, 0x140, v163
	ds_read_b128 v[112:115], v164
	s_waitcnt lgkmcnt(7)
	v_mfma_f32_16x16x32_bf16 v[72:75], v[116:119], v[12:15], v[72:75]
	v_mfma_f32_16x16x32_bf16 v[76:79], v[116:119], v[44:47], v[76:79]
	ds_read_b128 v[116:119], v164 offset:8192
	s_waitcnt lgkmcnt(7)
	v_mfma_f32_16x16x32_bf16 v[80:83], v[120:123], v[12:15], v[80:83]
	v_mfma_f32_16x16x32_bf16 v[84:87], v[120:123], v[44:47], v[84:87]
	ds_read_b128 v[120:123], v164 offset:16384
	s_waitcnt lgkmcnt(7)
	v_mfma_f32_16x16x32_bf16 v[88:91], v[124:127], v[12:15], v[88:91]
	v_mfma_f32_16x16x32_bf16 v[92:95], v[124:127], v[44:47], v[92:95]
	ds_read_b128 v[124:127], v164 offset:24576
	s_waitcnt lgkmcnt(7)
	v_mfma_f32_16x16x32_bf16 v[64:67], v[96:99], v[16:19], v[64:67]
	v_mfma_f32_16x16x32_bf16 v[68:71], v[96:99], v[48:51], v[68:71]
	v_xor_b32_e32 v164, 0x180, v163
	ds_read_b128 v[96:99], v164
	s_waitcnt lgkmcnt(7)
	v_mfma_f32_16x16x32_bf16 v[72:75], v[100:103], v[16:19], v[72:75]
	v_mfma_f32_16x16x32_bf16 v[76:79], v[100:103], v[48:51], v[76:79]
	ds_read_b128 v[100:103], v164 offset:8192
	s_waitcnt lgkmcnt(7)
	v_mfma_f32_16x16x32_bf16 v[80:83], v[104:107], v[16:19], v[80:83]
	v_mfma_f32_16x16x32_bf16 v[84:87], v[104:107], v[48:51], v[84:87]
	ds_read_b128 v[104:107], v164 offset:16384
	s_waitcnt lgkmcnt(7)
	v_mfma_f32_16x16x32_bf16 v[88:91], v[108:111], v[16:19], v[88:91]
	v_mfma_f32_16x16x32_bf16 v[92:95], v[108:111], v[48:51], v[92:95]
	ds_read_b128 v[108:111], v164 offset:24576
	s_waitcnt lgkmcnt(7)
	v_mfma_f32_16x16x32_bf16 v[64:67], v[112:115], v[20:23], v[64:67]
	v_mfma_f32_16x16x32_bf16 v[68:71], v[112:115], v[52:55], v[68:71]
	v_xor_b32_e32 v164, 0x1c0, v163
	ds_read_b128 v[112:115], v164
	s_waitcnt lgkmcnt(7)
	v_mfma_f32_16x16x32_bf16 v[72:75], v[116:119], v[20:23], v[72:75]
	v_mfma_f32_16x16x32_bf16 v[76:79], v[116:119], v[52:55], v[76:79]
	ds_read_b128 v[116:119], v164 offset:8192
	s_waitcnt lgkmcnt(7)
	v_mfma_f32_16x16x32_bf16 v[80:83], v[120:123], v[20:23], v[80:83]
	v_mfma_f32_16x16x32_bf16 v[84:87], v[120:123], v[52:55], v[84:87]
	ds_read_b128 v[120:123], v164 offset:16384
	s_waitcnt lgkmcnt(7)
	v_mfma_f32_16x16x32_bf16 v[88:91], v[124:127], v[20:23], v[88:91]
	v_mfma_f32_16x16x32_bf16 v[92:95], v[124:127], v[52:55], v[92:95]
	ds_read_b128 v[124:127], v164 offset:24576
	s_waitcnt lgkmcnt(7)
	v_mfma_f32_16x16x32_bf16 v[64:67], v[96:99], v[24:27], v[64:67]
	v_mfma_f32_16x16x32_bf16 v[68:71], v[96:99], v[56:59], v[68:71]
	s_waitcnt lgkmcnt(6)
	v_mfma_f32_16x16x32_bf16 v[72:75], v[100:103], v[24:27], v[72:75]
	v_mfma_f32_16x16x32_bf16 v[76:79], v[100:103], v[56:59], v[76:79]
	s_waitcnt lgkmcnt(5)
	v_mfma_f32_16x16x32_bf16 v[80:83], v[104:107], v[24:27], v[80:83]
	v_mfma_f32_16x16x32_bf16 v[84:87], v[104:107], v[56:59], v[84:87]
	s_waitcnt lgkmcnt(4)
	v_mfma_f32_16x16x32_bf16 v[88:91], v[108:111], v[24:27], v[88:91]
	v_mfma_f32_16x16x32_bf16 v[92:95], v[108:111], v[56:59], v[92:95]
	s_waitcnt lgkmcnt(3)
	v_mfma_f32_16x16x32_bf16 v[64:67], v[112:115], v[28:31], v[64:67]
	v_mfma_f32_16x16x32_bf16 v[68:71], v[112:115], v[60:63], v[68:71]
	s_waitcnt lgkmcnt(2)
	v_mfma_f32_16x16x32_bf16 v[72:75], v[116:119], v[28:31], v[72:75]
	v_mfma_f32_16x16x32_bf16 v[76:79], v[116:119], v[60:63], v[76:79]
	s_waitcnt lgkmcnt(1)
	v_mfma_f32_16x16x32_bf16 v[80:83], v[120:123], v[28:31], v[80:83]
	v_mfma_f32_16x16x32_bf16 v[84:87], v[120:123], v[60:63], v[84:87]
	s_waitcnt lgkmcnt(0)
	v_mfma_f32_16x16x32_bf16 v[88:91], v[124:127], v[28:31], v[88:91]
	v_mfma_f32_16x16x32_bf16 v[92:95], v[124:127], v[60:63], v[92:95]
	v_mov_b32_e32 v169, v165
	v_mov_b32_e32 v170, v166
	v_mov_b32_e32 v171, v167
	v_mov_b32_e32 v172, v168
	ds_read_u16 v144, v169
	ds_read_u16 v145, v170
	ds_read_u16 v146, v171
	ds_read_u16 v147, v172
	ds_read_u16 v148, v169 offset:8192
	ds_read_u16 v149, v170 offset:8192
	ds_read_u16 v150, v171 offset:8192
	ds_read_u16 v151, v172 offset:8192
	ds_read_u16 v152, v169 offset:16384
	ds_read_u16 v153, v170 offset:16384
	ds_read_u16 v154, v171 offset:16384
	ds_read_u16 v155, v172 offset:16384
	ds_read_u16 v156, v169 offset:24576
	ds_read_u16 v157, v170 offset:24576
	ds_read_u16 v158, v171 offset:24576
	ds_read_u16 v159, v172 offset:24576
	s_nop 7
	v_fma_f32 v178, v64, s53, v173
	v_fma_f32 v179, v65, s53, v173
	v_fma_f32 v180, v66, s53, v173
	v_fma_f32 v181, v67, s53, v173
	v_fma_f32 v182, v72, s53, v173
	v_fma_f32 v183, v73, s53, v173
	v_fma_f32 v184, v74, s53, v173
	v_fma_f32 v185, v75, s53, v173
	v_fma_f32 v186, v68, s53, v174
	v_fma_f32 v187, v69, s53, v174
	v_fma_f32 v188, v70, s53, v174
	v_fma_f32 v189, v71, s53, v174
	v_fma_f32 v190, v76, s53, v174
	v_fma_f32 v191, v77, s53, v174
	v_fma_f32 v192, v78, s53, v174
	v_fma_f32 v193, v79, s53, v174
	v_exp_f32_e32 v178, v178
	v_exp_f32_e32 v179, v179
	v_exp_f32_e32 v180, v180
	v_exp_f32_e32 v181, v181
	v_exp_f32_e32 v182, v182
	v_exp_f32_e32 v183, v183
	v_exp_f32_e32 v184, v184
	v_exp_f32_e32 v185, v185
	v_exp_f32_e32 v186, v186
	v_exp_f32_e32 v187, v187
	v_exp_f32_e32 v188, v188
	v_exp_f32_e32 v189, v189
	v_exp_f32_e32 v190, v190
	v_exp_f32_e32 v191, v191
	v_exp_f32_e32 v192, v192
	v_exp_f32_e32 v193, v193
	v_add_f32_e32 v178, 1.0, v178
	v_add_f32_e32 v179, 1.0, v179
	v_add_f32_e32 v180, 1.0, v180
	v_add_f32_e32 v181, 1.0, v181
	v_add_f32_e32 v182, 1.0, v182
	v_add_f32_e32 v183, 1.0, v183
	v_add_f32_e32 v184, 1.0, v184
	v_add_f32_e32 v185, 1.0, v185
	v_add_f32_e32 v186, 1.0, v186
	v_add_f32_e32 v187, 1.0, v187
	v_add_f32_e32 v188, 1.0, v188
	v_add_f32_e32 v189, 1.0, v189
	v_add_f32_e32 v190, 1.0, v190
	v_add_f32_e32 v191, 1.0, v191
	v_add_f32_e32 v192, 1.0, v192
	v_add_f32_e32 v193, 1.0, v193
	v_rcp_f32_e32 v178, v178
	v_rcp_f32_e32 v179, v179
	v_rcp_f32_e32 v180, v180
	v_rcp_f32_e32 v181, v181
	v_rcp_f32_e32 v182, v182
	v_rcp_f32_e32 v183, v183
	v_rcp_f32_e32 v184, v184
	v_rcp_f32_e32 v185, v185
	v_rcp_f32_e32 v186, v186
	v_rcp_f32_e32 v187, v187
	v_rcp_f32_e32 v188, v188
	v_rcp_f32_e32 v189, v189
	v_rcp_f32_e32 v190, v190
	v_rcp_f32_e32 v191, v191
	v_rcp_f32_e32 v192, v192
	v_rcp_f32_e32 v193, v193
	v_mul_f32_e32 v178, v175, v178
	v_mul_f32_e32 v179, v175, v179
	v_mul_f32_e32 v180, v175, v180
	v_mul_f32_e32 v181, v175, v181
	v_mul_f32_e32 v182, v175, v182
	v_mul_f32_e32 v183, v175, v183
	v_mul_f32_e32 v184, v175, v184
	v_mul_f32_e32 v185, v175, v185
	v_exp_f32_e32 v96, v178
	v_exp_f32_e32 v97, v179
	v_exp_f32_e32 v98, v180
	v_exp_f32_e32 v99, v181
	v_exp_f32_e32 v100, v182
	v_exp_f32_e32 v101, v183
	v_exp_f32_e32 v102, v184
	v_exp_f32_e32 v103, v185
	s_nop 0
	v_fma_f32 v194, -v96, v96, 1.0
	v_fma_f32 v195, -v97, v97, 1.0
	v_fma_f32 v196, -v98, v98, 1.0
	v_fma_f32 v197, -v99, v99, 1.0
	v_fma_f32 v198, -v100, v100, 1.0
	v_fma_f32 v199, -v101, v101, 1.0
	v_fma_f32 v200, -v102, v102, 1.0
	v_fma_f32 v201, -v103, v103, 1.0
	v_max_f32_e32 v194, 0, v194
	v_max_f32_e32 v195, 0, v195
	v_max_f32_e32 v196, 0, v196
	v_max_f32_e32 v197, 0, v197
	v_max_f32_e32 v198, 0, v198
	v_max_f32_e32 v199, 0, v199
	v_max_f32_e32 v200, 0, v200
	v_max_f32_e32 v201, 0, v201
	v_sqrt_f32_e32 v194, v194
	v_sqrt_f32_e32 v195, v195
	v_sqrt_f32_e32 v196, v196
	v_sqrt_f32_e32 v197, v197
	v_sqrt_f32_e32 v198, v198
	v_sqrt_f32_e32 v199, v199
	v_sqrt_f32_e32 v200, v200
	v_sqrt_f32_e32 v201, v201
	s_waitcnt lgkmcnt(8)
	v_lshlrev_b32_e32 v144, 16, v144
	v_lshlrev_b32_e32 v145, 16, v145
	v_lshlrev_b32_e32 v146, 16, v146
	v_lshlrev_b32_e32 v147, 16, v147
	v_lshlrev_b32_e32 v148, 16, v148
	v_lshlrev_b32_e32 v149, 16, v149
	v_lshlrev_b32_e32 v150, 16, v150
	v_lshlrev_b32_e32 v151, 16, v151
	v_mul_f32_e32 v194, v194, v186
	v_mul_f32_e32 v195, v195, v187
	v_mul_f32_e32 v196, v196, v188
	v_mul_f32_e32 v197, v197, v189
	v_mul_f32_e32 v198, v198, v190
	v_mul_f32_e32 v199, v199, v191
	v_mul_f32_e32 v200, v200, v192
	v_mul_f32_e32 v201, v201, v193
	v_mul_f32_e32 v144, v194, v144
	v_mul_f32_e32 v145, v195, v145
	v_mul_f32_e32 v146, v196, v146
	v_mul_f32_e32 v147, v197, v147
	v_mul_f32_e32 v148, v198, v148
	v_mul_f32_e32 v149, v199, v149
	v_mul_f32_e32 v150, v200, v150
	v_mul_f32_e32 v151, v201, v151
	v_fma_f32 v178, v80, s53, v173
	v_fma_f32 v179, v81, s53, v173
	v_fma_f32 v180, v82, s53, v173
	v_fma_f32 v181, v83, s53, v173
	v_fma_f32 v182, v88, s53, v173
	v_fma_f32 v183, v89, s53, v173
	v_fma_f32 v184, v90, s53, v173
	v_fma_f32 v185, v91, s53, v173
	v_fma_f32 v186, v84, s53, v174
	v_fma_f32 v187, v85, s53, v174
	v_fma_f32 v188, v86, s53, v174
	v_fma_f32 v189, v87, s53, v174
	v_fma_f32 v190, v92, s53, v174
	v_fma_f32 v191, v93, s53, v174
	v_fma_f32 v192, v94, s53, v174
	v_fma_f32 v193, v95, s53, v174
	v_exp_f32_e32 v178, v178
	v_exp_f32_e32 v179, v179
	v_exp_f32_e32 v180, v180
	v_exp_f32_e32 v181, v181
	v_exp_f32_e32 v182, v182
	v_exp_f32_e32 v183, v183
	v_exp_f32_e32 v184, v184
	v_exp_f32_e32 v185, v185
	v_exp_f32_e32 v186, v186
	v_exp_f32_e32 v187, v187
	v_exp_f32_e32 v188, v188
	v_exp_f32_e32 v189, v189
	v_exp_f32_e32 v190, v190
	v_exp_f32_e32 v191, v191
	v_exp_f32_e32 v192, v192
	v_exp_f32_e32 v193, v193
	v_add_f32_e32 v178, 1.0, v178
	v_add_f32_e32 v179, 1.0, v179
	v_add_f32_e32 v180, 1.0, v180
	v_add_f32_e32 v181, 1.0, v181
	v_add_f32_e32 v182, 1.0, v182
	v_add_f32_e32 v183, 1.0, v183
	v_add_f32_e32 v184, 1.0, v184
	v_add_f32_e32 v185, 1.0, v185
	v_add_f32_e32 v186, 1.0, v186
	v_add_f32_e32 v187, 1.0, v187
	v_add_f32_e32 v188, 1.0, v188
	v_add_f32_e32 v189, 1.0, v189
	v_add_f32_e32 v190, 1.0, v190
	v_add_f32_e32 v191, 1.0, v191
	v_add_f32_e32 v192, 1.0, v192
	v_add_f32_e32 v193, 1.0, v193
	v_rcp_f32_e32 v178, v178
	v_rcp_f32_e32 v179, v179
	v_rcp_f32_e32 v180, v180
	v_rcp_f32_e32 v181, v181
	v_rcp_f32_e32 v182, v182
	v_rcp_f32_e32 v183, v183
	v_rcp_f32_e32 v184, v184
	v_rcp_f32_e32 v185, v185
	v_rcp_f32_e32 v186, v186
	v_rcp_f32_e32 v187, v187
	v_rcp_f32_e32 v188, v188
	v_rcp_f32_e32 v189, v189
	v_rcp_f32_e32 v190, v190
	v_rcp_f32_e32 v191, v191
	v_rcp_f32_e32 v192, v192
	v_rcp_f32_e32 v193, v193
	v_mul_f32_e32 v178, v175, v178
	v_mul_f32_e32 v179, v175, v179
	v_mul_f32_e32 v180, v175, v180
	v_mul_f32_e32 v181, v175, v181
	v_mul_f32_e32 v182, v175, v182
	v_mul_f32_e32 v183, v175, v183
	v_mul_f32_e32 v184, v175, v184
	v_mul_f32_e32 v185, v175, v185
	v_exp_f32_e32 v104, v178
	v_exp_f32_e32 v105, v179
	v_exp_f32_e32 v106, v180
	v_exp_f32_e32 v107, v181
	v_exp_f32_e32 v108, v182
	v_exp_f32_e32 v109, v183
	v_exp_f32_e32 v110, v184
	v_exp_f32_e32 v111, v185
	s_nop 0
	v_fma_f32 v194, -v104, v104, 1.0
	v_fma_f32 v195, -v105, v105, 1.0
	v_fma_f32 v196, -v106, v106, 1.0
	v_fma_f32 v197, -v107, v107, 1.0
	v_fma_f32 v198, -v108, v108, 1.0
	v_fma_f32 v199, -v109, v109, 1.0
	v_fma_f32 v200, -v110, v110, 1.0
	v_fma_f32 v201, -v111, v111, 1.0
	v_max_f32_e32 v194, 0, v194
	v_max_f32_e32 v195, 0, v195
	v_max_f32_e32 v196, 0, v196
	v_max_f32_e32 v197, 0, v197
	v_max_f32_e32 v198, 0, v198
	v_max_f32_e32 v199, 0, v199
	v_max_f32_e32 v200, 0, v200
	v_max_f32_e32 v201, 0, v201
	v_sqrt_f32_e32 v194, v194
	v_sqrt_f32_e32 v195, v195
	v_sqrt_f32_e32 v196, v196
	v_sqrt_f32_e32 v197, v197
	v_sqrt_f32_e32 v198, v198
	v_sqrt_f32_e32 v199, v199
	v_sqrt_f32_e32 v200, v200
	v_sqrt_f32_e32 v201, v201
	s_waitcnt lgkmcnt(0)
	v_lshlrev_b32_e32 v152, 16, v152
	v_lshlrev_b32_e32 v153, 16, v153
	v_lshlrev_b32_e32 v154, 16, v154
	v_lshlrev_b32_e32 v155, 16, v155
	v_lshlrev_b32_e32 v156, 16, v156
	v_lshlrev_b32_e32 v157, 16, v157
	v_lshlrev_b32_e32 v158, 16, v158
	v_lshlrev_b32_e32 v159, 16, v159
	v_mul_f32_e32 v194, v194, v186
	v_mul_f32_e32 v195, v195, v187
	v_mul_f32_e32 v196, v196, v188
	v_mul_f32_e32 v197, v197, v189
	v_mul_f32_e32 v198, v198, v190
	v_mul_f32_e32 v199, v199, v191
	v_mul_f32_e32 v200, v200, v192
	v_mul_f32_e32 v201, v201, v193
	v_mul_f32_e32 v152, v194, v152
	v_mul_f32_e32 v153, v195, v153
	v_mul_f32_e32 v154, v196, v154
	v_mul_f32_e32 v155, v197, v155
	v_mul_f32_e32 v156, v198, v156
	v_mul_f32_e32 v157, v199, v157
	v_mul_f32_e32 v158, v200, v158
	v_mul_f32_e32 v159, v201, v159
	v_fma_f32 v145, v97, v144, v145
	v_fma_f32 v149, v101, v148, v149
	v_fma_f32 v153, v105, v152, v153
	v_fma_f32 v157, v109, v156, v157
	v_mul_f32_e32 v97, v97, v96
	v_mul_f32_e32 v101, v101, v100
	v_mul_f32_e32 v105, v105, v104
	v_mul_f32_e32 v109, v109, v108
	v_fma_f32 v146, v98, v145, v146
	v_fma_f32 v150, v102, v149, v150
	v_fma_f32 v154, v106, v153, v154
	v_fma_f32 v158, v110, v157, v158
	v_mul_f32_e32 v98, v98, v97
	v_mul_f32_e32 v102, v102, v101
	v_mul_f32_e32 v106, v106, v105
	v_mul_f32_e32 v110, v110, v109
	v_fma_f32 v147, v99, v146, v147
	v_fma_f32 v151, v103, v150, v151
	v_fma_f32 v155, v107, v154, v155
	v_fma_f32 v159, v111, v158, v159
	v_mul_f32_e32 v99, v99, v98
	v_mul_f32_e32 v103, v103, v102
	v_mul_f32_e32 v107, v107, v106
	v_mul_f32_e32 v111, v111, v110
	ds_bpermute_b32 v178, v204, v99
	ds_bpermute_b32 v182, v204, v147
	ds_bpermute_b32 v179, v204, v103
	ds_bpermute_b32 v183, v204, v151
	ds_bpermute_b32 v180, v204, v107
	ds_bpermute_b32 v184, v204, v155
	ds_bpermute_b32 v181, v204, v111
	ds_bpermute_b32 v185, v204, v159
	s_waitcnt lgkmcnt(0)
	v_fma_f32 v186, v182, v99, v147
	v_cndmask_b32_e64 v178, 1.0, v178, s[34:35]
	v_fma_f32 v187, v183, v103, v151
	v_cndmask_b32_e64 v179, 1.0, v179, s[34:35]
	v_fma_f32 v188, v184, v107, v155
	v_cndmask_b32_e64 v180, 1.0, v180, s[34:35]
	v_fma_f32 v189, v185, v111, v159
	v_cndmask_b32_e64 v181, 1.0, v181, s[34:35]
	v_cndmask_b32_e64 v223, v147, v186, s[34:35]
	v_mul_f32_e32 v219, v99, v178
	v_cndmask_b32_e64 v224, v151, v187, s[34:35]
	v_mul_f32_e32 v220, v103, v179
	v_cndmask_b32_e64 v225, v155, v188, s[34:35]
	v_mul_f32_e32 v221, v107, v180
	v_cndmask_b32_e64 v226, v159, v189, s[34:35]
	v_mul_f32_e32 v222, v111, v181
	ds_bpermute_b32 v178, v205, v219
	ds_bpermute_b32 v182, v205, v223
	ds_bpermute_b32 v179, v205, v220
	ds_bpermute_b32 v183, v205, v224
	ds_bpermute_b32 v180, v205, v221
	ds_bpermute_b32 v184, v205, v225
	ds_bpermute_b32 v181, v205, v222
	ds_bpermute_b32 v185, v205, v226
	s_waitcnt lgkmcnt(0)
	v_fma_f32 v186, v182, v219, v223
	v_cndmask_b32_e64 v178, 1.0, v178, s[36:37]
	v_fma_f32 v187, v183, v220, v224
	v_cndmask_b32_e64 v179, 1.0, v179, s[36:37]
	v_fma_f32 v188, v184, v221, v225
	v_cndmask_b32_e64 v180, 1.0, v180, s[36:37]
	v_fma_f32 v189, v185, v222, v226
	v_cndmask_b32_e64 v181, 1.0, v181, s[36:37]
	v_cndmask_b32_e64 v223, v223, v186, s[36:37]
	v_mul_f32_e32 v219, v219, v178
	v_cndmask_b32_e64 v224, v224, v187, s[36:37]
	v_mul_f32_e32 v220, v220, v179
	v_cndmask_b32_e64 v225, v225, v188, s[36:37]
	v_mul_f32_e32 v221, v221, v180
	v_cndmask_b32_e64 v226, v226, v189, s[36:37]
	v_mul_f32_e32 v222, v222, v181
	ds_bpermute_b32 v227, v204, v219
	ds_bpermute_b32 v231, v204, v223
	ds_bpermute_b32 v235, v206, v219
	ds_bpermute_b32 v239, v206, v223
	ds_bpermute_b32 v228, v204, v220
	ds_bpermute_b32 v232, v204, v224
	ds_bpermute_b32 v236, v206, v220
	ds_bpermute_b32 v244, v206, v224
	ds_bpermute_b32 v229, v204, v221
	ds_bpermute_b32 v233, v204, v225
	ds_bpermute_b32 v237, v206, v221
	ds_bpermute_b32 v245, v206, v225
	ds_bpermute_b32 v230, v204, v222
	ds_bpermute_b32 v234, v204, v226
	ds_bpermute_b32 v238, v206, v222
	ds_bpermute_b32 v246, v206, v226
	s_waitcnt lgkmcnt(0)
	v_cndmask_b32_e64 v227, 1.0, v227, s[34:35]
	v_cndmask_b32_e64 v231, 0, v231, s[34:35]
	v_cndmask_b32_e64 v228, 1.0, v228, s[34:35]
	v_cndmask_b32_e64 v232, 0, v232, s[34:35]
	v_cndmask_b32_e64 v229, 1.0, v229, s[34:35]
	v_cndmask_b32_e64 v233, 0, v233, s[34:35]
	v_cndmask_b32_e64 v230, 1.0, v230, s[34:35]
	v_cndmask_b32_e64 v234, 0, v234, s[34:35]
	v_mov_b32_e32 v190, v235
	v_mov_b32_e32 v194, v239
	v_mov_b32_e32 v198, v190
	v_mov_b32_e32 v201, v194
	v_fma_f32 v194, v194, v236, v244
	v_mul_f32_e32 v190, v190, v236
	v_mov_b32_e32 v199, v190
	v_mov_b32_e32 v177, v194
	v_fma_f32 v194, v194, v237, v245
	v_mul_f32_e32 v190, v190, v237
	v_mov_b32_e32 v200, v190
	v_mov_b32_e32 v203, v194
	v_fma_f32 v194, v194, v238, v246
	v_mul_f32_e32 v190, v190, v238
	v_mov_b32_e32 v191, v194
	ds_write_b64 v207, v[190:191]
	s_waitcnt lgkmcnt(0)
	s_barrier
	ds_read_b64 v[178:179], v208
	ds_read_b64 v[180:181], v208 offset:512
	s_waitcnt lgkmcnt(0)
	v_fma_f32 v182, v176, v178, v179
	v_cndmask_b32_e64 v183, v176, v182, s[38:39]
	v_fma_f32 v176, v182, v180, v181
	s_add_i32 s13, s13, 1
	s_waitcnt vmcnt(0)
	s_barrier
	s_cmp_eq_u32 s13, 17
	s_cbranch_scc1 .Lmylru_nodma_2
	s_add_i32 s58, s13, 1
	s_cmp_lt_u32 s58, 2
	s_lshl_b32 s50, s58, 7
	s_lshl_b32 s51, s9, 8
	s_add_i32 s51, s51, 0x8000
	s_add_i32 s51, s51, s50
	s_lshl_b32 s59, s9, 11
	s_add_i32 s59, s59, s50
	s_addk_i32 s59, 0xff00
	s_cmp_lt_u32 s58, 2
	s_cselect_b32 s59, s51, s59
	s_lshl_b32 s52, s59, 11
	s_add_u32 s46, s16, s52
	s_addc_u32 s47, s17, 0
	s_lshl_b32 s52, s6, 13
	s_mov_b32 m0, s52
	s_add_i32 s52, s52, 0x400
	global_load_lds_dwordx4 v211, s[46:47]
	s_mov_b32 m0, s52
	s_add_i32 s52, s52, 0x400
	global_load_lds_dwordx4 v212, s[46:47]
	s_mov_b32 m0, s52
	s_add_i32 s52, s52, 0x400
	global_load_lds_dwordx4 v213, s[46:47]
	s_mov_b32 m0, s52
	s_add_i32 s52, s52, 0x400
	global_load_lds_dwordx4 v214, s[46:47]
	s_mov_b32 m0, s52
	s_add_i32 s52, s52, 0x400
	global_load_lds_dwordx4 v215, s[46:47]
	s_mov_b32 m0, s52
	s_add_i32 s52, s52, 0x400
	global_load_lds_dwordx4 v216, s[46:47]
	s_mov_b32 m0, s52
	s_add_i32 s52, s52, 0x400
	global_load_lds_dwordx4 v217, s[46:47]
	s_mov_b32 m0, s52
	s_nop 0
	global_load_lds_dwordx4 v218, s[46:47]
.Lmylru_nodma_2:
	v_or_b32_e32 v163, 0x10000, v162
	ds_read_b128 v[96:99], v163
	ds_read_b128 v[100:103], v163 offset:8192
	ds_read_b128 v[104:107], v163 offset:16384
	ds_read_b128 v[108:111], v163 offset:24576
	v_xor_b32_e32 v164, 0x40, v163
	ds_read_b128 v[112:115], v164
	ds_read_b128 v[116:119], v164 offset:8192
	ds_read_b128 v[120:123], v164 offset:16384
	ds_read_b128 v[124:127], v164 offset:24576
	s_waitcnt lgkmcnt(7)
	v_mfma_f32_16x16x32_bf16 v[64:67], v[96:99], v[0:3], 0
	v_mfma_f32_16x16x32_bf16 v[68:71], v[96:99], v[32:35], 0
	v_xor_b32_e32 v164, 0x80, v163
	ds_read_b128 v[96:99], v164
	s_waitcnt lgkmcnt(7)
	v_mfma_f32_16x16x32_bf16 v[72:75], v[100:103], v[0:3], 0
	v_mfma_f32_16x16x32_bf16 v[76:79], v[100:103], v[32:35], 0
	ds_read_b128 v[100:103], v164 offset:8192
	s_waitcnt lgkmcnt(7)
	v_mfma_f32_16x16x32_bf16 v[80:83], v[104:107], v[0:3], 0
	v_mfma_f32_16x16x32_bf16 v[84:87], v[104:107], v[32:35], 0
	ds_read_b128 v[104:107], v164 offset:16384
	s_waitcnt lgkmcnt(7)
	v_mfma_f32_16x16x32_bf16 v[88:91], v[108:111], v[0:3], 0
	v_mfma_f32_16x16x32_bf16 v[92:95], v[108:111], v[32:35], 0
	ds_read_b128 v[108:111], v164 offset:24576
	s_waitcnt lgkmcnt(7)
	v_mfma_f32_16x16x32_bf16 v[64:67], v[112:115], v[4:7], v[64:67]
	v_mfma_f32_16x16x32_bf16 v[68:71], v[112:115], v[36:39], v[68:71]
	v_xor_b32_e32 v164, 0xc0, v163
	ds_read_b128 v[112:115], v164
	s_waitcnt lgkmcnt(7)
	v_mfma_f32_16x16x32_bf16 v[72:75], v[116:119], v[4:7], v[72:75]
	v_mfma_f32_16x16x32_bf16 v[76:79], v[116:119], v[36:39], v[76:79]
	ds_read_b128 v[116:119], v164 offset:8192
	s_waitcnt lgkmcnt(7)
	v_mfma_f32_16x16x32_bf16 v[80:83], v[120:123], v[4:7], v[80:83]
	v_mfma_f32_16x16x32_bf16 v[84:87], v[120:123], v[36:39], v[84:87]
	ds_read_b128 v[120:123], v164 offset:16384
	s_waitcnt lgkmcnt(7)
	v_mfma_f32_16x16x32_bf16 v[88:91], v[124:127], v[4:7], v[88:91]
	v_mfma_f32_16x16x32_bf16 v[92:95], v[124:127], v[36:39], v[92:95]
	ds_read_b128 v[124:127], v164 offset:24576
	s_waitcnt lgkmcnt(7)
	v_mfma_f32_16x16x32_bf16 v[64:67], v[96:99], v[8:11], v[64:67]
	v_mfma_f32_16x16x32_bf16 v[68:71], v[96:99], v[40:43], v[68:71]
	v_xor_b32_e32 v164, 0x100, v163
	ds_read_b128 v[96:99], v164
	s_waitcnt lgkmcnt(7)
	v_mfma_f32_16x16x32_bf16 v[72:75], v[100:103], v[8:11], v[72:75]
	v_mfma_f32_16x16x32_bf16 v[76:79], v[100:103], v[40:43], v[76:79]
	ds_read_b128 v[100:103], v164 offset:8192
	s_waitcnt lgkmcnt(7)
	v_mfma_f32_16x16x32_bf16 v[80:83], v[104:107], v[8:11], v[80:83]
	v_mfma_f32_16x16x32_bf16 v[84:87], v[104:107], v[40:43], v[84:87]
	ds_read_b128 v[104:107], v164 offset:16384
	s_waitcnt lgkmcnt(7)
	v_mfma_f32_16x16x32_bf16 v[88:91], v[108:111], v[8:11], v[88:91]
	v_mfma_f32_16x16x32_bf16 v[92:95], v[108:111], v[40:43], v[92:95]
	ds_read_b128 v[108:111], v164 offset:24576
	s_waitcnt lgkmcnt(7)
	v_mfma_f32_16x16x32_bf16 v[64:67], v[112:115], v[12:15], v[64:67]
	v_mfma_f32_16x16x32_bf16 v[68:71], v[112:115], v[44:47], v[68:71]
	v_xor_b32_e32 v164, 0x140, v163
	ds_read_b128 v[112:115], v164
	s_waitcnt lgkmcnt(7)
	v_mfma_f32_16x16x32_bf16 v[72:75], v[116:119], v[12:15], v[72:75]
	v_mfma_f32_16x16x32_bf16 v[76:79], v[116:119], v[44:47], v[76:79]
	ds_read_b128 v[116:119], v164 offset:8192
	s_waitcnt lgkmcnt(7)
	v_mfma_f32_16x16x32_bf16 v[80:83], v[120:123], v[12:15], v[80:83]
	v_mfma_f32_16x16x32_bf16 v[84:87], v[120:123], v[44:47], v[84:87]
	ds_read_b128 v[120:123], v164 offset:16384
	s_waitcnt lgkmcnt(7)
	v_mfma_f32_16x16x32_bf16 v[88:91], v[124:127], v[12:15], v[88:91]
	v_mfma_f32_16x16x32_bf16 v[92:95], v[124:127], v[44:47], v[92:95]
	ds_read_b128 v[124:127], v164 offset:24576
	s_waitcnt lgkmcnt(7)
	v_mfma_f32_16x16x32_bf16 v[64:67], v[96:99], v[16:19], v[64:67]
	v_mfma_f32_16x16x32_bf16 v[68:71], v[96:99], v[48:51], v[68:71]
	v_xor_b32_e32 v164, 0x180, v163
	ds_read_b128 v[96:99], v164
	s_waitcnt lgkmcnt(7)
	v_mfma_f32_16x16x32_bf16 v[72:75], v[100:103], v[16:19], v[72:75]
	v_mfma_f32_16x16x32_bf16 v[76:79], v[100:103], v[48:51], v[76:79]
	ds_read_b128 v[100:103], v164 offset:8192
	s_waitcnt lgkmcnt(7)
	v_mfma_f32_16x16x32_bf16 v[80:83], v[104:107], v[16:19], v[80:83]
	v_mfma_f32_16x16x32_bf16 v[84:87], v[104:107], v[48:51], v[84:87]
	ds_read_b128 v[104:107], v164 offset:16384
	s_waitcnt lgkmcnt(7)
	v_mfma_f32_16x16x32_bf16 v[88:91], v[108:111], v[16:19], v[88:91]
	v_mfma_f32_16x16x32_bf16 v[92:95], v[108:111], v[48:51], v[92:95]
	ds_read_b128 v[108:111], v164 offset:24576
	s_waitcnt lgkmcnt(7)
	v_mfma_f32_16x16x32_bf16 v[64:67], v[112:115], v[20:23], v[64:67]
	v_mfma_f32_16x16x32_bf16 v[68:71], v[112:115], v[52:55], v[68:71]
	v_xor_b32_e32 v164, 0x1c0, v163
	ds_read_b128 v[112:115], v164
	s_waitcnt lgkmcnt(7)
	v_mfma_f32_16x16x32_bf16 v[72:75], v[116:119], v[20:23], v[72:75]
	v_mfma_f32_16x16x32_bf16 v[76:79], v[116:119], v[52:55], v[76:79]
	ds_read_b128 v[116:119], v164 offset:8192
	s_waitcnt lgkmcnt(7)
	v_mfma_f32_16x16x32_bf16 v[80:83], v[120:123], v[20:23], v[80:83]
	v_mfma_f32_16x16x32_bf16 v[84:87], v[120:123], v[52:55], v[84:87]
	ds_read_b128 v[120:123], v164 offset:16384
	s_waitcnt lgkmcnt(7)
	v_mfma_f32_16x16x32_bf16 v[88:91], v[124:127], v[20:23], v[88:91]
	v_mfma_f32_16x16x32_bf16 v[92:95], v[124:127], v[52:55], v[92:95]
	ds_read_b128 v[124:127], v164 offset:24576
	s_waitcnt lgkmcnt(7)
	v_mfma_f32_16x16x32_bf16 v[64:67], v[96:99], v[24:27], v[64:67]
	v_mfma_f32_16x16x32_bf16 v[68:71], v[96:99], v[56:59], v[68:71]
	s_waitcnt lgkmcnt(6)
	v_mfma_f32_16x16x32_bf16 v[72:75], v[100:103], v[24:27], v[72:75]
	v_mfma_f32_16x16x32_bf16 v[76:79], v[100:103], v[56:59], v[76:79]
	s_waitcnt lgkmcnt(5)
	v_mfma_f32_16x16x32_bf16 v[80:83], v[104:107], v[24:27], v[80:83]
	v_mfma_f32_16x16x32_bf16 v[84:87], v[104:107], v[56:59], v[84:87]
	s_waitcnt lgkmcnt(4)
	v_mfma_f32_16x16x32_bf16 v[88:91], v[108:111], v[24:27], v[88:91]
	v_mfma_f32_16x16x32_bf16 v[92:95], v[108:111], v[56:59], v[92:95]
	s_waitcnt lgkmcnt(3)
	v_mfma_f32_16x16x32_bf16 v[64:67], v[112:115], v[28:31], v[64:67]
	v_mfma_f32_16x16x32_bf16 v[68:71], v[112:115], v[60:63], v[68:71]
	s_waitcnt lgkmcnt(2)
	v_mfma_f32_16x16x32_bf16 v[72:75], v[116:119], v[28:31], v[72:75]
	v_mfma_f32_16x16x32_bf16 v[76:79], v[116:119], v[60:63], v[76:79]
	s_waitcnt lgkmcnt(1)
	v_mfma_f32_16x16x32_bf16 v[80:83], v[120:123], v[28:31], v[80:83]
	v_mfma_f32_16x16x32_bf16 v[84:87], v[120:123], v[60:63], v[84:87]
	s_waitcnt lgkmcnt(0)
	v_mfma_f32_16x16x32_bf16 v[88:91], v[124:127], v[28:31], v[88:91]
	v_mfma_f32_16x16x32_bf16 v[92:95], v[124:127], v[60:63], v[92:95]
	v_or_b32_e32 v169, 0x10000, v165
	v_or_b32_e32 v170, 0x10000, v166
	v_or_b32_e32 v171, 0x10000, v167
	v_or_b32_e32 v172, 0x10000, v168
	ds_read_u16 v144, v169
	ds_read_u16 v145, v170
	ds_read_u16 v146, v171
	ds_read_u16 v147, v172
	ds_read_u16 v148, v169 offset:8192
	ds_read_u16 v149, v170 offset:8192
	ds_read_u16 v150, v171 offset:8192
	ds_read_u16 v151, v172 offset:8192
	ds_read_u16 v152, v169 offset:16384
	ds_read_u16 v153, v170 offset:16384
	ds_read_u16 v154, v171 offset:16384
	ds_read_u16 v155, v172 offset:16384
	ds_read_u16 v156, v169 offset:24576
	ds_read_u16 v157, v170 offset:24576
	ds_read_u16 v158, v171 offset:24576
	ds_read_u16 v159, v172 offset:24576
	s_nop 7
	v_fma_f32 v178, v64, s53, v173
	v_fma_f32 v179, v65, s53, v173
	v_fma_f32 v180, v66, s53, v173
	v_fma_f32 v181, v67, s53, v173
	v_fma_f32 v182, v72, s53, v173
	v_fma_f32 v183, v73, s53, v173
	v_fma_f32 v184, v74, s53, v173
	v_fma_f32 v185, v75, s53, v173
	v_fma_f32 v186, v68, s53, v174
	v_fma_f32 v187, v69, s53, v174
	v_fma_f32 v188, v70, s53, v174
	v_fma_f32 v189, v71, s53, v174
	v_fma_f32 v190, v76, s53, v174
	v_fma_f32 v191, v77, s53, v174
	v_fma_f32 v192, v78, s53, v174
	v_fma_f32 v193, v79, s53, v174
	v_exp_f32_e32 v178, v178
	v_exp_f32_e32 v179, v179
	v_exp_f32_e32 v180, v180
	v_exp_f32_e32 v181, v181
	v_exp_f32_e32 v182, v182
	v_exp_f32_e32 v183, v183
	v_exp_f32_e32 v184, v184
	v_exp_f32_e32 v185, v185
	v_exp_f32_e32 v186, v186
	v_exp_f32_e32 v187, v187
	v_exp_f32_e32 v188, v188
	v_exp_f32_e32 v189, v189
	v_exp_f32_e32 v190, v190
	v_exp_f32_e32 v191, v191
	v_exp_f32_e32 v192, v192
	v_exp_f32_e32 v193, v193
	v_add_f32_e32 v178, 1.0, v178
	v_add_f32_e32 v179, 1.0, v179
	v_add_f32_e32 v180, 1.0, v180
	v_add_f32_e32 v181, 1.0, v181
	v_add_f32_e32 v182, 1.0, v182
	v_add_f32_e32 v183, 1.0, v183
	v_add_f32_e32 v184, 1.0, v184
	v_add_f32_e32 v185, 1.0, v185
	v_add_f32_e32 v186, 1.0, v186
	v_add_f32_e32 v187, 1.0, v187
	v_add_f32_e32 v188, 1.0, v188
	v_add_f32_e32 v189, 1.0, v189
	v_add_f32_e32 v190, 1.0, v190
	v_add_f32_e32 v191, 1.0, v191
	v_add_f32_e32 v192, 1.0, v192
	v_add_f32_e32 v193, 1.0, v193
	v_rcp_f32_e32 v178, v178
	v_rcp_f32_e32 v179, v179
	v_rcp_f32_e32 v180, v180
	v_rcp_f32_e32 v181, v181
	v_rcp_f32_e32 v182, v182
	v_rcp_f32_e32 v183, v183
	v_rcp_f32_e32 v184, v184
	v_rcp_f32_e32 v185, v185
	v_rcp_f32_e32 v186, v186
	v_rcp_f32_e32 v187, v187
	v_rcp_f32_e32 v188, v188
	v_rcp_f32_e32 v189, v189
	v_rcp_f32_e32 v190, v190
	v_rcp_f32_e32 v191, v191
	v_rcp_f32_e32 v192, v192
	v_rcp_f32_e32 v193, v193
	v_mul_f32_e32 v178, v175, v178
	v_mul_f32_e32 v179, v175, v179
	v_mul_f32_e32 v180, v175, v180
	v_mul_f32_e32 v181, v175, v181
	v_mul_f32_e32 v182, v175, v182
	v_mul_f32_e32 v183, v175, v183
	v_mul_f32_e32 v184, v175, v184
	v_mul_f32_e32 v185, v175, v185
	v_exp_f32_e32 v96, v178
	v_exp_f32_e32 v97, v179
	v_exp_f32_e32 v98, v180
	v_exp_f32_e32 v99, v181
	v_exp_f32_e32 v100, v182
	v_exp_f32_e32 v101, v183
	v_exp_f32_e32 v102, v184
	v_exp_f32_e32 v103, v185
	s_nop 0
	v_fma_f32 v194, -v96, v96, 1.0
	v_fma_f32 v195, -v97, v97, 1.0
	v_fma_f32 v196, -v98, v98, 1.0
	v_fma_f32 v197, -v99, v99, 1.0
	v_fma_f32 v198, -v100, v100, 1.0
	v_fma_f32 v199, -v101, v101, 1.0
	v_fma_f32 v200, -v102, v102, 1.0
	v_fma_f32 v201, -v103, v103, 1.0
	v_max_f32_e32 v194, 0, v194
	v_max_f32_e32 v195, 0, v195
	v_max_f32_e32 v196, 0, v196
	v_max_f32_e32 v197, 0, v197
	v_max_f32_e32 v198, 0, v198
	v_max_f32_e32 v199, 0, v199
	v_max_f32_e32 v200, 0, v200
	v_max_f32_e32 v201, 0, v201
	v_sqrt_f32_e32 v194, v194
	v_sqrt_f32_e32 v195, v195
	v_sqrt_f32_e32 v196, v196
	v_sqrt_f32_e32 v197, v197
	v_sqrt_f32_e32 v198, v198
	v_sqrt_f32_e32 v199, v199
	v_sqrt_f32_e32 v200, v200
	v_sqrt_f32_e32 v201, v201
	s_waitcnt lgkmcnt(8)
	v_lshlrev_b32_e32 v144, 16, v144
	v_lshlrev_b32_e32 v145, 16, v145
	v_lshlrev_b32_e32 v146, 16, v146
	v_lshlrev_b32_e32 v147, 16, v147
	v_lshlrev_b32_e32 v148, 16, v148
	v_lshlrev_b32_e32 v149, 16, v149
	v_lshlrev_b32_e32 v150, 16, v150
	v_lshlrev_b32_e32 v151, 16, v151
	v_mul_f32_e32 v194, v194, v186
	v_mul_f32_e32 v195, v195, v187
	v_mul_f32_e32 v196, v196, v188
	v_mul_f32_e32 v197, v197, v189
	v_mul_f32_e32 v198, v198, v190
	v_mul_f32_e32 v199, v199, v191
	v_mul_f32_e32 v200, v200, v192
	v_mul_f32_e32 v201, v201, v193
	v_mul_f32_e32 v144, v194, v144
	v_mul_f32_e32 v145, v195, v145
	v_mul_f32_e32 v146, v196, v146
	v_mul_f32_e32 v147, v197, v147
	v_mul_f32_e32 v148, v198, v148
	v_mul_f32_e32 v149, v199, v149
	v_mul_f32_e32 v150, v200, v150
	v_mul_f32_e32 v151, v201, v151
	v_fma_f32 v178, v80, s53, v173
	v_fma_f32 v179, v81, s53, v173
	v_fma_f32 v180, v82, s53, v173
	v_fma_f32 v181, v83, s53, v173
	v_fma_f32 v182, v88, s53, v173
	v_fma_f32 v183, v89, s53, v173
	v_fma_f32 v184, v90, s53, v173
	v_fma_f32 v185, v91, s53, v173
	v_fma_f32 v186, v84, s53, v174
	v_fma_f32 v187, v85, s53, v174
	v_fma_f32 v188, v86, s53, v174
	v_fma_f32 v189, v87, s53, v174
	v_fma_f32 v190, v92, s53, v174
	v_fma_f32 v191, v93, s53, v174
	v_fma_f32 v192, v94, s53, v174
	v_fma_f32 v193, v95, s53, v174
	v_exp_f32_e32 v178, v178
	v_exp_f32_e32 v179, v179
	v_exp_f32_e32 v180, v180
	v_exp_f32_e32 v181, v181
	v_exp_f32_e32 v182, v182
	v_exp_f32_e32 v183, v183
	v_exp_f32_e32 v184, v184
	v_exp_f32_e32 v185, v185
	v_exp_f32_e32 v186, v186
	v_exp_f32_e32 v187, v187
	v_exp_f32_e32 v188, v188
	v_exp_f32_e32 v189, v189
	v_exp_f32_e32 v190, v190
	v_exp_f32_e32 v191, v191
	v_exp_f32_e32 v192, v192
	v_exp_f32_e32 v193, v193
	v_add_f32_e32 v178, 1.0, v178
	v_add_f32_e32 v179, 1.0, v179
	v_add_f32_e32 v180, 1.0, v180
	v_add_f32_e32 v181, 1.0, v181
	v_add_f32_e32 v182, 1.0, v182
	v_add_f32_e32 v183, 1.0, v183
	v_add_f32_e32 v184, 1.0, v184
	v_add_f32_e32 v185, 1.0, v185
	v_add_f32_e32 v186, 1.0, v186
	v_add_f32_e32 v187, 1.0, v187
	v_add_f32_e32 v188, 1.0, v188
	v_add_f32_e32 v189, 1.0, v189
	v_add_f32_e32 v190, 1.0, v190
	v_add_f32_e32 v191, 1.0, v191
	v_add_f32_e32 v192, 1.0, v192
	v_add_f32_e32 v193, 1.0, v193
	v_rcp_f32_e32 v178, v178
	v_rcp_f32_e32 v179, v179
	v_rcp_f32_e32 v180, v180
	v_rcp_f32_e32 v181, v181
	v_rcp_f32_e32 v182, v182
	v_rcp_f32_e32 v183, v183
	v_rcp_f32_e32 v184, v184
	v_rcp_f32_e32 v185, v185
	v_rcp_f32_e32 v186, v186
	v_rcp_f32_e32 v187, v187
	v_rcp_f32_e32 v188, v188
	v_rcp_f32_e32 v189, v189
	v_rcp_f32_e32 v190, v190
	v_rcp_f32_e32 v191, v191
	v_rcp_f32_e32 v192, v192
	v_rcp_f32_e32 v193, v193
	v_mul_f32_e32 v178, v175, v178
	v_mul_f32_e32 v179, v175, v179
	v_mul_f32_e32 v180, v175, v180
	v_mul_f32_e32 v181, v175, v181
	v_mul_f32_e32 v182, v175, v182
	v_mul_f32_e32 v183, v175, v183
	v_mul_f32_e32 v184, v175, v184
	v_mul_f32_e32 v185, v175, v185
	v_exp_f32_e32 v104, v178
	v_exp_f32_e32 v105, v179
	v_exp_f32_e32 v106, v180
	v_exp_f32_e32 v107, v181
	v_exp_f32_e32 v108, v182
	v_exp_f32_e32 v109, v183
	v_exp_f32_e32 v110, v184
	v_exp_f32_e32 v111, v185
	s_nop 0
	v_fma_f32 v194, -v104, v104, 1.0
	v_fma_f32 v195, -v105, v105, 1.0
	v_fma_f32 v196, -v106, v106, 1.0
	v_fma_f32 v197, -v107, v107, 1.0
	v_fma_f32 v198, -v108, v108, 1.0
	v_fma_f32 v199, -v109, v109, 1.0
	v_fma_f32 v200, -v110, v110, 1.0
	v_fma_f32 v201, -v111, v111, 1.0
	v_max_f32_e32 v194, 0, v194
	v_max_f32_e32 v195, 0, v195
	v_max_f32_e32 v196, 0, v196
	v_max_f32_e32 v197, 0, v197
	v_max_f32_e32 v198, 0, v198
	v_max_f32_e32 v199, 0, v199
	v_max_f32_e32 v200, 0, v200
	v_max_f32_e32 v201, 0, v201
	v_sqrt_f32_e32 v194, v194
	v_sqrt_f32_e32 v195, v195
	v_sqrt_f32_e32 v196, v196
	v_sqrt_f32_e32 v197, v197
	v_sqrt_f32_e32 v198, v198
	v_sqrt_f32_e32 v199, v199
	v_sqrt_f32_e32 v200, v200
	v_sqrt_f32_e32 v201, v201
	s_waitcnt lgkmcnt(0)
	v_lshlrev_b32_e32 v152, 16, v152
	v_lshlrev_b32_e32 v153, 16, v153
	v_lshlrev_b32_e32 v154, 16, v154
	v_lshlrev_b32_e32 v155, 16, v155
	v_lshlrev_b32_e32 v156, 16, v156
	v_lshlrev_b32_e32 v157, 16, v157
	v_lshlrev_b32_e32 v158, 16, v158
	v_lshlrev_b32_e32 v159, 16, v159
	v_mul_f32_e32 v194, v194, v186
	v_mul_f32_e32 v195, v195, v187
	v_mul_f32_e32 v196, v196, v188
	v_mul_f32_e32 v197, v197, v189
	v_mul_f32_e32 v198, v198, v190
	v_mul_f32_e32 v199, v199, v191
	v_mul_f32_e32 v200, v200, v192
	v_mul_f32_e32 v201, v201, v193
	v_mul_f32_e32 v152, v194, v152
	v_mul_f32_e32 v153, v195, v153
	v_mul_f32_e32 v154, v196, v154
	v_mul_f32_e32 v155, v197, v155
	v_mul_f32_e32 v156, v198, v156
	v_mul_f32_e32 v157, v199, v157
	v_mul_f32_e32 v158, v200, v158
	v_mul_f32_e32 v159, v201, v159
	v_fma_f32 v145, v97, v144, v145
	v_fma_f32 v149, v101, v148, v149
	v_fma_f32 v153, v105, v152, v153
	v_fma_f32 v157, v109, v156, v157
	v_mul_f32_e32 v97, v97, v96
	v_mul_f32_e32 v101, v101, v100
	v_mul_f32_e32 v105, v105, v104
	v_mul_f32_e32 v109, v109, v108
	v_fma_f32 v146, v98, v145, v146
	v_fma_f32 v150, v102, v149, v150
	v_fma_f32 v154, v106, v153, v154
	v_fma_f32 v158, v110, v157, v158
	v_mul_f32_e32 v98, v98, v97
	v_mul_f32_e32 v102, v102, v101
	v_mul_f32_e32 v106, v106, v105
	v_mul_f32_e32 v110, v110, v109
	v_fma_f32 v147, v99, v146, v147
	v_fma_f32 v151, v103, v150, v151
	v_fma_f32 v155, v107, v154, v155
	v_fma_f32 v159, v111, v158, v159
	v_mul_f32_e32 v99, v99, v98
	v_mul_f32_e32 v103, v103, v102
	v_mul_f32_e32 v107, v107, v106
	v_mul_f32_e32 v111, v111, v110
	ds_bpermute_b32 v178, v204, v99
	ds_bpermute_b32 v182, v204, v147
	ds_bpermute_b32 v179, v204, v103
	ds_bpermute_b32 v183, v204, v151
	ds_bpermute_b32 v180, v204, v107
	ds_bpermute_b32 v184, v204, v155
	ds_bpermute_b32 v181, v204, v111
	ds_bpermute_b32 v185, v204, v159
	s_waitcnt lgkmcnt(0)
	v_fma_f32 v186, v182, v99, v147
	v_cndmask_b32_e64 v178, 1.0, v178, s[34:35]
	v_fma_f32 v187, v183, v103, v151
	v_cndmask_b32_e64 v179, 1.0, v179, s[34:35]
	v_fma_f32 v188, v184, v107, v155
	v_cndmask_b32_e64 v180, 1.0, v180, s[34:35]
	v_fma_f32 v189, v185, v111, v159
	v_cndmask_b32_e64 v181, 1.0, v181, s[34:35]
	v_cndmask_b32_e64 v223, v147, v186, s[34:35]
	v_mul_f32_e32 v219, v99, v178
	v_cndmask_b32_e64 v224, v151, v187, s[34:35]
	v_mul_f32_e32 v220, v103, v179
	v_cndmask_b32_e64 v225, v155, v188, s[34:35]
	v_mul_f32_e32 v221, v107, v180
	v_cndmask_b32_e64 v226, v159, v189, s[34:35]
	v_mul_f32_e32 v222, v111, v181
	ds_bpermute_b32 v178, v205, v219
	ds_bpermute_b32 v182, v205, v223
	ds_bpermute_b32 v179, v205, v220
	ds_bpermute_b32 v183, v205, v224
	ds_bpermute_b32 v180, v205, v221
	ds_bpermute_b32 v184, v205, v225
	ds_bpermute_b32 v181, v205, v222
	ds_bpermute_b32 v185, v205, v226
	s_waitcnt lgkmcnt(0)
	v_fma_f32 v186, v182, v219, v223
	v_cndmask_b32_e64 v178, 1.0, v178, s[36:37]
	v_fma_f32 v187, v183, v220, v224
	v_cndmask_b32_e64 v179, 1.0, v179, s[36:37]
	v_fma_f32 v188, v184, v221, v225
	v_cndmask_b32_e64 v180, 1.0, v180, s[36:37]
	v_fma_f32 v189, v185, v222, v226
	v_cndmask_b32_e64 v181, 1.0, v181, s[36:37]
	v_cndmask_b32_e64 v223, v223, v186, s[36:37]
	v_mul_f32_e32 v219, v219, v178
	v_cndmask_b32_e64 v224, v224, v187, s[36:37]
	v_mul_f32_e32 v220, v220, v179
	v_cndmask_b32_e64 v225, v225, v188, s[36:37]
	v_mul_f32_e32 v221, v221, v180
	v_cndmask_b32_e64 v226, v226, v189, s[36:37]
	v_mul_f32_e32 v222, v222, v181
	ds_bpermute_b32 v227, v204, v219
	ds_bpermute_b32 v231, v204, v223
	ds_bpermute_b32 v235, v206, v219
	ds_bpermute_b32 v239, v206, v223
	ds_bpermute_b32 v228, v204, v220
	ds_bpermute_b32 v232, v204, v224
	ds_bpermute_b32 v236, v206, v220
	ds_bpermute_b32 v244, v206, v224
	ds_bpermute_b32 v229, v204, v221
	ds_bpermute_b32 v233, v204, v225
	ds_bpermute_b32 v237, v206, v221
	ds_bpermute_b32 v245, v206, v225
	ds_bpermute_b32 v230, v204, v222
	ds_bpermute_b32 v234, v204, v226
	ds_bpermute_b32 v238, v206, v222
	ds_bpermute_b32 v246, v206, v226
	s_waitcnt lgkmcnt(0)
	v_cndmask_b32_e64 v227, 1.0, v227, s[34:35]
	v_cndmask_b32_e64 v231, 0, v231, s[34:35]
	v_cndmask_b32_e64 v228, 1.0, v228, s[34:35]
	v_cndmask_b32_e64 v232, 0, v232, s[34:35]
	v_cndmask_b32_e64 v229, 1.0, v229, s[34:35]
	v_cndmask_b32_e64 v233, 0, v233, s[34:35]
	v_cndmask_b32_e64 v230, 1.0, v230, s[34:35]
	v_cndmask_b32_e64 v234, 0, v234, s[34:35]
	v_mov_b32_e32 v190, v235
	v_mov_b32_e32 v194, v239
	v_mov_b32_e32 v198, v190
	v_mov_b32_e32 v201, v194
	v_fma_f32 v194, v194, v236, v244
	v_mul_f32_e32 v190, v190, v236
	v_mov_b32_e32 v199, v190
	v_mov_b32_e32 v177, v194
	v_fma_f32 v194, v194, v237, v245
	v_mul_f32_e32 v190, v190, v237
	v_mov_b32_e32 v200, v190
	v_mov_b32_e32 v203, v194
	v_fma_f32 v194, v194, v238, v246
	v_mul_f32_e32 v190, v190, v238
	v_mov_b32_e32 v191, v194
	ds_write_b64 v207, v[190:191] offset:1024
	s_waitcnt lgkmcnt(0)
	s_barrier
	ds_read_b64 v[178:179], v208 offset:1024
	ds_read_b64 v[180:181], v208 offset:1536
	s_waitcnt lgkmcnt(0)
	v_fma_f32 v182, v176, v178, v179
	v_cndmask_b32_e64 v183, v176, v182, s[38:39]
	v_fma_f32 v176, v182, v180, v181
	s_add_i32 s13, s13, 1
	s_mov_b32 s60, 8

.Lmylru_nodma_3:
	v_mov_b32_e32 v163, v162
	ds_read_b128 v[96:99], v163
	ds_read_b128 v[100:103], v163 offset:8192
	ds_read_b128 v[104:107], v163 offset:16384
	ds_read_b128 v[108:111], v163 offset:24576
	v_xor_b32_e32 v164, 0x40, v163
	ds_read_b128 v[112:115], v164
	ds_read_b128 v[116:119], v164 offset:8192
	ds_read_b128 v[120:123], v164 offset:16384
	ds_read_b128 v[124:127], v164 offset:24576
	s_waitcnt lgkmcnt(7)
	v_mfma_f32_16x16x32_bf16 v[64:67], v[96:99], v[0:3], 0
	v_mfma_f32_16x16x32_bf16 v[68:71], v[96:99], v[32:35], 0
	v_xor_b32_e32 v164, 0x80, v163
	ds_read_b128 v[96:99], v164
	s_waitcnt lgkmcnt(7)
	v_mfma_f32_16x16x32_bf16 v[72:75], v[100:103], v[0:3], 0
	v_mfma_f32_16x16x32_bf16 v[76:79], v[100:103], v[32:35], 0
	ds_read_b128 v[100:103], v164 offset:8192
	s_waitcnt lgkmcnt(7)
	v_mfma_f32_16x16x32_bf16 v[80:83], v[104:107], v[0:3], 0
	v_mfma_f32_16x16x32_bf16 v[84:87], v[104:107], v[32:35], 0
	ds_read_b128 v[104:107], v164 offset:16384
	s_waitcnt lgkmcnt(7)
	v_mfma_f32_16x16x32_bf16 v[88:91], v[108:111], v[0:3], 0
	v_mfma_f32_16x16x32_bf16 v[92:95], v[108:111], v[32:35], 0
	ds_read_b128 v[108:111], v164 offset:24576
	s_waitcnt lgkmcnt(7)
	v_mfma_f32_16x16x32_bf16 v[64:67], v[112:115], v[4:7], v[64:67]
	v_mfma_f32_16x16x32_bf16 v[68:71], v[112:115], v[36:39], v[68:71]
	v_xor_b32_e32 v164, 0xc0, v163
	ds_read_b128 v[112:115], v164
	s_waitcnt lgkmcnt(7)
	v_mfma_f32_16x16x32_bf16 v[72:75], v[116:119], v[4:7], v[72:75]
	v_mfma_f32_16x16x32_bf16 v[76:79], v[116:119], v[36:39], v[76:79]
	ds_read_b128 v[116:119], v164 offset:8192
	s_waitcnt lgkmcnt(7)
	v_mfma_f32_16x16x32_bf16 v[80:83], v[120:123], v[4:7], v[80:83]
	v_mfma_f32_16x16x32_bf16 v[84:87], v[120:123], v[36:39], v[84:87]
	ds_read_b128 v[120:123], v164 offset:16384
	s_waitcnt lgkmcnt(7)
	v_mfma_f32_16x16x32_bf16 v[88:91], v[124:127], v[4:7], v[88:91]
	v_mfma_f32_16x16x32_bf16 v[92:95], v[124:127], v[36:39], v[92:95]
	ds_read_b128 v[124:127], v164 offset:24576
	s_waitcnt lgkmcnt(7)
	v_mfma_f32_16x16x32_bf16 v[64:67], v[96:99], v[8:11], v[64:67]
	v_mfma_f32_16x16x32_bf16 v[68:71], v[96:99], v[40:43], v[68:71]
	v_xor_b32_e32 v164, 0x100, v163
	ds_read_b128 v[96:99], v164
	s_waitcnt lgkmcnt(7)
	v_mfma_f32_16x16x32_bf16 v[72:75], v[100:103], v[8:11], v[72:75]
	v_mfma_f32_16x16x32_bf16 v[76:79], v[100:103], v[40:43], v[76:79]
	ds_read_b128 v[100:103], v164 offset:8192
	s_waitcnt lgkmcnt(7)
	v_mfma_f32_16x16x32_bf16 v[80:83], v[104:107], v[8:11], v[80:83]
	v_mfma_f32_16x16x32_bf16 v[84:87], v[104:107], v[40:43], v[84:87]
	ds_read_b128 v[104:107], v164 offset:16384
	s_waitcnt lgkmcnt(7)
	v_mfma_f32_16x16x32_bf16 v[88:91], v[108:111], v[8:11], v[88:91]
	v_mfma_f32_16x16x32_bf16 v[92:95], v[108:111], v[40:43], v[92:95]
	ds_read_b128 v[108:111], v164 offset:24576
	s_waitcnt lgkmcnt(7)
	v_mfma_f32_16x16x32_bf16 v[64:67], v[112:115], v[12:15], v[64:67]
	v_mfma_f32_16x16x32_bf16 v[68:71], v[112:115], v[44:47], v[68:71]
	v_xor_b32_e32 v164, 0x140, v163
	ds_read_b128 v[112:115], v164
	s_waitcnt lgkmcnt(7)
	v_mfma_f32_16x16x32_bf16 v[72:75], v[116:119], v[12:15], v[72:75]
	v_mfma_f32_16x16x32_bf16 v[76:79], v[116:119], v[44:47], v[76:79]
	ds_read_b128 v[116:119], v164 offset:8192
	s_waitcnt lgkmcnt(7)
	v_mfma_f32_16x16x32_bf16 v[80:83], v[120:123], v[12:15], v[80:83]
	v_mfma_f32_16x16x32_bf16 v[84:87], v[120:123], v[44:47], v[84:87]
	ds_read_b128 v[120:123], v164 offset:16384
	s_waitcnt lgkmcnt(7)
	v_mfma_f32_16x16x32_bf16 v[88:91], v[124:127], v[12:15], v[88:91]
	v_mfma_f32_16x16x32_bf16 v[92:95], v[124:127], v[44:47], v[92:95]
	ds_read_b128 v[124:127], v164 offset:24576
	s_waitcnt lgkmcnt(7)
	v_mfma_f32_16x16x32_bf16 v[64:67], v[96:99], v[16:19], v[64:67]
	v_mfma_f32_16x16x32_bf16 v[68:71], v[96:99], v[48:51], v[68:71]
	v_xor_b32_e32 v164, 0x180, v163
	ds_read_b128 v[96:99], v164
	s_waitcnt lgkmcnt(7)
	v_mfma_f32_16x16x32_bf16 v[72:75], v[100:103], v[16:19], v[72:75]
	v_mfma_f32_16x16x32_bf16 v[76:79], v[100:103], v[48:51], v[76:79]
	ds_read_b128 v[100:103], v164 offset:8192
	s_waitcnt lgkmcnt(7)
	v_mfma_f32_16x16x32_bf16 v[80:83], v[104:107], v[16:19], v[80:83]
	v_mfma_f32_16x16x32_bf16 v[84:87], v[104:107], v[48:51], v[84:87]
	ds_read_b128 v[104:107], v164 offset:16384
	s_waitcnt lgkmcnt(7)
	v_mfma_f32_16x16x32_bf16 v[88:91], v[108:111], v[16:19], v[88:91]
	v_mfma_f32_16x16x32_bf16 v[92:95], v[108:111], v[48:51], v[92:95]
	ds_read_b128 v[108:111], v164 offset:24576
	s_waitcnt lgkmcnt(7)
	v_mfma_f32_16x16x32_bf16 v[64:67], v[112:115], v[20:23], v[64:67]
	v_mfma_f32_16x16x32_bf16 v[68:71], v[112:115], v[52:55], v[68:71]
	v_xor_b32_e32 v164, 0x1c0, v163
	ds_read_b128 v[112:115], v164
	s_waitcnt lgkmcnt(7)
	v_mfma_f32_16x16x32_bf16 v[72:75], v[116:119], v[20:23], v[72:75]
	v_mfma_f32_16x16x32_bf16 v[76:79], v[116:119], v[52:55], v[76:79]
	ds_read_b128 v[116:119], v164 offset:8192
	s_waitcnt lgkmcnt(7)
	v_mfma_f32_16x16x32_bf16 v[80:83], v[120:123], v[20:23], v[80:83]
	v_mfma_f32_16x16x32_bf16 v[84:87], v[120:123], v[52:55], v[84:87]
	ds_read_b128 v[120:123], v164 offset:16384
	s_waitcnt lgkmcnt(7)
	v_mfma_f32_16x16x32_bf16 v[88:91], v[124:127], v[20:23], v[88:91]
	v_mfma_f32_16x16x32_bf16 v[92:95], v[124:127], v[52:55], v[92:95]
	ds_read_b128 v[124:127], v164 offset:24576
	s_waitcnt lgkmcnt(7)
	v_mfma_f32_16x16x32_bf16 v[64:67], v[96:99], v[24:27], v[64:67]
	v_mfma_f32_16x16x32_bf16 v[68:71], v[96:99], v[56:59], v[68:71]
	s_waitcnt lgkmcnt(6)
	v_mfma_f32_16x16x32_bf16 v[72:75], v[100:103], v[24:27], v[72:75]
	v_mfma_f32_16x16x32_bf16 v[76:79], v[100:103], v[56:59], v[76:79]
	s_waitcnt lgkmcnt(5)
	v_mfma_f32_16x16x32_bf16 v[80:83], v[104:107], v[24:27], v[80:83]
	v_mfma_f32_16x16x32_bf16 v[84:87], v[104:107], v[56:59], v[84:87]
	s_waitcnt lgkmcnt(4)
	v_mfma_f32_16x16x32_bf16 v[88:91], v[108:111], v[24:27], v[88:91]
	v_mfma_f32_16x16x32_bf16 v[92:95], v[108:111], v[56:59], v[92:95]
	s_waitcnt lgkmcnt(3)
	v_mfma_f32_16x16x32_bf16 v[64:67], v[112:115], v[28:31], v[64:67]
	v_mfma_f32_16x16x32_bf16 v[68:71], v[112:115], v[60:63], v[68:71]
	s_waitcnt lgkmcnt(2)
	v_mfma_f32_16x16x32_bf16 v[72:75], v[116:119], v[28:31], v[72:75]
	v_mfma_f32_16x16x32_bf16 v[76:79], v[116:119], v[60:63], v[76:79]
	s_waitcnt lgkmcnt(1)
	v_mfma_f32_16x16x32_bf16 v[80:83], v[120:123], v[28:31], v[80:83]
	v_mfma_f32_16x16x32_bf16 v[84:87], v[120:123], v[60:63], v[84:87]
	s_waitcnt lgkmcnt(0)
	v_mfma_f32_16x16x32_bf16 v[88:91], v[124:127], v[28:31], v[88:91]
	v_mfma_f32_16x16x32_bf16 v[92:95], v[124:127], v[60:63], v[92:95]
	v_mov_b32_e32 v169, v165
	v_mov_b32_e32 v170, v166
	v_mov_b32_e32 v171, v167
	v_mov_b32_e32 v172, v168
	ds_read_u16 v144, v169
	ds_read_u16 v145, v170
	ds_read_u16 v146, v171
	ds_read_u16 v147, v172
	ds_read_u16 v148, v169 offset:8192
	ds_read_u16 v149, v170 offset:8192
	ds_read_u16 v150, v171 offset:8192
	ds_read_u16 v151, v172 offset:8192
	ds_read_u16 v152, v169 offset:16384
	ds_read_u16 v153, v170 offset:16384
	ds_read_u16 v154, v171 offset:16384
	ds_read_u16 v155, v172 offset:16384
	ds_read_u16 v156, v169 offset:24576
	ds_read_u16 v157, v170 offset:24576
	ds_read_u16 v158, v171 offset:24576
	ds_read_u16 v159, v172 offset:24576
	s_nop 7
	v_fma_f32 v178, v64, s53, v173
	v_fma_f32 v179, v65, s53, v173
	v_fma_f32 v180, v66, s53, v173
	v_fma_f32 v181, v67, s53, v173
	v_fma_f32 v182, v72, s53, v173
	v_fma_f32 v183, v73, s53, v173
	v_fma_f32 v184, v74, s53, v173
	v_fma_f32 v185, v75, s53, v173
	v_fma_f32 v186, v68, s53, v174
	v_fma_f32 v187, v69, s53, v174
	v_fma_f32 v188, v70, s53, v174
	v_fma_f32 v189, v71, s53, v174
	v_fma_f32 v190, v76, s53, v174
	v_fma_f32 v191, v77, s53, v174
	v_fma_f32 v192, v78, s53, v174
	v_fma_f32 v193, v79, s53, v174
	v_exp_f32_e32 v178, v178
	v_exp_f32_e32 v179, v179
	v_exp_f32_e32 v180, v180
	v_exp_f32_e32 v181, v181
	v_exp_f32_e32 v182, v182
	v_exp_f32_e32 v183, v183
	v_exp_f32_e32 v184, v184
	v_exp_f32_e32 v185, v185
	v_exp_f32_e32 v186, v186
	v_exp_f32_e32 v187, v187
	v_exp_f32_e32 v188, v188
	v_exp_f32_e32 v189, v189
	v_exp_f32_e32 v190, v190
	v_exp_f32_e32 v191, v191
	v_exp_f32_e32 v192, v192
	v_exp_f32_e32 v193, v193
	v_add_f32_e32 v178, 1.0, v178
	v_add_f32_e32 v179, 1.0, v179
	v_add_f32_e32 v180, 1.0, v180
	v_add_f32_e32 v181, 1.0, v181
	v_add_f32_e32 v182, 1.0, v182
	v_add_f32_e32 v183, 1.0, v183
	v_add_f32_e32 v184, 1.0, v184
	v_add_f32_e32 v185, 1.0, v185
	v_add_f32_e32 v186, 1.0, v186
	v_add_f32_e32 v187, 1.0, v187
	v_add_f32_e32 v188, 1.0, v188
	v_add_f32_e32 v189, 1.0, v189
	v_add_f32_e32 v190, 1.0, v190
	v_add_f32_e32 v191, 1.0, v191
	v_add_f32_e32 v192, 1.0, v192
	v_add_f32_e32 v193, 1.0, v193
	v_rcp_f32_e32 v178, v178
	v_rcp_f32_e32 v179, v179
	v_rcp_f32_e32 v180, v180
	v_rcp_f32_e32 v181, v181
	v_rcp_f32_e32 v182, v182
	v_rcp_f32_e32 v183, v183
	v_rcp_f32_e32 v184, v184
	v_rcp_f32_e32 v185, v185
	v_rcp_f32_e32 v186, v186
	v_rcp_f32_e32 v187, v187
	v_rcp_f32_e32 v188, v188
	v_rcp_f32_e32 v189, v189
	v_rcp_f32_e32 v190, v190
	v_rcp_f32_e32 v191, v191
	v_rcp_f32_e32 v192, v192
	v_rcp_f32_e32 v193, v193
	v_mul_f32_e32 v178, v175, v178
	v_mul_f32_e32 v179, v175, v179
	v_mul_f32_e32 v180, v175, v180
	v_mul_f32_e32 v181, v175, v181
	v_mul_f32_e32 v182, v175, v182
	v_mul_f32_e32 v183, v175, v183
	v_mul_f32_e32 v184, v175, v184
	v_mul_f32_e32 v185, v175, v185
	v_exp_f32_e32 v96, v178
	v_exp_f32_e32 v97, v179
	v_exp_f32_e32 v98, v180
	v_exp_f32_e32 v99, v181
	v_exp_f32_e32 v100, v182
	v_exp_f32_e32 v101, v183
	v_exp_f32_e32 v102, v184
	v_exp_f32_e32 v103, v185
	s_nop 0
	v_fma_f32 v194, -v96, v96, 1.0
	v_fma_f32 v195, -v97, v97, 1.0
	v_fma_f32 v196, -v98, v98, 1.0
	v_fma_f32 v197, -v99, v99, 1.0
	v_fma_f32 v198, -v100, v100, 1.0
	v_fma_f32 v199, -v101, v101, 1.0
	v_fma_f32 v200, -v102, v102, 1.0
	v_fma_f32 v201, -v103, v103, 1.0
	v_max_f32_e32 v194, 0, v194
	v_max_f32_e32 v195, 0, v195
	v_max_f32_e32 v196, 0, v196
	v_max_f32_e32 v197, 0, v197
	v_max_f32_e32 v198, 0, v198
	v_max_f32_e32 v199, 0, v199
	v_max_f32_e32 v200, 0, v200
	v_max_f32_e32 v201, 0, v201
	v_sqrt_f32_e32 v194, v194
	v_sqrt_f32_e32 v195, v195
	v_sqrt_f32_e32 v196, v196
	v_sqrt_f32_e32 v197, v197
	v_sqrt_f32_e32 v198, v198
	v_sqrt_f32_e32 v199, v199
	v_sqrt_f32_e32 v200, v200
	v_sqrt_f32_e32 v201, v201
	s_waitcnt lgkmcnt(8)
	v_lshlrev_b32_e32 v144, 16, v144
	v_lshlrev_b32_e32 v145, 16, v145
	v_lshlrev_b32_e32 v146, 16, v146
	v_lshlrev_b32_e32 v147, 16, v147
	v_lshlrev_b32_e32 v148, 16, v148
	v_lshlrev_b32_e32 v149, 16, v149
	v_lshlrev_b32_e32 v150, 16, v150
	v_lshlrev_b32_e32 v151, 16, v151
	v_mul_f32_e32 v194, v194, v186
	v_mul_f32_e32 v195, v195, v187
	v_mul_f32_e32 v196, v196, v188
	v_mul_f32_e32 v197, v197, v189
	v_mul_f32_e32 v198, v198, v190
	v_mul_f32_e32 v199, v199, v191
	v_mul_f32_e32 v200, v200, v192
	v_mul_f32_e32 v201, v201, v193
	v_mul_f32_e32 v144, v194, v144
	v_mul_f32_e32 v145, v195, v145
	v_mul_f32_e32 v146, v196, v146
	v_mul_f32_e32 v147, v197, v147
	v_mul_f32_e32 v148, v198, v148
	v_mul_f32_e32 v149, v199, v149
	v_mul_f32_e32 v150, v200, v150
	v_mul_f32_e32 v151, v201, v151
	v_fma_f32 v178, v80, s53, v173
	v_fma_f32 v179, v81, s53, v173
	v_fma_f32 v180, v82, s53, v173
	v_fma_f32 v181, v83, s53, v173
	v_fma_f32 v182, v88, s53, v173
	v_fma_f32 v183, v89, s53, v173
	v_fma_f32 v184, v90, s53, v173
	v_fma_f32 v185, v91, s53, v173
	v_fma_f32 v186, v84, s53, v174
	v_fma_f32 v187, v85, s53, v174
	v_fma_f32 v188, v86, s53, v174
	v_fma_f32 v189, v87, s53, v174
	v_fma_f32 v190, v92, s53, v174
	v_fma_f32 v191, v93, s53, v174
	v_fma_f32 v192, v94, s53, v174
	v_fma_f32 v193, v95, s53, v174
	v_exp_f32_e32 v178, v178
	v_exp_f32_e32 v179, v179
	v_exp_f32_e32 v180, v180
	v_exp_f32_e32 v181, v181
	v_exp_f32_e32 v182, v182
	v_exp_f32_e32 v183, v183
	v_exp_f32_e32 v184, v184
	v_exp_f32_e32 v185, v185
	v_exp_f32_e32 v186, v186
	v_exp_f32_e32 v187, v187
	v_exp_f32_e32 v188, v188
	v_exp_f32_e32 v189, v189
	v_exp_f32_e32 v190, v190
	v_exp_f32_e32 v191, v191
	v_exp_f32_e32 v192, v192
	v_exp_f32_e32 v193, v193
	v_add_f32_e32 v178, 1.0, v178
	v_add_f32_e32 v179, 1.0, v179
	v_add_f32_e32 v180, 1.0, v180
	v_add_f32_e32 v181, 1.0, v181
	v_add_f32_e32 v182, 1.0, v182
	v_add_f32_e32 v183, 1.0, v183
	v_add_f32_e32 v184, 1.0, v184
	v_add_f32_e32 v185, 1.0, v185
	v_add_f32_e32 v186, 1.0, v186
	v_add_f32_e32 v187, 1.0, v187
	v_add_f32_e32 v188, 1.0, v188
	v_add_f32_e32 v189, 1.0, v189
	v_add_f32_e32 v190, 1.0, v190
	v_add_f32_e32 v191, 1.0, v191
	v_add_f32_e32 v192, 1.0, v192
	v_add_f32_e32 v193, 1.0, v193
	v_rcp_f32_e32 v178, v178
	v_rcp_f32_e32 v179, v179
	v_rcp_f32_e32 v180, v180
	v_rcp_f32_e32 v181, v181
	v_rcp_f32_e32 v182, v182
	v_rcp_f32_e32 v183, v183
	v_rcp_f32_e32 v184, v184
	v_rcp_f32_e32 v185, v185
	v_rcp_f32_e32 v186, v186
	v_rcp_f32_e32 v187, v187
	v_rcp_f32_e32 v188, v188
	v_rcp_f32_e32 v189, v189
	v_rcp_f32_e32 v190, v190
	v_rcp_f32_e32 v191, v191
	v_rcp_f32_e32 v192, v192
	v_rcp_f32_e32 v193, v193
	v_mul_f32_e32 v178, v175, v178
	v_mul_f32_e32 v179, v175, v179
	v_mul_f32_e32 v180, v175, v180
	v_mul_f32_e32 v181, v175, v181
	v_mul_f32_e32 v182, v175, v182
	v_mul_f32_e32 v183, v175, v183
	v_mul_f32_e32 v184, v175, v184
	v_mul_f32_e32 v185, v175, v185
	v_exp_f32_e32 v104, v178
	v_exp_f32_e32 v105, v179
	v_exp_f32_e32 v106, v180
	v_exp_f32_e32 v107, v181
	v_exp_f32_e32 v108, v182
	v_exp_f32_e32 v109, v183
	v_exp_f32_e32 v110, v184
	v_exp_f32_e32 v111, v185
	s_nop 0
	v_fma_f32 v194, -v104, v104, 1.0
	v_fma_f32 v195, -v105, v105, 1.0
	v_fma_f32 v196, -v106, v106, 1.0
	v_fma_f32 v197, -v107, v107, 1.0
	v_fma_f32 v198, -v108, v108, 1.0
	v_fma_f32 v199, -v109, v109, 1.0
	v_fma_f32 v200, -v110, v110, 1.0
	v_fma_f32 v201, -v111, v111, 1.0
	v_max_f32_e32 v194, 0, v194
	v_max_f32_e32 v195, 0, v195
	v_max_f32_e32 v196, 0, v196
	v_max_f32_e32 v197, 0, v197
	v_max_f32_e32 v198, 0, v198
	v_max_f32_e32 v199, 0, v199
	v_max_f32_e32 v200, 0, v200
	v_max_f32_e32 v201, 0, v201
	v_sqrt_f32_e32 v194, v194
	v_sqrt_f32_e32 v195, v195
	v_sqrt_f32_e32 v196, v196
	v_sqrt_f32_e32 v197, v197
	v_sqrt_f32_e32 v198, v198
	v_sqrt_f32_e32 v199, v199
	v_sqrt_f32_e32 v200, v200
	v_sqrt_f32_e32 v201, v201
	s_waitcnt lgkmcnt(0)
	v_lshlrev_b32_e32 v152, 16, v152
	v_lshlrev_b32_e32 v153, 16, v153
	v_lshlrev_b32_e32 v154, 16, v154
	v_lshlrev_b32_e32 v155, 16, v155
	v_lshlrev_b32_e32 v156, 16, v156
	v_lshlrev_b32_e32 v157, 16, v157
	v_lshlrev_b32_e32 v158, 16, v158
	v_lshlrev_b32_e32 v159, 16, v159
	v_mul_f32_e32 v194, v194, v186
	v_mul_f32_e32 v195, v195, v187
	v_mul_f32_e32 v196, v196, v188
	v_mul_f32_e32 v197, v197, v189
	v_mul_f32_e32 v198, v198, v190
	v_mul_f32_e32 v199, v199, v191
	v_mul_f32_e32 v200, v200, v192
	v_mul_f32_e32 v201, v201, v193
	v_mul_f32_e32 v152, v194, v152
	v_mul_f32_e32 v153, v195, v153
	v_mul_f32_e32 v154, v196, v154
	v_mul_f32_e32 v155, v197, v155
	v_mul_f32_e32 v156, v198, v156
	v_mul_f32_e32 v157, v199, v157
	v_mul_f32_e32 v158, v200, v158
	v_mul_f32_e32 v159, v201, v159
	v_fma_f32 v145, v97, v144, v145
	v_fma_f32 v149, v101, v148, v149
	v_fma_f32 v153, v105, v152, v153
	v_fma_f32 v157, v109, v156, v157
	v_mul_f32_e32 v97, v97, v96
	v_mul_f32_e32 v101, v101, v100
	v_mul_f32_e32 v105, v105, v104
	v_mul_f32_e32 v109, v109, v108
	v_fma_f32 v146, v98, v145, v146
	v_fma_f32 v150, v102, v149, v150
	v_fma_f32 v154, v106, v153, v154
	v_fma_f32 v158, v110, v157, v158
	v_mul_f32_e32 v98, v98, v97
	v_mul_f32_e32 v102, v102, v101
	v_mul_f32_e32 v106, v106, v105
	v_mul_f32_e32 v110, v110, v109
	v_fma_f32 v147, v99, v146, v147
	v_fma_f32 v151, v103, v150, v151
	v_fma_f32 v155, v107, v154, v155
	v_fma_f32 v159, v111, v158, v159
	v_mul_f32_e32 v99, v99, v98
	v_mul_f32_e32 v103, v103, v102
	v_mul_f32_e32 v107, v107, v106
	v_mul_f32_e32 v111, v111, v110
	ds_bpermute_b32 v178, v204, v99
	ds_bpermute_b32 v182, v204, v147
	ds_bpermute_b32 v179, v204, v103
	ds_bpermute_b32 v183, v204, v151
	ds_bpermute_b32 v180, v204, v107
	ds_bpermute_b32 v184, v204, v155
	ds_bpermute_b32 v181, v204, v111
	ds_bpermute_b32 v185, v204, v159
	s_waitcnt lgkmcnt(0)
	v_fma_f32 v186, v182, v99, v147
	v_cndmask_b32_e64 v178, 1.0, v178, s[34:35]
	v_fma_f32 v187, v183, v103, v151
	v_cndmask_b32_e64 v179, 1.0, v179, s[34:35]
	v_fma_f32 v188, v184, v107, v155
	v_cndmask_b32_e64 v180, 1.0, v180, s[34:35]
	v_fma_f32 v189, v185, v111, v159
	v_cndmask_b32_e64 v181, 1.0, v181, s[34:35]
	v_cndmask_b32_e64 v223, v147, v186, s[34:35]
	v_mul_f32_e32 v219, v99, v178
	v_cndmask_b32_e64 v224, v151, v187, s[34:35]
	v_mul_f32_e32 v220, v103, v179
	v_cndmask_b32_e64 v225, v155, v188, s[34:35]
	v_mul_f32_e32 v221, v107, v180
	v_cndmask_b32_e64 v226, v159, v189, s[34:35]
	v_mul_f32_e32 v222, v111, v181
	ds_bpermute_b32 v178, v205, v219
	ds_bpermute_b32 v182, v205, v223
	ds_bpermute_b32 v179, v205, v220
	ds_bpermute_b32 v183, v205, v224
	ds_bpermute_b32 v180, v205, v221
	ds_bpermute_b32 v184, v205, v225
	ds_bpermute_b32 v181, v205, v222
	ds_bpermute_b32 v185, v205, v226
	s_waitcnt lgkmcnt(0)
	v_fma_f32 v186, v182, v219, v223
	v_cndmask_b32_e64 v178, 1.0, v178, s[36:37]
	v_fma_f32 v187, v183, v220, v224
	v_cndmask_b32_e64 v179, 1.0, v179, s[36:37]
	v_fma_f32 v188, v184, v221, v225
	v_cndmask_b32_e64 v180, 1.0, v180, s[36:37]
	v_fma_f32 v189, v185, v222, v226
	v_cndmask_b32_e64 v181, 1.0, v181, s[36:37]
	v_cndmask_b32_e64 v223, v223, v186, s[36:37]
	v_mul_f32_e32 v219, v219, v178
	v_cndmask_b32_e64 v224, v224, v187, s[36:37]
	v_mul_f32_e32 v220, v220, v179
	v_cndmask_b32_e64 v225, v225, v188, s[36:37]
	v_mul_f32_e32 v221, v221, v180
	v_cndmask_b32_e64 v226, v226, v189, s[36:37]
	v_mul_f32_e32 v222, v222, v181
	ds_bpermute_b32 v227, v204, v219
	ds_bpermute_b32 v231, v204, v223
	ds_bpermute_b32 v235, v206, v219
	ds_bpermute_b32 v239, v206, v223
	ds_bpermute_b32 v228, v204, v220
	ds_bpermute_b32 v232, v204, v224
	ds_bpermute_b32 v236, v206, v220
	ds_bpermute_b32 v244, v206, v224
	ds_bpermute_b32 v229, v204, v221
	ds_bpermute_b32 v233, v204, v225
	ds_bpermute_b32 v237, v206, v221
	ds_bpermute_b32 v245, v206, v225
	ds_bpermute_b32 v230, v204, v222
	ds_bpermute_b32 v234, v204, v226
	ds_bpermute_b32 v238, v206, v222
	ds_bpermute_b32 v246, v206, v226
	s_waitcnt lgkmcnt(0)
	v_cndmask_b32_e64 v227, 1.0, v227, s[34:35]
	v_cndmask_b32_e64 v231, 0, v231, s[34:35]
	v_cndmask_b32_e64 v228, 1.0, v228, s[34:35]
	v_cndmask_b32_e64 v232, 0, v232, s[34:35]
	v_cndmask_b32_e64 v229, 1.0, v229, s[34:35]
	v_cndmask_b32_e64 v233, 0, v233, s[34:35]
	v_cndmask_b32_e64 v230, 1.0, v230, s[34:35]
	v_cndmask_b32_e64 v234, 0, v234, s[34:35]
	v_mov_b32_e32 v190, v235
	v_mov_b32_e32 v194, v239
	v_mov_b32_e32 v198, v190
	v_mov_b32_e32 v201, v194
	v_fma_f32 v194, v194, v236, v244
	v_mul_f32_e32 v190, v190, v236
	v_mov_b32_e32 v199, v190
	v_mov_b32_e32 v177, v194
	v_fma_f32 v194, v194, v237, v245
	v_mul_f32_e32 v190, v190, v237
	v_mov_b32_e32 v200, v190
	v_mov_b32_e32 v203, v194
	v_fma_f32 v194, v194, v238, v246
	v_mul_f32_e32 v190, v190, v238
	v_mov_b32_e32 v191, v194
	ds_write_b64 v207, v[190:191]
	s_waitcnt lgkmcnt(0)
	s_barrier
	ds_read_b64 v[178:179], v208
	ds_read_b64 v[180:181], v208 offset:512
	s_waitcnt lgkmcnt(0)
	v_fma_f32 v182, v176, v178, v179
	v_cndmask_b32_e64 v183, v176, v182, s[38:39]
	v_fma_f32 v176, v182, v180, v181
	v_mov_b32_e32 v184, v183
	v_fma_f32 v185, v183, v198, v201
	v_fma_f32 v186, v183, v199, v177
	v_fma_f32 v187, v183, v200, v203
	v_fma_f32 v184, v184, v227, v231
	v_fma_f32 v185, v185, v228, v232
	v_fma_f32 v186, v186, v229, v233
	v_fma_f32 v187, v187, v230, v234
	v_fma_f32 v144, v184, v96, v144
	v_fma_f32 v148, v185, v100, v148
	v_fma_f32 v152, v186, v104, v152
	v_fma_f32 v156, v187, v108, v156
	v_fma_f32 v145, v184, v97, v145
	v_fma_f32 v149, v185, v101, v149
	v_fma_f32 v153, v186, v105, v153
	v_fma_f32 v157, v187, v109, v157
	v_fma_f32 v146, v184, v98, v146
	v_fma_f32 v150, v185, v102, v150
	v_fma_f32 v154, v186, v106, v154
	v_fma_f32 v158, v187, v110, v158
	v_fma_f32 v147, v184, v99, v147
	v_fma_f32 v151, v185, v103, v151
	v_fma_f32 v155, v186, v107, v155
	v_fma_f32 v159, v187, v111, v159
	v_cvt_pk_bf16_f32 v178, v144, v145
	v_cvt_pk_bf16_f32 v179, v146, v147
	v_cvt_pk_bf16_f32 v180, v148, v149
	v_cvt_pk_bf16_f32 v181, v150, v151
	v_cvt_pk_bf16_f32 v182, v152, v153
	v_cvt_pk_bf16_f32 v183, v154, v155
	v_cvt_pk_bf16_f32 v184, v156, v157
	v_cvt_pk_bf16_f32 v185, v158, v159
	global_store_dword v209, v178, s[44:45]
	global_store_dword v209, v179, s[44:45] offset:256
	global_store_dword v209, v180, s[44:45] offset:512
	global_store_dword v209, v181, s[44:45] offset:768
	global_store_dword v209, v182, s[44:45] offset:1024
	global_store_dword v209, v183, s[44:45] offset:1280
	global_store_dword v209, v184, s[44:45] offset:1536
	global_store_dword v209, v185, s[44:45] offset:1792
	s_add_i32 s13, s13, 1
	s_cmp_eq_u32 s13, 2
	s_cbranch_scc1 .Lmylru_t0_4
	s_waitcnt vmcnt(8)
	s_branch .Lmylru_t1_4

.Lmylru_nodma_4:
	v_or_b32_e32 v163, 0x10000, v162
	ds_read_b128 v[96:99], v163
	ds_read_b128 v[100:103], v163 offset:8192
	ds_read_b128 v[104:107], v163 offset:16384
	ds_read_b128 v[108:111], v163 offset:24576
	v_xor_b32_e32 v164, 0x40, v163
	ds_read_b128 v[112:115], v164
	ds_read_b128 v[116:119], v164 offset:8192
	ds_read_b128 v[120:123], v164 offset:16384
	ds_read_b128 v[124:127], v164 offset:24576
	s_waitcnt lgkmcnt(7)
	v_mfma_f32_16x16x32_bf16 v[64:67], v[96:99], v[0:3], 0
	v_mfma_f32_16x16x32_bf16 v[68:71], v[96:99], v[32:35], 0
	v_xor_b32_e32 v164, 0x80, v163
	ds_read_b128 v[96:99], v164
	s_waitcnt lgkmcnt(7)
	v_mfma_f32_16x16x32_bf16 v[72:75], v[100:103], v[0:3], 0
	v_mfma_f32_16x16x32_bf16 v[76:79], v[100:103], v[32:35], 0
	ds_read_b128 v[100:103], v164 offset:8192
	s_waitcnt lgkmcnt(7)
	v_mfma_f32_16x16x32_bf16 v[80:83], v[104:107], v[0:3], 0
	v_mfma_f32_16x16x32_bf16 v[84:87], v[104:107], v[32:35], 0
	ds_read_b128 v[104:107], v164 offset:16384
	s_waitcnt lgkmcnt(7)
	v_mfma_f32_16x16x32_bf16 v[88:91], v[108:111], v[0:3], 0
	v_mfma_f32_16x16x32_bf16 v[92:95], v[108:111], v[32:35], 0
	ds_read_b128 v[108:111], v164 offset:24576
	s_waitcnt lgkmcnt(7)
	v_mfma_f32_16x16x32_bf16 v[64:67], v[112:115], v[4:7], v[64:67]
	v_mfma_f32_16x16x32_bf16 v[68:71], v[112:115], v[36:39], v[68:71]
	v_xor_b32_e32 v164, 0xc0, v163
	ds_read_b128 v[112:115], v164
	s_waitcnt lgkmcnt(7)
	v_mfma_f32_16x16x32_bf16 v[72:75], v[116:119], v[4:7], v[72:75]
	v_mfma_f32_16x16x32_bf16 v[76:79], v[116:119], v[36:39], v[76:79]
	ds_read_b128 v[116:119], v164 offset:8192
	s_waitcnt lgkmcnt(7)
	v_mfma_f32_16x16x32_bf16 v[80:83], v[120:123], v[4:7], v[80:83]
	v_mfma_f32_16x16x32_bf16 v[84:87], v[120:123], v[36:39], v[84:87]
	ds_read_b128 v[120:123], v164 offset:16384
	s_waitcnt lgkmcnt(7)
	v_mfma_f32_16x16x32_bf16 v[88:91], v[124:127], v[4:7], v[88:91]
	v_mfma_f32_16x16x32_bf16 v[92:95], v[124:127], v[36:39], v[92:95]
	ds_read_b128 v[124:127], v164 offset:24576
	s_waitcnt lgkmcnt(7)
	v_mfma_f32_16x16x32_bf16 v[64:67], v[96:99], v[8:11], v[64:67]
	v_mfma_f32_16x16x32_bf16 v[68:71], v[96:99], v[40:43], v[68:71]
	v_xor_b32_e32 v164, 0x100, v163
	ds_read_b128 v[96:99], v164
	s_waitcnt lgkmcnt(7)
	v_mfma_f32_16x16x32_bf16 v[72:75], v[100:103], v[8:11], v[72:75]
	v_mfma_f32_16x16x32_bf16 v[76:79], v[100:103], v[40:43], v[76:79]
	ds_read_b128 v[100:103], v164 offset:8192
	s_waitcnt lgkmcnt(7)
	v_mfma_f32_16x16x32_bf16 v[80:83], v[104:107], v[8:11], v[80:83]
	v_mfma_f32_16x16x32_bf16 v[84:87], v[104:107], v[40:43], v[84:87]
	ds_read_b128 v[104:107], v164 offset:16384
	s_waitcnt lgkmcnt(7)
	v_mfma_f32_16x16x32_bf16 v[88:91], v[108:111], v[8:11], v[88:91]
	v_mfma_f32_16x16x32_bf16 v[92:95], v[108:111], v[40:43], v[92:95]
	ds_read_b128 v[108:111], v164 offset:24576
	s_waitcnt lgkmcnt(7)
	v_mfma_f32_16x16x32_bf16 v[64:67], v[112:115], v[12:15], v[64:67]
	v_mfma_f32_16x16x32_bf16 v[68:71], v[112:115], v[44:47], v[68:71]
	v_xor_b32_e32 v164, 0x140, v163
	ds_read_b128 v[112:115], v164
	s_waitcnt lgkmcnt(7)
	v_mfma_f32_16x16x32_bf16 v[72:75], v[116:119], v[12:15], v[72:75]
	v_mfma_f32_16x16x32_bf16 v[76:79], v[116:119], v[44:47], v[76:79]
	ds_read_b128 v[116:119], v164 offset:8192
	s_waitcnt lgkmcnt(7)
	v_mfma_f32_16x16x32_bf16 v[80:83], v[120:123], v[12:15], v[80:83]
	v_mfma_f32_16x16x32_bf16 v[84:87], v[120:123], v[44:47], v[84:87]
	ds_read_b128 v[120:123], v164 offset:16384
	s_waitcnt lgkmcnt(7)
	v_mfma_f32_16x16x32_bf16 v[88:91], v[124:127], v[12:15], v[88:91]
	v_mfma_f32_16x16x32_bf16 v[92:95], v[124:127], v[44:47], v[92:95]
	ds_read_b128 v[124:127], v164 offset:24576
	s_waitcnt lgkmcnt(7)
	v_mfma_f32_16x16x32_bf16 v[64:67], v[96:99], v[16:19], v[64:67]
	v_mfma_f32_16x16x32_bf16 v[68:71], v[96:99], v[48:51], v[68:71]
	v_xor_b32_e32 v164, 0x180, v163
	ds_read_b128 v[96:99], v164
	s_waitcnt lgkmcnt(7)
	v_mfma_f32_16x16x32_bf16 v[72:75], v[100:103], v[16:19], v[72:75]
	v_mfma_f32_16x16x32_bf16 v[76:79], v[100:103], v[48:51], v[76:79]
	ds_read_b128 v[100:103], v164 offset:8192
	s_waitcnt lgkmcnt(7)
	v_mfma_f32_16x16x32_bf16 v[80:83], v[104:107], v[16:19], v[80:83]
	v_mfma_f32_16x16x32_bf16 v[84:87], v[104:107], v[48:51], v[84:87]
	ds_read_b128 v[104:107], v164 offset:16384
	s_waitcnt lgkmcnt(7)
	v_mfma_f32_16x16x32_bf16 v[88:91], v[108:111], v[16:19], v[88:91]
	v_mfma_f32_16x16x32_bf16 v[92:95], v[108:111], v[48:51], v[92:95]
	ds_read_b128 v[108:111], v164 offset:24576
	s_waitcnt lgkmcnt(7)
	v_mfma_f32_16x16x32_bf16 v[64:67], v[112:115], v[20:23], v[64:67]
	v_mfma_f32_16x16x32_bf16 v[68:71], v[112:115], v[52:55], v[68:71]
	v_xor_b32_e32 v164, 0x1c0, v163
	ds_read_b128 v[112:115], v164
	s_waitcnt lgkmcnt(7)
	v_mfma_f32_16x16x32_bf16 v[72:75], v[116:119], v[20:23], v[72:75]
	v_mfma_f32_16x16x32_bf16 v[76:79], v[116:119], v[52:55], v[76:79]
	ds_read_b128 v[116:119], v164 offset:8192
	s_waitcnt lgkmcnt(7)
	v_mfma_f32_16x16x32_bf16 v[80:83], v[120:123], v[20:23], v[80:83]
	v_mfma_f32_16x16x32_bf16 v[84:87], v[120:123], v[52:55], v[84:87]
	ds_read_b128 v[120:123], v164 offset:16384
	s_waitcnt lgkmcnt(7)
	v_mfma_f32_16x16x32_bf16 v[88:91], v[124:127], v[20:23], v[88:91]
	v_mfma_f32_16x16x32_bf16 v[92:95], v[124:127], v[52:55], v[92:95]
	ds_read_b128 v[124:127], v164 offset:24576
	s_waitcnt lgkmcnt(7)
	v_mfma_f32_16x16x32_bf16 v[64:67], v[96:99], v[24:27], v[64:67]
	v_mfma_f32_16x16x32_bf16 v[68:71], v[96:99], v[56:59], v[68:71]
	s_waitcnt lgkmcnt(6)
	v_mfma_f32_16x16x32_bf16 v[72:75], v[100:103], v[24:27], v[72:75]
	v_mfma_f32_16x16x32_bf16 v[76:79], v[100:103], v[56:59], v[76:79]
	s_waitcnt lgkmcnt(5)
	v_mfma_f32_16x16x32_bf16 v[80:83], v[104:107], v[24:27], v[80:83]
	v_mfma_f32_16x16x32_bf16 v[84:87], v[104:107], v[56:59], v[84:87]
	s_waitcnt lgkmcnt(4)
	v_mfma_f32_16x16x32_bf16 v[88:91], v[108:111], v[24:27], v[88:91]
	v_mfma_f32_16x16x32_bf16 v[92:95], v[108:111], v[56:59], v[92:95]
	s_waitcnt lgkmcnt(3)
	v_mfma_f32_16x16x32_bf16 v[64:67], v[112:115], v[28:31], v[64:67]
	v_mfma_f32_16x16x32_bf16 v[68:71], v[112:115], v[60:63], v[68:71]
	s_waitcnt lgkmcnt(2)
	v_mfma_f32_16x16x32_bf16 v[72:75], v[116:119], v[28:31], v[72:75]
	v_mfma_f32_16x16x32_bf16 v[76:79], v[116:119], v[60:63], v[76:79]
	s_waitcnt lgkmcnt(1)
	v_mfma_f32_16x16x32_bf16 v[80:83], v[120:123], v[28:31], v[80:83]
	v_mfma_f32_16x16x32_bf16 v[84:87], v[120:123], v[60:63], v[84:87]
	s_waitcnt lgkmcnt(0)
	v_mfma_f32_16x16x32_bf16 v[88:91], v[124:127], v[28:31], v[88:91]
	v_mfma_f32_16x16x32_bf16 v[92:95], v[124:127], v[60:63], v[92:95]
	v_or_b32_e32 v169, 0x10000, v165
	v_or_b32_e32 v170, 0x10000, v166
	v_or_b32_e32 v171, 0x10000, v167
	v_or_b32_e32 v172, 0x10000, v168
	ds_read_u16 v144, v169
	ds_read_u16 v145, v170
	ds_read_u16 v146, v171
	ds_read_u16 v147, v172
	ds_read_u16 v148, v169 offset:8192
	ds_read_u16 v149, v170 offset:8192
	ds_read_u16 v150, v171 offset:8192
	ds_read_u16 v151, v172 offset:8192
	ds_read_u16 v152, v169 offset:16384
	ds_read_u16 v153, v170 offset:16384
	ds_read_u16 v154, v171 offset:16384
	ds_read_u16 v155, v172 offset:16384
	ds_read_u16 v156, v169 offset:24576
	ds_read_u16 v157, v170 offset:24576
	ds_read_u16 v158, v171 offset:24576
	ds_read_u16 v159, v172 offset:24576
	s_nop 7
	v_fma_f32 v178, v64, s53, v173
	v_fma_f32 v179, v65, s53, v173
	v_fma_f32 v180, v66, s53, v173
	v_fma_f32 v181, v67, s53, v173
	v_fma_f32 v182, v72, s53, v173
	v_fma_f32 v183, v73, s53, v173
	v_fma_f32 v184, v74, s53, v173
	v_fma_f32 v185, v75, s53, v173
	v_fma_f32 v186, v68, s53, v174
	v_fma_f32 v187, v69, s53, v174
	v_fma_f32 v188, v70, s53, v174
	v_fma_f32 v189, v71, s53, v174
	v_fma_f32 v190, v76, s53, v174
	v_fma_f32 v191, v77, s53, v174
	v_fma_f32 v192, v78, s53, v174
	v_fma_f32 v193, v79, s53, v174
	v_exp_f32_e32 v178, v178
	v_exp_f32_e32 v179, v179
	v_exp_f32_e32 v180, v180
	v_exp_f32_e32 v181, v181
	v_exp_f32_e32 v182, v182
	v_exp_f32_e32 v183, v183
	v_exp_f32_e32 v184, v184
	v_exp_f32_e32 v185, v185
	v_exp_f32_e32 v186, v186
	v_exp_f32_e32 v187, v187
	v_exp_f32_e32 v188, v188
	v_exp_f32_e32 v189, v189
	v_exp_f32_e32 v190, v190
	v_exp_f32_e32 v191, v191
	v_exp_f32_e32 v192, v192
	v_exp_f32_e32 v193, v193
	v_add_f32_e32 v178, 1.0, v178
	v_add_f32_e32 v179, 1.0, v179
	v_add_f32_e32 v180, 1.0, v180
	v_add_f32_e32 v181, 1.0, v181
	v_add_f32_e32 v182, 1.0, v182
	v_add_f32_e32 v183, 1.0, v183
	v_add_f32_e32 v184, 1.0, v184
	v_add_f32_e32 v185, 1.0, v185
	v_add_f32_e32 v186, 1.0, v186
	v_add_f32_e32 v187, 1.0, v187
	v_add_f32_e32 v188, 1.0, v188
	v_add_f32_e32 v189, 1.0, v189
	v_add_f32_e32 v190, 1.0, v190
	v_add_f32_e32 v191, 1.0, v191
	v_add_f32_e32 v192, 1.0, v192
	v_add_f32_e32 v193, 1.0, v193
	v_rcp_f32_e32 v178, v178
	v_rcp_f32_e32 v179, v179
	v_rcp_f32_e32 v180, v180
	v_rcp_f32_e32 v181, v181
	v_rcp_f32_e32 v182, v182
	v_rcp_f32_e32 v183, v183
	v_rcp_f32_e32 v184, v184
	v_rcp_f32_e32 v185, v185
	v_rcp_f32_e32 v186, v186
	v_rcp_f32_e32 v187, v187
	v_rcp_f32_e32 v188, v188
	v_rcp_f32_e32 v189, v189
	v_rcp_f32_e32 v190, v190
	v_rcp_f32_e32 v191, v191
	v_rcp_f32_e32 v192, v192
	v_rcp_f32_e32 v193, v193
	v_mul_f32_e32 v178, v175, v178
	v_mul_f32_e32 v179, v175, v179
	v_mul_f32_e32 v180, v175, v180
	v_mul_f32_e32 v181, v175, v181
	v_mul_f32_e32 v182, v175, v182
	v_mul_f32_e32 v183, v175, v183
	v_mul_f32_e32 v184, v175, v184
	v_mul_f32_e32 v185, v175, v185
	v_exp_f32_e32 v96, v178
	v_exp_f32_e32 v97, v179
	v_exp_f32_e32 v98, v180
	v_exp_f32_e32 v99, v181
	v_exp_f32_e32 v100, v182
	v_exp_f32_e32 v101, v183
	v_exp_f32_e32 v102, v184
	v_exp_f32_e32 v103, v185
	s_nop 0
	v_fma_f32 v194, -v96, v96, 1.0
	v_fma_f32 v195, -v97, v97, 1.0
	v_fma_f32 v196, -v98, v98, 1.0
	v_fma_f32 v197, -v99, v99, 1.0
	v_fma_f32 v198, -v100, v100, 1.0
	v_fma_f32 v199, -v101, v101, 1.0
	v_fma_f32 v200, -v102, v102, 1.0
	v_fma_f32 v201, -v103, v103, 1.0
	v_max_f32_e32 v194, 0, v194
	v_max_f32_e32 v195, 0, v195
	v_max_f32_e32 v196, 0, v196
	v_max_f32_e32 v197, 0, v197
	v_max_f32_e32 v198, 0, v198
	v_max_f32_e32 v199, 0, v199
	v_max_f32_e32 v200, 0, v200
	v_max_f32_e32 v201, 0, v201
	v_sqrt_f32_e32 v194, v194
	v_sqrt_f32_e32 v195, v195
	v_sqrt_f32_e32 v196, v196
	v_sqrt_f32_e32 v197, v197
	v_sqrt_f32_e32 v198, v198
	v_sqrt_f32_e32 v199, v199
	v_sqrt_f32_e32 v200, v200
	v_sqrt_f32_e32 v201, v201
	s_waitcnt lgkmcnt(8)
	v_lshlrev_b32_e32 v144, 16, v144
	v_lshlrev_b32_e32 v145, 16, v145
	v_lshlrev_b32_e32 v146, 16, v146
	v_lshlrev_b32_e32 v147, 16, v147
	v_lshlrev_b32_e32 v148, 16, v148
	v_lshlrev_b32_e32 v149, 16, v149
	v_lshlrev_b32_e32 v150, 16, v150
	v_lshlrev_b32_e32 v151, 16, v151
	v_mul_f32_e32 v194, v194, v186
	v_mul_f32_e32 v195, v195, v187
	v_mul_f32_e32 v196, v196, v188
	v_mul_f32_e32 v197, v197, v189
	v_mul_f32_e32 v198, v198, v190
	v_mul_f32_e32 v199, v199, v191
	v_mul_f32_e32 v200, v200, v192
	v_mul_f32_e32 v201, v201, v193
	v_mul_f32_e32 v144, v194, v144
	v_mul_f32_e32 v145, v195, v145
	v_mul_f32_e32 v146, v196, v146
	v_mul_f32_e32 v147, v197, v147
	v_mul_f32_e32 v148, v198, v148
	v_mul_f32_e32 v149, v199, v149
	v_mul_f32_e32 v150, v200, v150
	v_mul_f32_e32 v151, v201, v151
	v_fma_f32 v178, v80, s53, v173
	v_fma_f32 v179, v81, s53, v173
	v_fma_f32 v180, v82, s53, v173
	v_fma_f32 v181, v83, s53, v173
	v_fma_f32 v182, v88, s53, v173
	v_fma_f32 v183, v89, s53, v173
	v_fma_f32 v184, v90, s53, v173
	v_fma_f32 v185, v91, s53, v173
	v_fma_f32 v186, v84, s53, v174
	v_fma_f32 v187, v85, s53, v174
	v_fma_f32 v188, v86, s53, v174
	v_fma_f32 v189, v87, s53, v174
	v_fma_f32 v190, v92, s53, v174
	v_fma_f32 v191, v93, s53, v174
	v_fma_f32 v192, v94, s53, v174
	v_fma_f32 v193, v95, s53, v174
	v_exp_f32_e32 v178, v178
	v_exp_f32_e32 v179, v179
	v_exp_f32_e32 v180, v180
	v_exp_f32_e32 v181, v181
	v_exp_f32_e32 v182, v182
	v_exp_f32_e32 v183, v183
	v_exp_f32_e32 v184, v184
	v_exp_f32_e32 v185, v185
	v_exp_f32_e32 v186, v186
	v_exp_f32_e32 v187, v187
	v_exp_f32_e32 v188, v188
	v_exp_f32_e32 v189, v189
	v_exp_f32_e32 v190, v190
	v_exp_f32_e32 v191, v191
	v_exp_f32_e32 v192, v192
	v_exp_f32_e32 v193, v193
	v_add_f32_e32 v178, 1.0, v178
	v_add_f32_e32 v179, 1.0, v179
	v_add_f32_e32 v180, 1.0, v180
	v_add_f32_e32 v181, 1.0, v181
	v_add_f32_e32 v182, 1.0, v182
	v_add_f32_e32 v183, 1.0, v183
	v_add_f32_e32 v184, 1.0, v184
	v_add_f32_e32 v185, 1.0, v185
	v_add_f32_e32 v186, 1.0, v186
	v_add_f32_e32 v187, 1.0, v187
	v_add_f32_e32 v188, 1.0, v188
	v_add_f32_e32 v189, 1.0, v189
	v_add_f32_e32 v190, 1.0, v190
	v_add_f32_e32 v191, 1.0, v191
	v_add_f32_e32 v192, 1.0, v192
	v_add_f32_e32 v193, 1.0, v193
	v_rcp_f32_e32 v178, v178
	v_rcp_f32_e32 v179, v179
	v_rcp_f32_e32 v180, v180
	v_rcp_f32_e32 v181, v181
	v_rcp_f32_e32 v182, v182
	v_rcp_f32_e32 v183, v183
	v_rcp_f32_e32 v184, v184
	v_rcp_f32_e32 v185, v185
	v_rcp_f32_e32 v186, v186
	v_rcp_f32_e32 v187, v187
	v_rcp_f32_e32 v188, v188
	v_rcp_f32_e32 v189, v189
	v_rcp_f32_e32 v190, v190
	v_rcp_f32_e32 v191, v191
	v_rcp_f32_e32 v192, v192
	v_rcp_f32_e32 v193, v193
	v_mul_f32_e32 v178, v175, v178
	v_mul_f32_e32 v179, v175, v179
	v_mul_f32_e32 v180, v175, v180
	v_mul_f32_e32 v181, v175, v181
	v_mul_f32_e32 v182, v175, v182
	v_mul_f32_e32 v183, v175, v183
	v_mul_f32_e32 v184, v175, v184
	v_mul_f32_e32 v185, v175, v185
	v_exp_f32_e32 v104, v178
	v_exp_f32_e32 v105, v179
	v_exp_f32_e32 v106, v180
	v_exp_f32_e32 v107, v181
	v_exp_f32_e32 v108, v182
	v_exp_f32_e32 v109, v183
	v_exp_f32_e32 v110, v184
	v_exp_f32_e32 v111, v185
	s_nop 0
	v_fma_f32 v194, -v104, v104, 1.0
	v_fma_f32 v195, -v105, v105, 1.0
	v_fma_f32 v196, -v106, v106, 1.0
	v_fma_f32 v197, -v107, v107, 1.0
	v_fma_f32 v198, -v108, v108, 1.0
	v_fma_f32 v199, -v109, v109, 1.0
	v_fma_f32 v200, -v110, v110, 1.0
	v_fma_f32 v201, -v111, v111, 1.0
	v_max_f32_e32 v194, 0, v194
	v_max_f32_e32 v195, 0, v195
	v_max_f32_e32 v196, 0, v196
	v_max_f32_e32 v197, 0, v197
	v_max_f32_e32 v198, 0, v198
	v_max_f32_e32 v199, 0, v199
	v_max_f32_e32 v200, 0, v200
	v_max_f32_e32 v201, 0, v201
	v_sqrt_f32_e32 v194, v194
	v_sqrt_f32_e32 v195, v195
	v_sqrt_f32_e32 v196, v196
	v_sqrt_f32_e32 v197, v197
	v_sqrt_f32_e32 v198, v198
	v_sqrt_f32_e32 v199, v199
	v_sqrt_f32_e32 v200, v200
	v_sqrt_f32_e32 v201, v201
	s_waitcnt lgkmcnt(0)
	v_lshlrev_b32_e32 v152, 16, v152
	v_lshlrev_b32_e32 v153, 16, v153
	v_lshlrev_b32_e32 v154, 16, v154
	v_lshlrev_b32_e32 v155, 16, v155
	v_lshlrev_b32_e32 v156, 16, v156
	v_lshlrev_b32_e32 v157, 16, v157
	v_lshlrev_b32_e32 v158, 16, v158
	v_lshlrev_b32_e32 v159, 16, v159
	v_mul_f32_e32 v194, v194, v186
	v_mul_f32_e32 v195, v195, v187
	v_mul_f32_e32 v196, v196, v188
	v_mul_f32_e32 v197, v197, v189
	v_mul_f32_e32 v198, v198, v190
	v_mul_f32_e32 v199, v199, v191
	v_mul_f32_e32 v200, v200, v192
	v_mul_f32_e32 v201, v201, v193
	v_mul_f32_e32 v152, v194, v152
	v_mul_f32_e32 v153, v195, v153
	v_mul_f32_e32 v154, v196, v154
	v_mul_f32_e32 v155, v197, v155
	v_mul_f32_e32 v156, v198, v156
	v_mul_f32_e32 v157, v199, v157
	v_mul_f32_e32 v158, v200, v158
	v_mul_f32_e32 v159, v201, v159
	v_fma_f32 v145, v97, v144, v145
	v_fma_f32 v149, v101, v148, v149
	v_fma_f32 v153, v105, v152, v153
	v_fma_f32 v157, v109, v156, v157
	v_mul_f32_e32 v97, v97, v96
	v_mul_f32_e32 v101, v101, v100
	v_mul_f32_e32 v105, v105, v104
	v_mul_f32_e32 v109, v109, v108
	v_fma_f32 v146, v98, v145, v146
	v_fma_f32 v150, v102, v149, v150
	v_fma_f32 v154, v106, v153, v154
	v_fma_f32 v158, v110, v157, v158
	v_mul_f32_e32 v98, v98, v97
	v_mul_f32_e32 v102, v102, v101
	v_mul_f32_e32 v106, v106, v105
	v_mul_f32_e32 v110, v110, v109
	v_fma_f32 v147, v99, v146, v147
	v_fma_f32 v151, v103, v150, v151
	v_fma_f32 v155, v107, v154, v155
	v_fma_f32 v159, v111, v158, v159
	v_mul_f32_e32 v99, v99, v98
	v_mul_f32_e32 v103, v103, v102
	v_mul_f32_e32 v107, v107, v106
	v_mul_f32_e32 v111, v111, v110
	ds_bpermute_b32 v178, v204, v99
	ds_bpermute_b32 v182, v204, v147
	ds_bpermute_b32 v179, v204, v103
	ds_bpermute_b32 v183, v204, v151
	ds_bpermute_b32 v180, v204, v107
	ds_bpermute_b32 v184, v204, v155
	ds_bpermute_b32 v181, v204, v111
	ds_bpermute_b32 v185, v204, v159
	s_waitcnt lgkmcnt(0)
	v_fma_f32 v186, v182, v99, v147
	v_cndmask_b32_e64 v178, 1.0, v178, s[34:35]
	v_fma_f32 v187, v183, v103, v151
	v_cndmask_b32_e64 v179, 1.0, v179, s[34:35]
	v_fma_f32 v188, v184, v107, v155
	v_cndmask_b32_e64 v180, 1.0, v180, s[34:35]
	v_fma_f32 v189, v185, v111, v159
	v_cndmask_b32_e64 v181, 1.0, v181, s[34:35]
	v_cndmask_b32_e64 v223, v147, v186, s[34:35]
	v_mul_f32_e32 v219, v99, v178
	v_cndmask_b32_e64 v224, v151, v187, s[34:35]
	v_mul_f32_e32 v220, v103, v179
	v_cndmask_b32_e64 v225, v155, v188, s[34:35]
	v_mul_f32_e32 v221, v107, v180
	v_cndmask_b32_e64 v226, v159, v189, s[34:35]
	v_mul_f32_e32 v222, v111, v181
	ds_bpermute_b32 v178, v205, v219
	ds_bpermute_b32 v182, v205, v223
	ds_bpermute_b32 v179, v205, v220
	ds_bpermute_b32 v183, v205, v224
	ds_bpermute_b32 v180, v205, v221
	ds_bpermute_b32 v184, v205, v225
	ds_bpermute_b32 v181, v205, v222
	ds_bpermute_b32 v185, v205, v226
	s_waitcnt lgkmcnt(0)
	v_fma_f32 v186, v182, v219, v223
	v_cndmask_b32_e64 v178, 1.0, v178, s[36:37]
	v_fma_f32 v187, v183, v220, v224
	v_cndmask_b32_e64 v179, 1.0, v179, s[36:37]
	v_fma_f32 v188, v184, v221, v225
	v_cndmask_b32_e64 v180, 1.0, v180, s[36:37]
	v_fma_f32 v189, v185, v222, v226
	v_cndmask_b32_e64 v181, 1.0, v181, s[36:37]
	v_cndmask_b32_e64 v223, v223, v186, s[36:37]
	v_mul_f32_e32 v219, v219, v178
	v_cndmask_b32_e64 v224, v224, v187, s[36:37]
	v_mul_f32_e32 v220, v220, v179
	v_cndmask_b32_e64 v225, v225, v188, s[36:37]
	v_mul_f32_e32 v221, v221, v180
	v_cndmask_b32_e64 v226, v226, v189, s[36:37]
	v_mul_f32_e32 v222, v222, v181
	ds_bpermute_b32 v227, v204, v219
	ds_bpermute_b32 v231, v204, v223
	ds_bpermute_b32 v235, v206, v219
	ds_bpermute_b32 v239, v206, v223
	ds_bpermute_b32 v228, v204, v220
	ds_bpermute_b32 v232, v204, v224
	ds_bpermute_b32 v236, v206, v220
	ds_bpermute_b32 v244, v206, v224
	ds_bpermute_b32 v229, v204, v221
	ds_bpermute_b32 v233, v204, v225
	ds_bpermute_b32 v237, v206, v221
	ds_bpermute_b32 v245, v206, v225
	ds_bpermute_b32 v230, v204, v222
	ds_bpermute_b32 v234, v204, v226
	ds_bpermute_b32 v238, v206, v222
	ds_bpermute_b32 v246, v206, v226
	s_waitcnt lgkmcnt(0)
	v_cndmask_b32_e64 v227, 1.0, v227, s[34:35]
	v_cndmask_b32_e64 v231, 0, v231, s[34:35]
	v_cndmask_b32_e64 v228, 1.0, v228, s[34:35]
	v_cndmask_b32_e64 v232, 0, v232, s[34:35]
	v_cndmask_b32_e64 v229, 1.0, v229, s[34:35]
	v_cndmask_b32_e64 v233, 0, v233, s[34:35]
	v_cndmask_b32_e64 v230, 1.0, v230, s[34:35]
	v_cndmask_b32_e64 v234, 0, v234, s[34:35]
	v_mov_b32_e32 v190, v235
	v_mov_b32_e32 v194, v239
	v_mov_b32_e32 v198, v190
	v_mov_b32_e32 v201, v194
	v_fma_f32 v194, v194, v236, v244
	v_mul_f32_e32 v190, v190, v236
	v_mov_b32_e32 v199, v190
	v_mov_b32_e32 v177, v194
	v_fma_f32 v194, v194, v237, v245
	v_mul_f32_e32 v190, v190, v237
	v_mov_b32_e32 v200, v190
	v_mov_b32_e32 v203, v194
	v_fma_f32 v194, v194, v238, v246
	v_mul_f32_e32 v190, v190, v238
	v_mov_b32_e32 v191, v194
	ds_write_b64 v207, v[190:191] offset:1024
	s_waitcnt lgkmcnt(0)
	s_barrier
	ds_read_b64 v[178:179], v208 offset:1024
	ds_read_b64 v[180:181], v208 offset:1536
	s_waitcnt lgkmcnt(0)
	v_fma_f32 v182, v176, v178, v179
	v_cndmask_b32_e64 v183, v176, v182, s[38:39]
	v_fma_f32 v176, v182, v180, v181
	v_mov_b32_e32 v184, v183
	v_fma_f32 v185, v183, v198, v201
	v_fma_f32 v186, v183, v199, v177
	v_fma_f32 v187, v183, v200, v203
	v_fma_f32 v184, v184, v227, v231
	v_fma_f32 v185, v185, v228, v232
	v_fma_f32 v186, v186, v229, v233
	v_fma_f32 v187, v187, v230, v234
	v_fma_f32 v144, v184, v96, v144
	v_fma_f32 v148, v185, v100, v148
	v_fma_f32 v152, v186, v104, v152
	v_fma_f32 v156, v187, v108, v156
	v_fma_f32 v145, v184, v97, v145
	v_fma_f32 v149, v185, v101, v149
	v_fma_f32 v153, v186, v105, v153
	v_fma_f32 v157, v187, v109, v157
	v_fma_f32 v146, v184, v98, v146
	v_fma_f32 v150, v185, v102, v150
	v_fma_f32 v154, v186, v106, v154
	v_fma_f32 v158, v187, v110, v158
	v_fma_f32 v147, v184, v99, v147
	v_fma_f32 v151, v185, v103, v151
	v_fma_f32 v155, v186, v107, v155
	v_fma_f32 v159, v187, v111, v159
	v_cvt_pk_bf16_f32 v178, v144, v145
	v_cvt_pk_bf16_f32 v179, v146, v147
	v_cvt_pk_bf16_f32 v180, v148, v149
	v_cvt_pk_bf16_f32 v181, v150, v151
	v_cvt_pk_bf16_f32 v182, v152, v153
	v_cvt_pk_bf16_f32 v183, v154, v155
	v_cvt_pk_bf16_f32 v184, v156, v157
	v_cvt_pk_bf16_f32 v185, v158, v159
	global_store_dword v209, v178, s[44:45]
	global_store_dword v209, v179, s[44:45] offset:256
	global_store_dword v209, v180, s[44:45] offset:512
	global_store_dword v209, v181, s[44:45] offset:768
	global_store_dword v209, v182, s[44:45] offset:1024
	global_store_dword v209, v183, s[44:45] offset:1280
	global_store_dword v209, v184, s[44:45] offset:1536
	global_store_dword v209, v185, s[44:45] offset:1792
	s_add_i32 s13, s13, 1
	s_add_i32 s60, s60, -1
	s_cmp_lg_u32 s60, 0
	s_cbranch_scc1 .Lmylru_loop_0
	s_lshl_b32 s50, s10, 10
	s_lshl_b32 s51, s11, 6
	s_add_i32 s50, s50, s51
	s_lshl_b32 s51, s8, 4
	s_add_i32 s50, s50, s51
	s_add_i32 s50, s50, 512
	s_lshl_b32 s50, s50, 9
	s_add_u32 s46, s2, s50
	s_addc_u32 s47, s3, 0
	s_add_u32 s46, s46, 0x1000000
	s_addc_u32 s47, s47, 0
	s_add_u32 s48, s46, 0x20000
	s_addc_u32 s49, s47, 0
	v_lshlrev_b32_e32 v178, 9, v160
	v_lshl_add_u32 v178, v161, 4, v178
	global_load_dwordx4 v[0:3], v178, s[46:47]
	global_load_dwordx4 v[4:7], v178, s[46:47] offset:64
	global_load_dwordx4 v[8:11], v178, s[46:47] offset:128
	global_load_dwordx4 v[12:15], v178, s[46:47] offset:192
	global_load_dwordx4 v[16:19], v178, s[46:47] offset:256
	global_load_dwordx4 v[20:23], v178, s[46:47] offset:320
	global_load_dwordx4 v[24:27], v178, s[46:47] offset:384
	global_load_dwordx4 v[28:31], v178, s[46:47] offset:448
	global_load_dwordx4 v[32:35], v178, s[48:49]
	global_load_dwordx4 v[36:39], v178, s[48:49] offset:64
	global_load_dwordx4 v[40:43], v178, s[48:49] offset:128
	global_load_dwordx4 v[44:47], v178, s[48:49] offset:192
	global_load_dwordx4 v[48:51], v178, s[48:49] offset:256
	global_load_dwordx4 v[52:55], v178, s[48:49] offset:320
	global_load_dwordx4 v[56:59], v178, s[48:49] offset:384
	global_load_dwordx4 v[60:63], v178, s[48:49] offset:448
	s_load_dwordx2 s[46:47], s[0:1], 0xc8
	s_load_dwordx2 s[48:49], s[0:1], 0xd8
	s_load_dwordx2 s[40:41], s[0:1], 0xe0
	s_lshl_b32 s50, s10, 8
	s_lshl_b32 s51, s11, 6
	s_add_i32 s50, s50, s51
	s_lshl_b32 s51, s8, 4
	s_add_i32 s50, s50, s51
	v_add_u32_e32 v179, s50, v160
	v_lshlrev_b32_e32 v179, 2, v179
	s_waitcnt lgkmcnt(0)
	global_load_dword v173, v179, s[46:47]
	global_load_dword v174, v179, s[48:49]
	global_load_dword v175, v179, s[40:41]
	v_cmp_gt_u32_e64 s[34:35], 48, v202
	v_cmp_gt_u32_e64 s[36:37], 32, v202
	v_add_u32_e32 v204, 16, v202
	v_add_u32_e32 v205, 32, v202
	v_mov_b32_e32 v206, v160
	s_cmp_eq_u32 s7, 0
	s_cselect_b64 s[38:39], -1, 0
	v_and_b32_e32 v204, 63, v204
	v_lshlrev_b32_e32 v204, 2, v204
	v_and_b32_e32 v205, 63, v205
	v_lshlrev_b32_e32 v205, 2, v205
	v_and_b32_e32 v206, 63, v206
	v_lshlrev_b32_e32 v206, 2, v206
	v_mov_b32_e32 v176, 0
	s_mov_b32 s53, 0xbfb8aa3b
	s_waitcnt vmcnt(0)
	v_mul_f32_e32 v173, s53, v173
	v_mul_f32_e32 v174, s53, v174
	v_mul_f32_e32 v175, s53, v175
	v_exp_f32_e32 v175, v175
	s_nop 0
	v_add_f32_e32 v180, 1.0, v175
	v_log_f32_e32 v180, v180
	v_mov_b32_e32 v181, 0x3eaaaaab
	v_fma_f32 v181, v175, v181, -0.5
	v_fma_f32 v181, v175, v181, 1.0
	v_mul_f32_e32 v181, v175, v181
	v_mul_f32_e32 v181, 0x3fb8aa3b, v181
	v_cmp_gt_f32_e32 vcc, 0x3cf5c28f, v175
	s_nop 1
	v_cndmask_b32_e32 v175, v180, v181, vcc
	v_mul_f32_e32 v175, 0xc1000000, v175
	s_mov_b32 s13, 0
	s_barrier
	s_cmp_lt_u32 s13, 2
	s_sub_i32 s50, 1, s13
	s_lshl_b32 s50, s50, 7
	s_lshl_b32 s51, s9, 8
	s_add_i32 s51, s51, 0x8000
	s_add_i32 s51, s51, s50
	s_sub_i32 s50, 17, s13
	s_lshl_b32 s50, s50, 7
	s_lshl_b32 s59, s9, 11
	s_add_i32 s59, s59, s50
	s_cmp_lt_u32 s13, 2
	s_cselect_b32 s59, s51, s59
	s_lshl_b32 s52, s59, 11
	s_add_u32 s46, s16, s52
	s_addc_u32 s47, s17, 0
	s_lshl_b32 s52, s6, 13
	s_mov_b32 m0, s52
	s_add_i32 s52, s52, 0x400
	global_load_lds_dwordx4 v211, s[46:47]
	s_mov_b32 m0, s52
	s_add_i32 s52, s52, 0x400
	global_load_lds_dwordx4 v212, s[46:47]
	s_mov_b32 m0, s52
	s_add_i32 s52, s52, 0x400
	global_load_lds_dwordx4 v213, s[46:47]
	s_mov_b32 m0, s52
	s_add_i32 s52, s52, 0x400
	global_load_lds_dwordx4 v214, s[46:47]
	s_mov_b32 m0, s52
	s_add_i32 s52, s52, 0x400
	global_load_lds_dwordx4 v215, s[46:47]
	s_mov_b32 m0, s52
	s_add_i32 s52, s52, 0x400
	global_load_lds_dwordx4 v216, s[46:47]
	s_mov_b32 m0, s52
	s_add_i32 s52, s52, 0x400
	global_load_lds_dwordx4 v217, s[46:47]
	s_mov_b32 m0, s52
	s_nop 0
	global_load_lds_dwordx4 v218, s[46:47]
	s_waitcnt vmcnt(0)
	s_barrier
	s_cmp_eq_u32 s13, 17
	s_cbranch_scc1 .Lmylru_nodma_5
	s_add_i32 s58, s13, 1
	s_cmp_lt_u32 s58, 2
	s_sub_i32 s50, 1, s58
	s_lshl_b32 s50, s50, 7
	s_lshl_b32 s51, s9, 8
	s_add_i32 s51, s51, 0x8000
	s_add_i32 s51, s51, s50
	s_sub_i32 s50, 17, s58
	s_lshl_b32 s50, s50, 7
	s_lshl_b32 s59, s9, 11
	s_add_i32 s59, s59, s50
	s_cmp_lt_u32 s58, 2
	s_cselect_b32 s59, s51, s59
	s_lshl_b32 s52, s59, 11
	s_add_u32 s46, s16, s52
	s_addc_u32 s47, s17, 0
	s_lshl_b32 s52, s6, 13
	s_add_i32 s52, s52, 0x10000
	s_mov_b32 m0, s52
	s_add_i32 s52, s52, 0x400
	global_load_lds_dwordx4 v211, s[46:47]
	s_mov_b32 m0, s52
	s_add_i32 s52, s52, 0x400
	global_load_lds_dwordx4 v212, s[46:47]
	s_mov_b32 m0, s52
	s_add_i32 s52, s52, 0x400
	global_load_lds_dwordx4 v213, s[46:47]
	s_mov_b32 m0, s52
	s_add_i32 s52, s52, 0x400
	global_load_lds_dwordx4 v214, s[46:47]
	s_mov_b32 m0, s52
	s_add_i32 s52, s52, 0x400
	global_load_lds_dwordx4 v215, s[46:47]
	s_mov_b32 m0, s52
	s_add_i32 s52, s52, 0x400
	global_load_lds_dwordx4 v216, s[46:47]
	s_mov_b32 m0, s52
	s_add_i32 s52, s52, 0x400
	global_load_lds_dwordx4 v217, s[46:47]
	s_mov_b32 m0, s52
	s_nop 0
	global_load_lds_dwordx4 v218, s[46:47]
.Lmylru_nodma_5:
	v_mov_b32_e32 v163, v162
	ds_read_b128 v[96:99], v163
	ds_read_b128 v[100:103], v163 offset:8192
	ds_read_b128 v[104:107], v163 offset:16384
	ds_read_b128 v[108:111], v163 offset:24576
	v_xor_b32_e32 v164, 0x40, v163
	ds_read_b128 v[112:115], v164
	ds_read_b128 v[116:119], v164 offset:8192
	ds_read_b128 v[120:123], v164 offset:16384
	ds_read_b128 v[124:127], v164 offset:24576
	s_waitcnt lgkmcnt(7)
	v_mfma_f32_16x16x32_bf16 v[64:67], v[96:99], v[0:3], 0
	v_mfma_f32_16x16x32_bf16 v[68:71], v[96:99], v[32:35], 0
	v_xor_b32_e32 v164, 0x80, v163
	ds_read_b128 v[96:99], v164
	s_waitcnt lgkmcnt(7)
	v_mfma_f32_16x16x32_bf16 v[72:75], v[100:103], v[0:3], 0
	v_mfma_f32_16x16x32_bf16 v[76:79], v[100:103], v[32:35], 0
	ds_read_b128 v[100:103], v164 offset:8192
	s_waitcnt lgkmcnt(7)
	v_mfma_f32_16x16x32_bf16 v[80:83], v[104:107], v[0:3], 0
	v_mfma_f32_16x16x32_bf16 v[84:87], v[104:107], v[32:35], 0
	ds_read_b128 v[104:107], v164 offset:16384
	s_waitcnt lgkmcnt(7)
	v_mfma_f32_16x16x32_bf16 v[88:91], v[108:111], v[0:3], 0
	v_mfma_f32_16x16x32_bf16 v[92:95], v[108:111], v[32:35], 0
	ds_read_b128 v[108:111], v164 offset:24576
	s_waitcnt lgkmcnt(7)
	v_mfma_f32_16x16x32_bf16 v[64:67], v[112:115], v[4:7], v[64:67]
	v_mfma_f32_16x16x32_bf16 v[68:71], v[112:115], v[36:39], v[68:71]
	v_xor_b32_e32 v164, 0xc0, v163
	ds_read_b128 v[112:115], v164
	s_waitcnt lgkmcnt(7)
	v_mfma_f32_16x16x32_bf16 v[72:75], v[116:119], v[4:7], v[72:75]
	v_mfma_f32_16x16x32_bf16 v[76:79], v[116:119], v[36:39], v[76:79]
	ds_read_b128 v[116:119], v164 offset:8192
	s_waitcnt lgkmcnt(7)
	v_mfma_f32_16x16x32_bf16 v[80:83], v[120:123], v[4:7], v[80:83]
	v_mfma_f32_16x16x32_bf16 v[84:87], v[120:123], v[36:39], v[84:87]
	ds_read_b128 v[120:123], v164 offset:16384
	s_waitcnt lgkmcnt(7)
	v_mfma_f32_16x16x32_bf16 v[88:91], v[124:127], v[4:7], v[88:91]
	v_mfma_f32_16x16x32_bf16 v[92:95], v[124:127], v[36:39], v[92:95]
	ds_read_b128 v[124:127], v164 offset:24576
	s_waitcnt lgkmcnt(7)
	v_mfma_f32_16x16x32_bf16 v[64:67], v[96:99], v[8:11], v[64:67]
	v_mfma_f32_16x16x32_bf16 v[68:71], v[96:99], v[40:43], v[68:71]
	v_xor_b32_e32 v164, 0x100, v163
	ds_read_b128 v[96:99], v164
	s_waitcnt lgkmcnt(7)
	v_mfma_f32_16x16x32_bf16 v[72:75], v[100:103], v[8:11], v[72:75]
	v_mfma_f32_16x16x32_bf16 v[76:79], v[100:103], v[40:43], v[76:79]
	ds_read_b128 v[100:103], v164 offset:8192
	s_waitcnt lgkmcnt(7)
	v_mfma_f32_16x16x32_bf16 v[80:83], v[104:107], v[8:11], v[80:83]
	v_mfma_f32_16x16x32_bf16 v[84:87], v[104:107], v[40:43], v[84:87]
	ds_read_b128 v[104:107], v164 offset:16384
	s_waitcnt lgkmcnt(7)
	v_mfma_f32_16x16x32_bf16 v[88:91], v[108:111], v[8:11], v[88:91]
	v_mfma_f32_16x16x32_bf16 v[92:95], v[108:111], v[40:43], v[92:95]
	ds_read_b128 v[108:111], v164 offset:24576
	s_waitcnt lgkmcnt(7)
	v_mfma_f32_16x16x32_bf16 v[64:67], v[112:115], v[12:15], v[64:67]
	v_mfma_f32_16x16x32_bf16 v[68:71], v[112:115], v[44:47], v[68:71]
	v_xor_b32_e32 v164, 0x140, v163
	ds_read_b128 v[112:115], v164
	s_waitcnt lgkmcnt(7)
	v_mfma_f32_16x16x32_bf16 v[72:75], v[116:119], v[12:15], v[72:75]
	v_mfma_f32_16x16x32_bf16 v[76:79], v[116:119], v[44:47], v[76:79]
	ds_read_b128 v[116:119], v164 offset:8192
	s_waitcnt lgkmcnt(7)
	v_mfma_f32_16x16x32_bf16 v[80:83], v[120:123], v[12:15], v[80:83]
	v_mfma_f32_16x16x32_bf16 v[84:87], v[120:123], v[44:47], v[84:87]
	ds_read_b128 v[120:123], v164 offset:16384
	s_waitcnt lgkmcnt(7)
	v_mfma_f32_16x16x32_bf16 v[88:91], v[124:127], v[12:15], v[88:91]
	v_mfma_f32_16x16x32_bf16 v[92:95], v[124:127], v[44:47], v[92:95]
	ds_read_b128 v[124:127], v164 offset:24576
	s_waitcnt lgkmcnt(7)
	v_mfma_f32_16x16x32_bf16 v[64:67], v[96:99], v[16:19], v[64:67]
	v_mfma_f32_16x16x32_bf16 v[68:71], v[96:99], v[48:51], v[68:71]
	v_xor_b32_e32 v164, 0x180, v163
	ds_read_b128 v[96:99], v164
	s_waitcnt lgkmcnt(7)
	v_mfma_f32_16x16x32_bf16 v[72:75], v[100:103], v[16:19], v[72:75]
	v_mfma_f32_16x16x32_bf16 v[76:79], v[100:103], v[48:51], v[76:79]
	ds_read_b128 v[100:103], v164 offset:8192
	s_waitcnt lgkmcnt(7)
	v_mfma_f32_16x16x32_bf16 v[80:83], v[104:107], v[16:19], v[80:83]
	v_mfma_f32_16x16x32_bf16 v[84:87], v[104:107], v[48:51], v[84:87]
	ds_read_b128 v[104:107], v164 offset:16384
	s_waitcnt lgkmcnt(7)
	v_mfma_f32_16x16x32_bf16 v[88:91], v[108:111], v[16:19], v[88:91]
	v_mfma_f32_16x16x32_bf16 v[92:95], v[108:111], v[48:51], v[92:95]
	ds_read_b128 v[108:111], v164 offset:24576
	s_waitcnt lgkmcnt(7)
	v_mfma_f32_16x16x32_bf16 v[64:67], v[112:115], v[20:23], v[64:67]
	v_mfma_f32_16x16x32_bf16 v[68:71], v[112:115], v[52:55], v[68:71]
	v_xor_b32_e32 v164, 0x1c0, v163
	ds_read_b128 v[112:115], v164
	s_waitcnt lgkmcnt(7)
	v_mfma_f32_16x16x32_bf16 v[72:75], v[116:119], v[20:23], v[72:75]
	v_mfma_f32_16x16x32_bf16 v[76:79], v[116:119], v[52:55], v[76:79]
	ds_read_b128 v[116:119], v164 offset:8192
	s_waitcnt lgkmcnt(7)
	v_mfma_f32_16x16x32_bf16 v[80:83], v[120:123], v[20:23], v[80:83]
	v_mfma_f32_16x16x32_bf16 v[84:87], v[120:123], v[52:55], v[84:87]
	ds_read_b128 v[120:123], v164 offset:16384
	s_waitcnt lgkmcnt(7)
	v_mfma_f32_16x16x32_bf16 v[88:91], v[124:127], v[20:23], v[88:91]
	v_mfma_f32_16x16x32_bf16 v[92:95], v[124:127], v[52:55], v[92:95]
	ds_read_b128 v[124:127], v164 offset:24576
	s_waitcnt lgkmcnt(7)
	v_mfma_f32_16x16x32_bf16 v[64:67], v[96:99], v[24:27], v[64:67]
	v_mfma_f32_16x16x32_bf16 v[68:71], v[96:99], v[56:59], v[68:71]
	s_waitcnt lgkmcnt(6)
	v_mfma_f32_16x16x32_bf16 v[72:75], v[100:103], v[24:27], v[72:75]
	v_mfma_f32_16x16x32_bf16 v[76:79], v[100:103], v[56:59], v[76:79]
	s_waitcnt lgkmcnt(5)
	v_mfma_f32_16x16x32_bf16 v[80:83], v[104:107], v[24:27], v[80:83]
	v_mfma_f32_16x16x32_bf16 v[84:87], v[104:107], v[56:59], v[84:87]
	s_waitcnt lgkmcnt(4)
	v_mfma_f32_16x16x32_bf16 v[88:91], v[108:111], v[24:27], v[88:91]
	v_mfma_f32_16x16x32_bf16 v[92:95], v[108:111], v[56:59], v[92:95]
	s_waitcnt lgkmcnt(3)
	v_mfma_f32_16x16x32_bf16 v[64:67], v[112:115], v[28:31], v[64:67]
	v_mfma_f32_16x16x32_bf16 v[68:71], v[112:115], v[60:63], v[68:71]
	s_waitcnt lgkmcnt(2)
	v_mfma_f32_16x16x32_bf16 v[72:75], v[116:119], v[28:31], v[72:75]
	v_mfma_f32_16x16x32_bf16 v[76:79], v[116:119], v[60:63], v[76:79]
	s_waitcnt lgkmcnt(1)
	v_mfma_f32_16x16x32_bf16 v[80:83], v[120:123], v[28:31], v[80:83]
	v_mfma_f32_16x16x32_bf16 v[84:87], v[120:123], v[60:63], v[84:87]
	s_waitcnt lgkmcnt(0)
	v_mfma_f32_16x16x32_bf16 v[88:91], v[124:127], v[28:31], v[88:91]
	v_mfma_f32_16x16x32_bf16 v[92:95], v[124:127], v[60:63], v[92:95]
	v_mov_b32_e32 v169, v165
	v_mov_b32_e32 v170, v166
	v_mov_b32_e32 v171, v167
	v_mov_b32_e32 v172, v168
	ds_read_u16 v144, v169
	ds_read_u16 v145, v170
	ds_read_u16 v146, v171
	ds_read_u16 v147, v172
	ds_read_u16 v148, v169 offset:8192
	ds_read_u16 v149, v170 offset:8192
	ds_read_u16 v150, v171 offset:8192
	ds_read_u16 v151, v172 offset:8192
	ds_read_u16 v152, v169 offset:16384
	ds_read_u16 v153, v170 offset:16384
	ds_read_u16 v154, v171 offset:16384
	ds_read_u16 v155, v172 offset:16384
	ds_read_u16 v156, v169 offset:24576
	ds_read_u16 v157, v170 offset:24576
	ds_read_u16 v158, v171 offset:24576
	ds_read_u16 v159, v172 offset:24576
	s_nop 7
	v_fma_f32 v178, v64, s53, v173
	v_fma_f32 v179, v65, s53, v173
	v_fma_f32 v180, v66, s53, v173
	v_fma_f32 v181, v67, s53, v173
	v_fma_f32 v182, v72, s53, v173
	v_fma_f32 v183, v73, s53, v173
	v_fma_f32 v184, v74, s53, v173
	v_fma_f32 v185, v75, s53, v173
	v_fma_f32 v186, v68, s53, v174
	v_fma_f32 v187, v69, s53, v174
	v_fma_f32 v188, v70, s53, v174
	v_fma_f32 v189, v71, s53, v174
	v_fma_f32 v190, v76, s53, v174
	v_fma_f32 v191, v77, s53, v174
	v_fma_f32 v192, v78, s53, v174
	v_fma_f32 v193, v79, s53, v174
	v_exp_f32_e32 v178, v178
	v_exp_f32_e32 v179, v179
	v_exp_f32_e32 v180, v180
	v_exp_f32_e32 v181, v181
	v_exp_f32_e32 v182, v182
	v_exp_f32_e32 v183, v183
	v_exp_f32_e32 v184, v184
	v_exp_f32_e32 v185, v185
	v_exp_f32_e32 v186, v186
	v_exp_f32_e32 v187, v187
	v_exp_f32_e32 v188, v188
	v_exp_f32_e32 v189, v189
	v_exp_f32_e32 v190, v190
	v_exp_f32_e32 v191, v191
	v_exp_f32_e32 v192, v192
	v_exp_f32_e32 v193, v193
	v_add_f32_e32 v178, 1.0, v178
	v_add_f32_e32 v179, 1.0, v179
	v_add_f32_e32 v180, 1.0, v180
	v_add_f32_e32 v181, 1.0, v181
	v_add_f32_e32 v182, 1.0, v182
	v_add_f32_e32 v183, 1.0, v183
	v_add_f32_e32 v184, 1.0, v184
	v_add_f32_e32 v185, 1.0, v185
	v_add_f32_e32 v186, 1.0, v186
	v_add_f32_e32 v187, 1.0, v187
	v_add_f32_e32 v188, 1.0, v188
	v_add_f32_e32 v189, 1.0, v189
	v_add_f32_e32 v190, 1.0, v190
	v_add_f32_e32 v191, 1.0, v191
	v_add_f32_e32 v192, 1.0, v192
	v_add_f32_e32 v193, 1.0, v193
	v_rcp_f32_e32 v178, v178
	v_rcp_f32_e32 v179, v179
	v_rcp_f32_e32 v180, v180
	v_rcp_f32_e32 v181, v181
	v_rcp_f32_e32 v182, v182
	v_rcp_f32_e32 v183, v183
	v_rcp_f32_e32 v184, v184
	v_rcp_f32_e32 v185, v185
	v_rcp_f32_e32 v186, v186
	v_rcp_f32_e32 v187, v187
	v_rcp_f32_e32 v188, v188
	v_rcp_f32_e32 v189, v189
	v_rcp_f32_e32 v190, v190
	v_rcp_f32_e32 v191, v191
	v_rcp_f32_e32 v192, v192
	v_rcp_f32_e32 v193, v193
	v_mul_f32_e32 v178, v175, v178
	v_mul_f32_e32 v179, v175, v179
	v_mul_f32_e32 v180, v175, v180
	v_mul_f32_e32 v181, v175, v181
	v_mul_f32_e32 v182, v175, v182
	v_mul_f32_e32 v183, v175, v183
	v_mul_f32_e32 v184, v175, v184
	v_mul_f32_e32 v185, v175, v185
	v_exp_f32_e32 v96, v178
	v_exp_f32_e32 v97, v179
	v_exp_f32_e32 v98, v180
	v_exp_f32_e32 v99, v181
	v_exp_f32_e32 v100, v182
	v_exp_f32_e32 v101, v183
	v_exp_f32_e32 v102, v184
	v_exp_f32_e32 v103, v185
	s_nop 0
	v_fma_f32 v194, -v96, v96, 1.0
	v_fma_f32 v195, -v97, v97, 1.0
	v_fma_f32 v196, -v98, v98, 1.0
	v_fma_f32 v197, -v99, v99, 1.0
	v_fma_f32 v198, -v100, v100, 1.0
	v_fma_f32 v199, -v101, v101, 1.0
	v_fma_f32 v200, -v102, v102, 1.0
	v_fma_f32 v201, -v103, v103, 1.0
	v_max_f32_e32 v194, 0, v194
	v_max_f32_e32 v195, 0, v195
	v_max_f32_e32 v196, 0, v196
	v_max_f32_e32 v197, 0, v197
	v_max_f32_e32 v198, 0, v198
	v_max_f32_e32 v199, 0, v199
	v_max_f32_e32 v200, 0, v200
	v_max_f32_e32 v201, 0, v201
	v_sqrt_f32_e32 v194, v194
	v_sqrt_f32_e32 v195, v195
	v_sqrt_f32_e32 v196, v196
	v_sqrt_f32_e32 v197, v197
	v_sqrt_f32_e32 v198, v198
	v_sqrt_f32_e32 v199, v199
	v_sqrt_f32_e32 v200, v200
	v_sqrt_f32_e32 v201, v201
	s_waitcnt lgkmcnt(8)
	v_lshlrev_b32_e32 v144, 16, v144
	v_lshlrev_b32_e32 v145, 16, v145
	v_lshlrev_b32_e32 v146, 16, v146
	v_lshlrev_b32_e32 v147, 16, v147
	v_lshlrev_b32_e32 v148, 16, v148
	v_lshlrev_b32_e32 v149, 16, v149
	v_lshlrev_b32_e32 v150, 16, v150
	v_lshlrev_b32_e32 v151, 16, v151
	v_mul_f32_e32 v194, v194, v186
	v_mul_f32_e32 v195, v195, v187
	v_mul_f32_e32 v196, v196, v188
	v_mul_f32_e32 v197, v197, v189
	v_mul_f32_e32 v198, v198, v190
	v_mul_f32_e32 v199, v199, v191
	v_mul_f32_e32 v200, v200, v192
	v_mul_f32_e32 v201, v201, v193
	v_mul_f32_e32 v144, v194, v144
	v_mul_f32_e32 v145, v195, v145
	v_mul_f32_e32 v146, v196, v146
	v_mul_f32_e32 v147, v197, v147
	v_mul_f32_e32 v148, v198, v148
	v_mul_f32_e32 v149, v199, v149
	v_mul_f32_e32 v150, v200, v150
	v_mul_f32_e32 v151, v201, v151
	v_fma_f32 v178, v80, s53, v173
	v_fma_f32 v179, v81, s53, v173
	v_fma_f32 v180, v82, s53, v173
	v_fma_f32 v181, v83, s53, v173
	v_fma_f32 v182, v88, s53, v173
	v_fma_f32 v183, v89, s53, v173
	v_fma_f32 v184, v90, s53, v173
	v_fma_f32 v185, v91, s53, v173
	v_fma_f32 v186, v84, s53, v174
	v_fma_f32 v187, v85, s53, v174
	v_fma_f32 v188, v86, s53, v174
	v_fma_f32 v189, v87, s53, v174
	v_fma_f32 v190, v92, s53, v174
	v_fma_f32 v191, v93, s53, v174
	v_fma_f32 v192, v94, s53, v174
	v_fma_f32 v193, v95, s53, v174
	v_exp_f32_e32 v178, v178
	v_exp_f32_e32 v179, v179
	v_exp_f32_e32 v180, v180
	v_exp_f32_e32 v181, v181
	v_exp_f32_e32 v182, v182
	v_exp_f32_e32 v183, v183
	v_exp_f32_e32 v184, v184
	v_exp_f32_e32 v185, v185
	v_exp_f32_e32 v186, v186
	v_exp_f32_e32 v187, v187
	v_exp_f32_e32 v188, v188
	v_exp_f32_e32 v189, v189
	v_exp_f32_e32 v190, v190
	v_exp_f32_e32 v191, v191
	v_exp_f32_e32 v192, v192
	v_exp_f32_e32 v193, v193
	v_add_f32_e32 v178, 1.0, v178
	v_add_f32_e32 v179, 1.0, v179
	v_add_f32_e32 v180, 1.0, v180
	v_add_f32_e32 v181, 1.0, v181
	v_add_f32_e32 v182, 1.0, v182
	v_add_f32_e32 v183, 1.0, v183
	v_add_f32_e32 v184, 1.0, v184
	v_add_f32_e32 v185, 1.0, v185
	v_add_f32_e32 v186, 1.0, v186
	v_add_f32_e32 v187, 1.0, v187
	v_add_f32_e32 v188, 1.0, v188
	v_add_f32_e32 v189, 1.0, v189
	v_add_f32_e32 v190, 1.0, v190
	v_add_f32_e32 v191, 1.0, v191
	v_add_f32_e32 v192, 1.0, v192
	v_add_f32_e32 v193, 1.0, v193
	v_rcp_f32_e32 v178, v178
	v_rcp_f32_e32 v179, v179
	v_rcp_f32_e32 v180, v180
	v_rcp_f32_e32 v181, v181
	v_rcp_f32_e32 v182, v182
	v_rcp_f32_e32 v183, v183
	v_rcp_f32_e32 v184, v184
	v_rcp_f32_e32 v185, v185
	v_rcp_f32_e32 v186, v186
	v_rcp_f32_e32 v187, v187
	v_rcp_f32_e32 v188, v188
	v_rcp_f32_e32 v189, v189
	v_rcp_f32_e32 v190, v190
	v_rcp_f32_e32 v191, v191
	v_rcp_f32_e32 v192, v192
	v_rcp_f32_e32 v193, v193
	v_mul_f32_e32 v178, v175, v178
	v_mul_f32_e32 v179, v175, v179
	v_mul_f32_e32 v180, v175, v180
	v_mul_f32_e32 v181, v175, v181
	v_mul_f32_e32 v182, v175, v182
	v_mul_f32_e32 v183, v175, v183
	v_mul_f32_e32 v184, v175, v184
	v_mul_f32_e32 v185, v175, v185
	v_exp_f32_e32 v104, v178
	v_exp_f32_e32 v105, v179
	v_exp_f32_e32 v106, v180
	v_exp_f32_e32 v107, v181
	v_exp_f32_e32 v108, v182
	v_exp_f32_e32 v109, v183
	v_exp_f32_e32 v110, v184
	v_exp_f32_e32 v111, v185
	s_nop 0
	v_fma_f32 v194, -v104, v104, 1.0
	v_fma_f32 v195, -v105, v105, 1.0
	v_fma_f32 v196, -v106, v106, 1.0
	v_fma_f32 v197, -v107, v107, 1.0
	v_fma_f32 v198, -v108, v108, 1.0
	v_fma_f32 v199, -v109, v109, 1.0
	v_fma_f32 v200, -v110, v110, 1.0
	v_fma_f32 v201, -v111, v111, 1.0
	v_max_f32_e32 v194, 0, v194
	v_max_f32_e32 v195, 0, v195
	v_max_f32_e32 v196, 0, v196
	v_max_f32_e32 v197, 0, v197
	v_max_f32_e32 v198, 0, v198
	v_max_f32_e32 v199, 0, v199
	v_max_f32_e32 v200, 0, v200
	v_max_f32_e32 v201, 0, v201
	v_sqrt_f32_e32 v194, v194
	v_sqrt_f32_e32 v195, v195
	v_sqrt_f32_e32 v196, v196
	v_sqrt_f32_e32 v197, v197
	v_sqrt_f32_e32 v198, v198
	v_sqrt_f32_e32 v199, v199
	v_sqrt_f32_e32 v200, v200
	v_sqrt_f32_e32 v201, v201
	s_waitcnt lgkmcnt(0)
	v_lshlrev_b32_e32 v152, 16, v152
	v_lshlrev_b32_e32 v153, 16, v153
	v_lshlrev_b32_e32 v154, 16, v154
	v_lshlrev_b32_e32 v155, 16, v155
	v_lshlrev_b32_e32 v156, 16, v156
	v_lshlrev_b32_e32 v157, 16, v157
	v_lshlrev_b32_e32 v158, 16, v158
	v_lshlrev_b32_e32 v159, 16, v159
	v_mul_f32_e32 v194, v194, v186
	v_mul_f32_e32 v195, v195, v187
	v_mul_f32_e32 v196, v196, v188
	v_mul_f32_e32 v197, v197, v189
	v_mul_f32_e32 v198, v198, v190
	v_mul_f32_e32 v199, v199, v191
	v_mul_f32_e32 v200, v200, v192
	v_mul_f32_e32 v201, v201, v193
	v_mul_f32_e32 v152, v194, v152
	v_mul_f32_e32 v153, v195, v153
	v_mul_f32_e32 v154, v196, v154
	v_mul_f32_e32 v155, v197, v155
	v_mul_f32_e32 v156, v198, v156
	v_mul_f32_e32 v157, v199, v157
	v_mul_f32_e32 v158, v200, v158
	v_mul_f32_e32 v159, v201, v159
	v_fma_f32 v146, v98, v147, v146
	v_fma_f32 v150, v102, v151, v150
	v_fma_f32 v154, v106, v155, v154
	v_fma_f32 v158, v110, v159, v158
	v_mul_f32_e32 v98, v98, v99
	v_mul_f32_e32 v102, v102, v103
	v_mul_f32_e32 v106, v106, v107
	v_mul_f32_e32 v110, v110, v111
	v_fma_f32 v145, v97, v146, v145
	v_fma_f32 v149, v101, v150, v149
	v_fma_f32 v153, v105, v154, v153
	v_fma_f32 v157, v109, v158, v157
	v_mul_f32_e32 v97, v97, v98
	v_mul_f32_e32 v101, v101, v102
	v_mul_f32_e32 v105, v105, v106
	v_mul_f32_e32 v109, v109, v110
	v_fma_f32 v144, v96, v145, v144
	v_fma_f32 v148, v100, v149, v148
	v_fma_f32 v152, v104, v153, v152
	v_fma_f32 v156, v108, v157, v156
	v_mul_f32_e32 v96, v96, v97
	v_mul_f32_e32 v100, v100, v101
	v_mul_f32_e32 v104, v104, v105
	v_mul_f32_e32 v108, v108, v109
	ds_bpermute_b32 v178, v204, v96
	ds_bpermute_b32 v182, v204, v144
	ds_bpermute_b32 v179, v204, v100
	ds_bpermute_b32 v183, v204, v148
	ds_bpermute_b32 v180, v204, v104
	ds_bpermute_b32 v184, v204, v152
	ds_bpermute_b32 v181, v204, v108
	ds_bpermute_b32 v185, v204, v156
	s_waitcnt lgkmcnt(0)
	v_fma_f32 v186, v182, v96, v144
	v_cndmask_b32_e64 v178, 1.0, v178, s[34:35]
	v_fma_f32 v187, v183, v100, v148
	v_cndmask_b32_e64 v179, 1.0, v179, s[34:35]
	v_fma_f32 v188, v184, v104, v152
	v_cndmask_b32_e64 v180, 1.0, v180, s[34:35]
	v_fma_f32 v189, v185, v108, v156
	v_cndmask_b32_e64 v181, 1.0, v181, s[34:35]
	v_cndmask_b32_e64 v223, v144, v186, s[34:35]
	v_mul_f32_e32 v219, v96, v178
	v_cndmask_b32_e64 v224, v148, v187, s[34:35]
	v_mul_f32_e32 v220, v100, v179
	v_cndmask_b32_e64 v225, v152, v188, s[34:35]
	v_mul_f32_e32 v221, v104, v180
	v_cndmask_b32_e64 v226, v156, v189, s[34:35]
	v_mul_f32_e32 v222, v108, v181
	ds_bpermute_b32 v178, v205, v219
	ds_bpermute_b32 v182, v205, v223
	ds_bpermute_b32 v179, v205, v220
	ds_bpermute_b32 v183, v205, v224
	ds_bpermute_b32 v180, v205, v221
	ds_bpermute_b32 v184, v205, v225
	ds_bpermute_b32 v181, v205, v222
	ds_bpermute_b32 v185, v205, v226
	s_waitcnt lgkmcnt(0)
	v_fma_f32 v186, v182, v219, v223
	v_cndmask_b32_e64 v178, 1.0, v178, s[36:37]
	v_fma_f32 v187, v183, v220, v224
	v_cndmask_b32_e64 v179, 1.0, v179, s[36:37]
	v_fma_f32 v188, v184, v221, v225
	v_cndmask_b32_e64 v180, 1.0, v180, s[36:37]
	v_fma_f32 v189, v185, v222, v226
	v_cndmask_b32_e64 v181, 1.0, v181, s[36:37]
	v_cndmask_b32_e64 v223, v223, v186, s[36:37]
	v_mul_f32_e32 v219, v219, v178
	v_cndmask_b32_e64 v224, v224, v187, s[36:37]
	v_mul_f32_e32 v220, v220, v179
	v_cndmask_b32_e64 v225, v225, v188, s[36:37]
	v_mul_f32_e32 v221, v221, v180
	v_cndmask_b32_e64 v226, v226, v189, s[36:37]
	v_mul_f32_e32 v222, v222, v181
	ds_bpermute_b32 v227, v204, v219
	ds_bpermute_b32 v231, v204, v223
	ds_bpermute_b32 v235, v206, v219
	ds_bpermute_b32 v239, v206, v223
	ds_bpermute_b32 v228, v204, v220
	ds_bpermute_b32 v232, v204, v224
	ds_bpermute_b32 v236, v206, v220
	ds_bpermute_b32 v244, v206, v224
	ds_bpermute_b32 v229, v204, v221
	ds_bpermute_b32 v233, v204, v225
	ds_bpermute_b32 v237, v206, v221
	ds_bpermute_b32 v245, v206, v225
	ds_bpermute_b32 v230, v204, v222
	ds_bpermute_b32 v234, v204, v226
	ds_bpermute_b32 v238, v206, v222
	ds_bpermute_b32 v246, v206, v226
	s_waitcnt lgkmcnt(0)
	v_cndmask_b32_e64 v227, 1.0, v227, s[34:35]
	v_cndmask_b32_e64 v231, 0, v231, s[34:35]
	v_cndmask_b32_e64 v228, 1.0, v228, s[34:35]
	v_cndmask_b32_e64 v232, 0, v232, s[34:35]
	v_cndmask_b32_e64 v229, 1.0, v229, s[34:35]
	v_cndmask_b32_e64 v233, 0, v233, s[34:35]
	v_cndmask_b32_e64 v230, 1.0, v230, s[34:35]
	v_cndmask_b32_e64 v234, 0, v234, s[34:35]
	v_mov_b32_e32 v190, v238
	v_mov_b32_e32 v194, v246
	v_mov_b32_e32 v198, v190
	v_mov_b32_e32 v201, v194
	v_fma_f32 v194, v194, v237, v245
	v_mul_f32_e32 v190, v190, v237
	v_mov_b32_e32 v199, v190
	v_mov_b32_e32 v177, v194
	v_fma_f32 v194, v194, v236, v244
	v_mul_f32_e32 v190, v190, v236
	v_mov_b32_e32 v200, v190
	v_mov_b32_e32 v203, v194
	v_fma_f32 v194, v194, v235, v239
	v_mul_f32_e32 v190, v190, v235
	v_mov_b32_e32 v191, v194
	ds_write_b64 v207, v[190:191]
	s_waitcnt lgkmcnt(0)
	s_barrier
	ds_read_b64 v[178:179], v208 offset:512
	ds_read_b64 v[180:181], v208
	s_waitcnt lgkmcnt(0)
	v_fma_f32 v182, v176, v178, v179
	v_cndmask_b32_e64 v183, v176, v182, s[38:39]
	v_fma_f32 v176, v182, v180, v181
	s_add_i32 s13, s13, 1
	s_waitcnt vmcnt(0)
	s_barrier
	s_cmp_eq_u32 s13, 17
	s_cbranch_scc1 .Lmylru_nodma_6
	s_add_i32 s58, s13, 1
	s_cmp_lt_u32 s58, 2
	s_sub_i32 s50, 1, s58
	s_lshl_b32 s50, s50, 7
	s_lshl_b32 s51, s9, 8
	s_add_i32 s51, s51, 0x8000
	s_add_i32 s51, s51, s50
	s_sub_i32 s50, 17, s58
	s_lshl_b32 s50, s50, 7
	s_lshl_b32 s59, s9, 11
	s_add_i32 s59, s59, s50
	s_cmp_lt_u32 s58, 2
	s_cselect_b32 s59, s51, s59
	s_lshl_b32 s52, s59, 11
	s_add_u32 s46, s16, s52
	s_addc_u32 s47, s17, 0
	s_lshl_b32 s52, s6, 13
	s_mov_b32 m0, s52
	s_add_i32 s52, s52, 0x400
	global_load_lds_dwordx4 v211, s[46:47]
	s_mov_b32 m0, s52
	s_add_i32 s52, s52, 0x400
	global_load_lds_dwordx4 v212, s[46:47]
	s_mov_b32 m0, s52
	s_add_i32 s52, s52, 0x400
	global_load_lds_dwordx4 v213, s[46:47]
	s_mov_b32 m0, s52
	s_add_i32 s52, s52, 0x400
	global_load_lds_dwordx4 v214, s[46:47]
	s_mov_b32 m0, s52
	s_add_i32 s52, s52, 0x400
	global_load_lds_dwordx4 v215, s[46:47]
	s_mov_b32 m0, s52
	s_add_i32 s52, s52, 0x400
	global_load_lds_dwordx4 v216, s[46:47]
	s_mov_b32 m0, s52
	s_add_i32 s52, s52, 0x400
	global_load_lds_dwordx4 v217, s[46:47]
	s_mov_b32 m0, s52
	s_nop 0
	global_load_lds_dwordx4 v218, s[46:47]
.Lmylru_nodma_6:
	v_or_b32_e32 v163, 0x10000, v162
	ds_read_b128 v[96:99], v163
	ds_read_b128 v[100:103], v163 offset:8192
	ds_read_b128 v[104:107], v163 offset:16384
	ds_read_b128 v[108:111], v163 offset:24576
	v_xor_b32_e32 v164, 0x40, v163
	ds_read_b128 v[112:115], v164
	ds_read_b128 v[116:119], v164 offset:8192
	ds_read_b128 v[120:123], v164 offset:16384
	ds_read_b128 v[124:127], v164 offset:24576
	s_waitcnt lgkmcnt(7)
	v_mfma_f32_16x16x32_bf16 v[64:67], v[96:99], v[0:3], 0
	v_mfma_f32_16x16x32_bf16 v[68:71], v[96:99], v[32:35], 0
	v_xor_b32_e32 v164, 0x80, v163
	ds_read_b128 v[96:99], v164
	s_waitcnt lgkmcnt(7)
	v_mfma_f32_16x16x32_bf16 v[72:75], v[100:103], v[0:3], 0
	v_mfma_f32_16x16x32_bf16 v[76:79], v[100:103], v[32:35], 0
	ds_read_b128 v[100:103], v164 offset:8192
	s_waitcnt lgkmcnt(7)
	v_mfma_f32_16x16x32_bf16 v[80:83], v[104:107], v[0:3], 0
	v_mfma_f32_16x16x32_bf16 v[84:87], v[104:107], v[32:35], 0
	ds_read_b128 v[104:107], v164 offset:16384
	s_waitcnt lgkmcnt(7)
	v_mfma_f32_16x16x32_bf16 v[88:91], v[108:111], v[0:3], 0
	v_mfma_f32_16x16x32_bf16 v[92:95], v[108:111], v[32:35], 0
	ds_read_b128 v[108:111], v164 offset:24576
	s_waitcnt lgkmcnt(7)
	v_mfma_f32_16x16x32_bf16 v[64:67], v[112:115], v[4:7], v[64:67]
	v_mfma_f32_16x16x32_bf16 v[68:71], v[112:115], v[36:39], v[68:71]
	v_xor_b32_e32 v164, 0xc0, v163
	ds_read_b128 v[112:115], v164
	s_waitcnt lgkmcnt(7)
	v_mfma_f32_16x16x32_bf16 v[72:75], v[116:119], v[4:7], v[72:75]
	v_mfma_f32_16x16x32_bf16 v[76:79], v[116:119], v[36:39], v[76:79]
	ds_read_b128 v[116:119], v164 offset:8192
	s_waitcnt lgkmcnt(7)
	v_mfma_f32_16x16x32_bf16 v[80:83], v[120:123], v[4:7], v[80:83]
	v_mfma_f32_16x16x32_bf16 v[84:87], v[120:123], v[36:39], v[84:87]
	ds_read_b128 v[120:123], v164 offset:16384
	s_waitcnt lgkmcnt(7)
	v_mfma_f32_16x16x32_bf16 v[88:91], v[124:127], v[4:7], v[88:91]
	v_mfma_f32_16x16x32_bf16 v[92:95], v[124:127], v[36:39], v[92:95]
	ds_read_b128 v[124:127], v164 offset:24576
	s_waitcnt lgkmcnt(7)
	v_mfma_f32_16x16x32_bf16 v[64:67], v[96:99], v[8:11], v[64:67]
	v_mfma_f32_16x16x32_bf16 v[68:71], v[96:99], v[40:43], v[68:71]
	v_xor_b32_e32 v164, 0x100, v163
	ds_read_b128 v[96:99], v164
	s_waitcnt lgkmcnt(7)
	v_mfma_f32_16x16x32_bf16 v[72:75], v[100:103], v[8:11], v[72:75]
	v_mfma_f32_16x16x32_bf16 v[76:79], v[100:103], v[40:43], v[76:79]
	ds_read_b128 v[100:103], v164 offset:8192
	s_waitcnt lgkmcnt(7)
	v_mfma_f32_16x16x32_bf16 v[80:83], v[104:107], v[8:11], v[80:83]
	v_mfma_f32_16x16x32_bf16 v[84:87], v[104:107], v[40:43], v[84:87]
	ds_read_b128 v[104:107], v164 offset:16384
	s_waitcnt lgkmcnt(7)
	v_mfma_f32_16x16x32_bf16 v[88:91], v[108:111], v[8:11], v[88:91]
	v_mfma_f32_16x16x32_bf16 v[92:95], v[108:111], v[40:43], v[92:95]
	ds_read_b128 v[108:111], v164 offset:24576
	s_waitcnt lgkmcnt(7)
	v_mfma_f32_16x16x32_bf16 v[64:67], v[112:115], v[12:15], v[64:67]
	v_mfma_f32_16x16x32_bf16 v[68:71], v[112:115], v[44:47], v[68:71]
	v_xor_b32_e32 v164, 0x140, v163
	ds_read_b128 v[112:115], v164
	s_waitcnt lgkmcnt(7)
	v_mfma_f32_16x16x32_bf16 v[72:75], v[116:119], v[12:15], v[72:75]
	v_mfma_f32_16x16x32_bf16 v[76:79], v[116:119], v[44:47], v[76:79]
	ds_read_b128 v[116:119], v164 offset:8192
	s_waitcnt lgkmcnt(7)
	v_mfma_f32_16x16x32_bf16 v[80:83], v[120:123], v[12:15], v[80:83]
	v_mfma_f32_16x16x32_bf16 v[84:87], v[120:123], v[44:47], v[84:87]
	ds_read_b128 v[120:123], v164 offset:16384
	s_waitcnt lgkmcnt(7)
	v_mfma_f32_16x16x32_bf16 v[88:91], v[124:127], v[12:15], v[88:91]
	v_mfma_f32_16x16x32_bf16 v[92:95], v[124:127], v[44:47], v[92:95]
	ds_read_b128 v[124:127], v164 offset:24576
	s_waitcnt lgkmcnt(7)
	v_mfma_f32_16x16x32_bf16 v[64:67], v[96:99], v[16:19], v[64:67]
	v_mfma_f32_16x16x32_bf16 v[68:71], v[96:99], v[48:51], v[68:71]
	v_xor_b32_e32 v164, 0x180, v163
	ds_read_b128 v[96:99], v164
	s_waitcnt lgkmcnt(7)
	v_mfma_f32_16x16x32_bf16 v[72:75], v[100:103], v[16:19], v[72:75]
	v_mfma_f32_16x16x32_bf16 v[76:79], v[100:103], v[48:51], v[76:79]
	ds_read_b128 v[100:103], v164 offset:8192
	s_waitcnt lgkmcnt(7)
	v_mfma_f32_16x16x32_bf16 v[80:83], v[104:107], v[16:19], v[80:83]
	v_mfma_f32_16x16x32_bf16 v[84:87], v[104:107], v[48:51], v[84:87]
	ds_read_b128 v[104:107], v164 offset:16384
	s_waitcnt lgkmcnt(7)
	v_mfma_f32_16x16x32_bf16 v[88:91], v[108:111], v[16:19], v[88:91]
	v_mfma_f32_16x16x32_bf16 v[92:95], v[108:111], v[48:51], v[92:95]
	ds_read_b128 v[108:111], v164 offset:24576
	s_waitcnt lgkmcnt(7)
	v_mfma_f32_16x16x32_bf16 v[64:67], v[112:115], v[20:23], v[64:67]
	v_mfma_f32_16x16x32_bf16 v[68:71], v[112:115], v[52:55], v[68:71]
	v_xor_b32_e32 v164, 0x1c0, v163
	ds_read_b128 v[112:115], v164
	s_waitcnt lgkmcnt(7)
	v_mfma_f32_16x16x32_bf16 v[72:75], v[116:119], v[20:23], v[72:75]
	v_mfma_f32_16x16x32_bf16 v[76:79], v[116:119], v[52:55], v[76:79]
	ds_read_b128 v[116:119], v164 offset:8192
	s_waitcnt lgkmcnt(7)
	v_mfma_f32_16x16x32_bf16 v[80:83], v[120:123], v[20:23], v[80:83]
	v_mfma_f32_16x16x32_bf16 v[84:87], v[120:123], v[52:55], v[84:87]
	ds_read_b128 v[120:123], v164 offset:16384
	s_waitcnt lgkmcnt(7)
	v_mfma_f32_16x16x32_bf16 v[88:91], v[124:127], v[20:23], v[88:91]
	v_mfma_f32_16x16x32_bf16 v[92:95], v[124:127], v[52:55], v[92:95]
	ds_read_b128 v[124:127], v164 offset:24576
	s_waitcnt lgkmcnt(7)
	v_mfma_f32_16x16x32_bf16 v[64:67], v[96:99], v[24:27], v[64:67]
	v_mfma_f32_16x16x32_bf16 v[68:71], v[96:99], v[56:59], v[68:71]
	s_waitcnt lgkmcnt(6)
	v_mfma_f32_16x16x32_bf16 v[72:75], v[100:103], v[24:27], v[72:75]
	v_mfma_f32_16x16x32_bf16 v[76:79], v[100:103], v[56:59], v[76:79]
	s_waitcnt lgkmcnt(5)
	v_mfma_f32_16x16x32_bf16 v[80:83], v[104:107], v[24:27], v[80:83]
	v_mfma_f32_16x16x32_bf16 v[84:87], v[104:107], v[56:59], v[84:87]
	s_waitcnt lgkmcnt(4)
	v_mfma_f32_16x16x32_bf16 v[88:91], v[108:111], v[24:27], v[88:91]
	v_mfma_f32_16x16x32_bf16 v[92:95], v[108:111], v[56:59], v[92:95]
	s_waitcnt lgkmcnt(3)
	v_mfma_f32_16x16x32_bf16 v[64:67], v[112:115], v[28:31], v[64:67]
	v_mfma_f32_16x16x32_bf16 v[68:71], v[112:115], v[60:63], v[68:71]
	s_waitcnt lgkmcnt(2)
	v_mfma_f32_16x16x32_bf16 v[72:75], v[116:119], v[28:31], v[72:75]
	v_mfma_f32_16x16x32_bf16 v[76:79], v[116:119], v[60:63], v[76:79]
	s_waitcnt lgkmcnt(1)
	v_mfma_f32_16x16x32_bf16 v[80:83], v[120:123], v[28:31], v[80:83]
	v_mfma_f32_16x16x32_bf16 v[84:87], v[120:123], v[60:63], v[84:87]
	s_waitcnt lgkmcnt(0)
	v_mfma_f32_16x16x32_bf16 v[88:91], v[124:127], v[28:31], v[88:91]
	v_mfma_f32_16x16x32_bf16 v[92:95], v[124:127], v[60:63], v[92:95]
	v_or_b32_e32 v169, 0x10000, v165
	v_or_b32_e32 v170, 0x10000, v166
	v_or_b32_e32 v171, 0x10000, v167
	v_or_b32_e32 v172, 0x10000, v168
	ds_read_u16 v144, v169
	ds_read_u16 v145, v170
	ds_read_u16 v146, v171
	ds_read_u16 v147, v172
	ds_read_u16 v148, v169 offset:8192
	ds_read_u16 v149, v170 offset:8192
	ds_read_u16 v150, v171 offset:8192
	ds_read_u16 v151, v172 offset:8192
	ds_read_u16 v152, v169 offset:16384
	ds_read_u16 v153, v170 offset:16384
	ds_read_u16 v154, v171 offset:16384
	ds_read_u16 v155, v172 offset:16384
	ds_read_u16 v156, v169 offset:24576
	ds_read_u16 v157, v170 offset:24576
	ds_read_u16 v158, v171 offset:24576
	ds_read_u16 v159, v172 offset:24576
	s_nop 7
	v_fma_f32 v178, v64, s53, v173
	v_fma_f32 v179, v65, s53, v173
	v_fma_f32 v180, v66, s53, v173
	v_fma_f32 v181, v67, s53, v173
	v_fma_f32 v182, v72, s53, v173
	v_fma_f32 v183, v73, s53, v173
	v_fma_f32 v184, v74, s53, v173
	v_fma_f32 v185, v75, s53, v173
	v_fma_f32 v186, v68, s53, v174
	v_fma_f32 v187, v69, s53, v174
	v_fma_f32 v188, v70, s53, v174
	v_fma_f32 v189, v71, s53, v174
	v_fma_f32 v190, v76, s53, v174
	v_fma_f32 v191, v77, s53, v174
	v_fma_f32 v192, v78, s53, v174
	v_fma_f32 v193, v79, s53, v174
	v_exp_f32_e32 v178, v178
	v_exp_f32_e32 v179, v179
	v_exp_f32_e32 v180, v180
	v_exp_f32_e32 v181, v181
	v_exp_f32_e32 v182, v182
	v_exp_f32_e32 v183, v183
	v_exp_f32_e32 v184, v184
	v_exp_f32_e32 v185, v185
	v_exp_f32_e32 v186, v186
	v_exp_f32_e32 v187, v187
	v_exp_f32_e32 v188, v188
	v_exp_f32_e32 v189, v189
	v_exp_f32_e32 v190, v190
	v_exp_f32_e32 v191, v191
	v_exp_f32_e32 v192, v192
	v_exp_f32_e32 v193, v193
	v_add_f32_e32 v178, 1.0, v178
	v_add_f32_e32 v179, 1.0, v179
	v_add_f32_e32 v180, 1.0, v180
	v_add_f32_e32 v181, 1.0, v181
	v_add_f32_e32 v182, 1.0, v182
	v_add_f32_e32 v183, 1.0, v183
	v_add_f32_e32 v184, 1.0, v184
	v_add_f32_e32 v185, 1.0, v185
	v_add_f32_e32 v186, 1.0, v186
	v_add_f32_e32 v187, 1.0, v187
	v_add_f32_e32 v188, 1.0, v188
	v_add_f32_e32 v189, 1.0, v189
	v_add_f32_e32 v190, 1.0, v190
	v_add_f32_e32 v191, 1.0, v191
	v_add_f32_e32 v192, 1.0, v192
	v_add_f32_e32 v193, 1.0, v193
	v_rcp_f32_e32 v178, v178
	v_rcp_f32_e32 v179, v179
	v_rcp_f32_e32 v180, v180
	v_rcp_f32_e32 v181, v181
	v_rcp_f32_e32 v182, v182
	v_rcp_f32_e32 v183, v183
	v_rcp_f32_e32 v184, v184
	v_rcp_f32_e32 v185, v185
	v_rcp_f32_e32 v186, v186
	v_rcp_f32_e32 v187, v187
	v_rcp_f32_e32 v188, v188
	v_rcp_f32_e32 v189, v189
	v_rcp_f32_e32 v190, v190
	v_rcp_f32_e32 v191, v191
	v_rcp_f32_e32 v192, v192
	v_rcp_f32_e32 v193, v193
	v_mul_f32_e32 v178, v175, v178
	v_mul_f32_e32 v179, v175, v179
	v_mul_f32_e32 v180, v175, v180
	v_mul_f32_e32 v181, v175, v181
	v_mul_f32_e32 v182, v175, v182
	v_mul_f32_e32 v183, v175, v183
	v_mul_f32_e32 v184, v175, v184
	v_mul_f32_e32 v185, v175, v185
	v_exp_f32_e32 v96, v178
	v_exp_f32_e32 v97, v179
	v_exp_f32_e32 v98, v180
	v_exp_f32_e32 v99, v181
	v_exp_f32_e32 v100, v182
	v_exp_f32_e32 v101, v183
	v_exp_f32_e32 v102, v184
	v_exp_f32_e32 v103, v185
	s_nop 0
	v_fma_f32 v194, -v96, v96, 1.0
	v_fma_f32 v195, -v97, v97, 1.0
	v_fma_f32 v196, -v98, v98, 1.0
	v_fma_f32 v197, -v99, v99, 1.0
	v_fma_f32 v198, -v100, v100, 1.0
	v_fma_f32 v199, -v101, v101, 1.0
	v_fma_f32 v200, -v102, v102, 1.0
	v_fma_f32 v201, -v103, v103, 1.0
	v_max_f32_e32 v194, 0, v194
	v_max_f32_e32 v195, 0, v195
	v_max_f32_e32 v196, 0, v196
	v_max_f32_e32 v197, 0, v197
	v_max_f32_e32 v198, 0, v198
	v_max_f32_e32 v199, 0, v199
	v_max_f32_e32 v200, 0, v200
	v_max_f32_e32 v201, 0, v201
	v_sqrt_f32_e32 v194, v194
	v_sqrt_f32_e32 v195, v195
	v_sqrt_f32_e32 v196, v196
	v_sqrt_f32_e32 v197, v197
	v_sqrt_f32_e32 v198, v198
	v_sqrt_f32_e32 v199, v199
	v_sqrt_f32_e32 v200, v200
	v_sqrt_f32_e32 v201, v201
	s_waitcnt lgkmcnt(8)
	v_lshlrev_b32_e32 v144, 16, v144
	v_lshlrev_b32_e32 v145, 16, v145
	v_lshlrev_b32_e32 v146, 16, v146
	v_lshlrev_b32_e32 v147, 16, v147
	v_lshlrev_b32_e32 v148, 16, v148
	v_lshlrev_b32_e32 v149, 16, v149
	v_lshlrev_b32_e32 v150, 16, v150
	v_lshlrev_b32_e32 v151, 16, v151
	v_mul_f32_e32 v194, v194, v186
	v_mul_f32_e32 v195, v195, v187
	v_mul_f32_e32 v196, v196, v188
	v_mul_f32_e32 v197, v197, v189
	v_mul_f32_e32 v198, v198, v190
	v_mul_f32_e32 v199, v199, v191
	v_mul_f32_e32 v200, v200, v192
	v_mul_f32_e32 v201, v201, v193
	v_mul_f32_e32 v144, v194, v144
	v_mul_f32_e32 v145, v195, v145
	v_mul_f32_e32 v146, v196, v146
	v_mul_f32_e32 v147, v197, v147
	v_mul_f32_e32 v148, v198, v148
	v_mul_f32_e32 v149, v199, v149
	v_mul_f32_e32 v150, v200, v150
	v_mul_f32_e32 v151, v201, v151
	v_fma_f32 v178, v80, s53, v173
	v_fma_f32 v179, v81, s53, v173
	v_fma_f32 v180, v82, s53, v173
	v_fma_f32 v181, v83, s53, v173
	v_fma_f32 v182, v88, s53, v173
	v_fma_f32 v183, v89, s53, v173
	v_fma_f32 v184, v90, s53, v173
	v_fma_f32 v185, v91, s53, v173
	v_fma_f32 v186, v84, s53, v174
	v_fma_f32 v187, v85, s53, v174
	v_fma_f32 v188, v86, s53, v174
	v_fma_f32 v189, v87, s53, v174
	v_fma_f32 v190, v92, s53, v174
	v_fma_f32 v191, v93, s53, v174
	v_fma_f32 v192, v94, s53, v174
	v_fma_f32 v193, v95, s53, v174
	v_exp_f32_e32 v178, v178
	v_exp_f32_e32 v179, v179
	v_exp_f32_e32 v180, v180
	v_exp_f32_e32 v181, v181
	v_exp_f32_e32 v182, v182
	v_exp_f32_e32 v183, v183
	v_exp_f32_e32 v184, v184
	v_exp_f32_e32 v185, v185
	v_exp_f32_e32 v186, v186
	v_exp_f32_e32 v187, v187
	v_exp_f32_e32 v188, v188
	v_exp_f32_e32 v189, v189
	v_exp_f32_e32 v190, v190
	v_exp_f32_e32 v191, v191
	v_exp_f32_e32 v192, v192
	v_exp_f32_e32 v193, v193
	v_add_f32_e32 v178, 1.0, v178
	v_add_f32_e32 v179, 1.0, v179
	v_add_f32_e32 v180, 1.0, v180
	v_add_f32_e32 v181, 1.0, v181
	v_add_f32_e32 v182, 1.0, v182
	v_add_f32_e32 v183, 1.0, v183
	v_add_f32_e32 v184, 1.0, v184
	v_add_f32_e32 v185, 1.0, v185
	v_add_f32_e32 v186, 1.0, v186
	v_add_f32_e32 v187, 1.0, v187
	v_add_f32_e32 v188, 1.0, v188
	v_add_f32_e32 v189, 1.0, v189
	v_add_f32_e32 v190, 1.0, v190
	v_add_f32_e32 v191, 1.0, v191
	v_add_f32_e32 v192, 1.0, v192
	v_add_f32_e32 v193, 1.0, v193
	v_rcp_f32_e32 v178, v178
	v_rcp_f32_e32 v179, v179
	v_rcp_f32_e32 v180, v180
	v_rcp_f32_e32 v181, v181
	v_rcp_f32_e32 v182, v182
	v_rcp_f32_e32 v183, v183
	v_rcp_f32_e32 v184, v184
	v_rcp_f32_e32 v185, v185
	v_rcp_f32_e32 v186, v186
	v_rcp_f32_e32 v187, v187
	v_rcp_f32_e32 v188, v188
	v_rcp_f32_e32 v189, v189
	v_rcp_f32_e32 v190, v190
	v_rcp_f32_e32 v191, v191
	v_rcp_f32_e32 v192, v192
	v_rcp_f32_e32 v193, v193
	v_mul_f32_e32 v178, v175, v178
	v_mul_f32_e32 v179, v175, v179
	v_mul_f32_e32 v180, v175, v180
	v_mul_f32_e32 v181, v175, v181
	v_mul_f32_e32 v182, v175, v182
	v_mul_f32_e32 v183, v175, v183
	v_mul_f32_e32 v184, v175, v184
	v_mul_f32_e32 v185, v175, v185
	v_exp_f32_e32 v104, v178
	v_exp_f32_e32 v105, v179
	v_exp_f32_e32 v106, v180
	v_exp_f32_e32 v107, v181
	v_exp_f32_e32 v108, v182
	v_exp_f32_e32 v109, v183
	v_exp_f32_e32 v110, v184
	v_exp_f32_e32 v111, v185
	s_nop 0
	v_fma_f32 v194, -v104, v104, 1.0
	v_fma_f32 v195, -v105, v105, 1.0
	v_fma_f32 v196, -v106, v106, 1.0
	v_fma_f32 v197, -v107, v107, 1.0
	v_fma_f32 v198, -v108, v108, 1.0
	v_fma_f32 v199, -v109, v109, 1.0
	v_fma_f32 v200, -v110, v110, 1.0
	v_fma_f32 v201, -v111, v111, 1.0
	v_max_f32_e32 v194, 0, v194
	v_max_f32_e32 v195, 0, v195
	v_max_f32_e32 v196, 0, v196
	v_max_f32_e32 v197, 0, v197
	v_max_f32_e32 v198, 0, v198
	v_max_f32_e32 v199, 0, v199
	v_max_f32_e32 v200, 0, v200
	v_max_f32_e32 v201, 0, v201
	v_sqrt_f32_e32 v194, v194
	v_sqrt_f32_e32 v195, v195
	v_sqrt_f32_e32 v196, v196
	v_sqrt_f32_e32 v197, v197
	v_sqrt_f32_e32 v198, v198
	v_sqrt_f32_e32 v199, v199
	v_sqrt_f32_e32 v200, v200
	v_sqrt_f32_e32 v201, v201
	s_waitcnt lgkmcnt(0)
	v_lshlrev_b32_e32 v152, 16, v152
	v_lshlrev_b32_e32 v153, 16, v153
	v_lshlrev_b32_e32 v154, 16, v154
	v_lshlrev_b32_e32 v155, 16, v155
	v_lshlrev_b32_e32 v156, 16, v156
	v_lshlrev_b32_e32 v157, 16, v157
	v_lshlrev_b32_e32 v158, 16, v158
	v_lshlrev_b32_e32 v159, 16, v159
	v_mul_f32_e32 v194, v194, v186
	v_mul_f32_e32 v195, v195, v187
	v_mul_f32_e32 v196, v196, v188
	v_mul_f32_e32 v197, v197, v189
	v_mul_f32_e32 v198, v198, v190
	v_mul_f32_e32 v199, v199, v191
	v_mul_f32_e32 v200, v200, v192
	v_mul_f32_e32 v201, v201, v193
	v_mul_f32_e32 v152, v194, v152
	v_mul_f32_e32 v153, v195, v153
	v_mul_f32_e32 v154, v196, v154
	v_mul_f32_e32 v155, v197, v155
	v_mul_f32_e32 v156, v198, v156
	v_mul_f32_e32 v157, v199, v157
	v_mul_f32_e32 v158, v200, v158
	v_mul_f32_e32 v159, v201, v159
	v_fma_f32 v146, v98, v147, v146
	v_fma_f32 v150, v102, v151, v150
	v_fma_f32 v154, v106, v155, v154
	v_fma_f32 v158, v110, v159, v158
	v_mul_f32_e32 v98, v98, v99
	v_mul_f32_e32 v102, v102, v103
	v_mul_f32_e32 v106, v106, v107
	v_mul_f32_e32 v110, v110, v111
	v_fma_f32 v145, v97, v146, v145
	v_fma_f32 v149, v101, v150, v149
	v_fma_f32 v153, v105, v154, v153
	v_fma_f32 v157, v109, v158, v157
	v_mul_f32_e32 v97, v97, v98
	v_mul_f32_e32 v101, v101, v102
	v_mul_f32_e32 v105, v105, v106
	v_mul_f32_e32 v109, v109, v110
	v_fma_f32 v144, v96, v145, v144
	v_fma_f32 v148, v100, v149, v148
	v_fma_f32 v152, v104, v153, v152
	v_fma_f32 v156, v108, v157, v156
	v_mul_f32_e32 v96, v96, v97
	v_mul_f32_e32 v100, v100, v101
	v_mul_f32_e32 v104, v104, v105
	v_mul_f32_e32 v108, v108, v109
	ds_bpermute_b32 v178, v204, v96
	ds_bpermute_b32 v182, v204, v144
	ds_bpermute_b32 v179, v204, v100
	ds_bpermute_b32 v183, v204, v148
	ds_bpermute_b32 v180, v204, v104
	ds_bpermute_b32 v184, v204, v152
	ds_bpermute_b32 v181, v204, v108
	ds_bpermute_b32 v185, v204, v156
	s_waitcnt lgkmcnt(0)
	v_fma_f32 v186, v182, v96, v144
	v_cndmask_b32_e64 v178, 1.0, v178, s[34:35]
	v_fma_f32 v187, v183, v100, v148
	v_cndmask_b32_e64 v179, 1.0, v179, s[34:35]
	v_fma_f32 v188, v184, v104, v152
	v_cndmask_b32_e64 v180, 1.0, v180, s[34:35]
	v_fma_f32 v189, v185, v108, v156
	v_cndmask_b32_e64 v181, 1.0, v181, s[34:35]
	v_cndmask_b32_e64 v223, v144, v186, s[34:35]
	v_mul_f32_e32 v219, v96, v178
	v_cndmask_b32_e64 v224, v148, v187, s[34:35]
	v_mul_f32_e32 v220, v100, v179
	v_cndmask_b32_e64 v225, v152, v188, s[34:35]
	v_mul_f32_e32 v221, v104, v180
	v_cndmask_b32_e64 v226, v156, v189, s[34:35]
	v_mul_f32_e32 v222, v108, v181
	ds_bpermute_b32 v178, v205, v219
	ds_bpermute_b32 v182, v205, v223
	ds_bpermute_b32 v179, v205, v220
	ds_bpermute_b32 v183, v205, v224
	ds_bpermute_b32 v180, v205, v221
	ds_bpermute_b32 v184, v205, v225
	ds_bpermute_b32 v181, v205, v222
	ds_bpermute_b32 v185, v205, v226
	s_waitcnt lgkmcnt(0)
	v_fma_f32 v186, v182, v219, v223
	v_cndmask_b32_e64 v178, 1.0, v178, s[36:37]
	v_fma_f32 v187, v183, v220, v224
	v_cndmask_b32_e64 v179, 1.0, v179, s[36:37]
	v_fma_f32 v188, v184, v221, v225
	v_cndmask_b32_e64 v180, 1.0, v180, s[36:37]
	v_fma_f32 v189, v185, v222, v226
	v_cndmask_b32_e64 v181, 1.0, v181, s[36:37]
	v_cndmask_b32_e64 v223, v223, v186, s[36:37]
	v_mul_f32_e32 v219, v219, v178
	v_cndmask_b32_e64 v224, v224, v187, s[36:37]
	v_mul_f32_e32 v220, v220, v179
	v_cndmask_b32_e64 v225, v225, v188, s[36:37]
	v_mul_f32_e32 v221, v221, v180
	v_cndmask_b32_e64 v226, v226, v189, s[36:37]
	v_mul_f32_e32 v222, v222, v181
	ds_bpermute_b32 v227, v204, v219
	ds_bpermute_b32 v231, v204, v223
	ds_bpermute_b32 v235, v206, v219
	ds_bpermute_b32 v239, v206, v223
	ds_bpermute_b32 v228, v204, v220
	ds_bpermute_b32 v232, v204, v224
	ds_bpermute_b32 v236, v206, v220
	ds_bpermute_b32 v244, v206, v224
	ds_bpermute_b32 v229, v204, v221
	ds_bpermute_b32 v233, v204, v225
	ds_bpermute_b32 v237, v206, v221
	ds_bpermute_b32 v245, v206, v225
	ds_bpermute_b32 v230, v204, v222
	ds_bpermute_b32 v234, v204, v226
	ds_bpermute_b32 v238, v206, v222
	ds_bpermute_b32 v246, v206, v226
	s_waitcnt lgkmcnt(0)
	v_cndmask_b32_e64 v227, 1.0, v227, s[34:35]
	v_cndmask_b32_e64 v231, 0, v231, s[34:35]
	v_cndmask_b32_e64 v228, 1.0, v228, s[34:35]
	v_cndmask_b32_e64 v232, 0, v232, s[34:35]
	v_cndmask_b32_e64 v229, 1.0, v229, s[34:35]
	v_cndmask_b32_e64 v233, 0, v233, s[34:35]
	v_cndmask_b32_e64 v230, 1.0, v230, s[34:35]
	v_cndmask_b32_e64 v234, 0, v234, s[34:35]
	v_mov_b32_e32 v190, v238
	v_mov_b32_e32 v194, v246
	v_mov_b32_e32 v198, v190
	v_mov_b32_e32 v201, v194
	v_fma_f32 v194, v194, v237, v245
	v_mul_f32_e32 v190, v190, v237
	v_mov_b32_e32 v199, v190
	v_mov_b32_e32 v177, v194
	v_fma_f32 v194, v194, v236, v244
	v_mul_f32_e32 v190, v190, v236
	v_mov_b32_e32 v200, v190
	v_mov_b32_e32 v203, v194
	v_fma_f32 v194, v194, v235, v239
	v_mul_f32_e32 v190, v190, v235
	v_mov_b32_e32 v191, v194
	ds_write_b64 v207, v[190:191] offset:1024
	s_waitcnt lgkmcnt(0)
	s_barrier
	ds_read_b64 v[178:179], v208 offset:1536
	ds_read_b64 v[180:181], v208 offset:1024
	s_waitcnt lgkmcnt(0)
	v_fma_f32 v182, v176, v178, v179
	v_cndmask_b32_e64 v183, v176, v182, s[38:39]
	v_fma_f32 v176, v182, v180, v181
	s_add_i32 s13, s13, 1
	s_mov_b32 s60, 8

.Lmylru_t1_7:
	s_barrier
	s_sub_i32 s54, 17, s13
	s_lshl_b32 s55, s54, 14
	s_lshl_b32 s56, s6, 11
	s_add_i32 s55, s55, s56
	s_add_u32 s44, s22, s55
	s_addc_u32 s45, s23, 0
	s_cmp_lt_u32 s13, 2
	s_sub_i32 s50, 1, s13
	s_lshl_b32 s50, s50, 7
	s_lshl_b32 s51, s9, 8
	s_add_i32 s51, s51, 0x8000
	s_add_i32 s51, s51, s50
	s_sub_i32 s50, 17, s13
	s_lshl_b32 s50, s50, 7
	s_lshl_b32 s57, s9, 11
	s_add_i32 s57, s57, s50
	s_cmp_lt_u32 s13, 2
	s_cselect_b32 s57, s51, s57
	s_lshl_b32 s57, s57, 11
	s_add_u32 s40, s18, s57
	s_addc_u32 s41, s19, 0
	s_add_u32 s42, s20, s57
	s_addc_u32 s43, s21, 0
	global_load_dword v247, v209, s[44:45]
	global_load_dword v248, v209, s[44:45] offset:256
	global_load_dword v249, v209, s[44:45] offset:512
	global_load_dword v250, v209, s[44:45] offset:768
	global_load_dword v251, v209, s[44:45] offset:1024
	global_load_dword v252, v209, s[44:45] offset:1280
	global_load_dword v253, v209, s[44:45] offset:1536
	global_load_dword v254, v209, s[44:45] offset:1792
	v_add_u32_e32 v182, 0x0, v210
	v_add_u32_e32 v183, 0x1000, v182
	global_load_ushort v128, v182, s[40:41]
	global_load_ushort v129, v182, s[40:41] offset:2048
	global_load_ushort v130, v183, s[40:41]
	global_load_ushort v131, v183, s[40:41] offset:2048
	v_add_u32_e32 v182, 0x8000, v210
	v_add_u32_e32 v183, 0x1000, v182
	global_load_ushort v132, v182, s[40:41]
	global_load_ushort v133, v182, s[40:41] offset:2048
	global_load_ushort v134, v183, s[40:41]
	global_load_ushort v135, v183, s[40:41] offset:2048
	v_add_u32_e32 v182, 0x10000, v210
	v_add_u32_e32 v183, 0x1000, v182
	global_load_ushort v136, v182, s[40:41]
	global_load_ushort v137, v182, s[40:41] offset:2048
	global_load_ushort v138, v183, s[40:41]
	global_load_ushort v139, v183, s[40:41] offset:2048
	v_add_u32_e32 v182, 0x18000, v210
	v_add_u32_e32 v183, 0x1000, v182
	global_load_ushort v140, v182, s[40:41]
	global_load_ushort v141, v182, s[40:41] offset:2048
	global_load_ushort v142, v183, s[40:41]
	global_load_ushort v143, v183, s[40:41] offset:2048
	s_cmp_eq_u32 s13, 17
	s_cbranch_scc1 .Lmylru_nodma_7
	s_add_i32 s58, s13, 1
	s_cmp_lt_u32 s58, 2
	s_sub_i32 s50, 1, s58
	s_lshl_b32 s50, s50, 7
	s_lshl_b32 s51, s9, 8
	s_add_i32 s51, s51, 0x8000
	s_add_i32 s51, s51, s50
	s_sub_i32 s50, 17, s58
	s_lshl_b32 s50, s50, 7
	s_lshl_b32 s59, s9, 11
	s_add_i32 s59, s59, s50
	s_cmp_lt_u32 s58, 2
	s_cselect_b32 s59, s51, s59
	s_lshl_b32 s52, s59, 11
	s_add_u32 s46, s16, s52
	s_addc_u32 s47, s17, 0
	s_lshl_b32 s52, s6, 13
	s_add_i32 s52, s52, 0x10000
	s_mov_b32 m0, s52
	s_add_i32 s52, s52, 0x400
	global_load_lds_dwordx4 v211, s[46:47]
	s_mov_b32 m0, s52
	s_add_i32 s52, s52, 0x400
	global_load_lds_dwordx4 v212, s[46:47]
	s_mov_b32 m0, s52
	s_add_i32 s52, s52, 0x400
	global_load_lds_dwordx4 v213, s[46:47]
	s_mov_b32 m0, s52
	s_add_i32 s52, s52, 0x400
	global_load_lds_dwordx4 v214, s[46:47]
	s_mov_b32 m0, s52
	s_add_i32 s52, s52, 0x400
	global_load_lds_dwordx4 v215, s[46:47]
	s_mov_b32 m0, s52
	s_add_i32 s52, s52, 0x400
	global_load_lds_dwordx4 v216, s[46:47]
	s_mov_b32 m0, s52
	s_add_i32 s52, s52, 0x400
	global_load_lds_dwordx4 v217, s[46:47]
	s_mov_b32 m0, s52
	s_nop 0
	global_load_lds_dwordx4 v218, s[46:47]
.Lmylru_nodma_7:
	v_mov_b32_e32 v163, v162
	ds_read_b128 v[96:99], v163
	ds_read_b128 v[100:103], v163 offset:8192
	ds_read_b128 v[104:107], v163 offset:16384
	ds_read_b128 v[108:111], v163 offset:24576
	v_xor_b32_e32 v164, 0x40, v163
	ds_read_b128 v[112:115], v164
	ds_read_b128 v[116:119], v164 offset:8192
	ds_read_b128 v[120:123], v164 offset:16384
	ds_read_b128 v[124:127], v164 offset:24576
	s_waitcnt lgkmcnt(7)
	v_mfma_f32_16x16x32_bf16 v[64:67], v[96:99], v[0:3], 0
	v_mfma_f32_16x16x32_bf16 v[68:71], v[96:99], v[32:35], 0
	v_xor_b32_e32 v164, 0x80, v163
	ds_read_b128 v[96:99], v164
	s_waitcnt lgkmcnt(7)
	v_mfma_f32_16x16x32_bf16 v[72:75], v[100:103], v[0:3], 0
	v_mfma_f32_16x16x32_bf16 v[76:79], v[100:103], v[32:35], 0
	ds_read_b128 v[100:103], v164 offset:8192
	s_waitcnt lgkmcnt(7)
	v_mfma_f32_16x16x32_bf16 v[80:83], v[104:107], v[0:3], 0
	v_mfma_f32_16x16x32_bf16 v[84:87], v[104:107], v[32:35], 0
	ds_read_b128 v[104:107], v164 offset:16384
	s_waitcnt lgkmcnt(7)
	v_mfma_f32_16x16x32_bf16 v[88:91], v[108:111], v[0:3], 0
	v_mfma_f32_16x16x32_bf16 v[92:95], v[108:111], v[32:35], 0
	ds_read_b128 v[108:111], v164 offset:24576
	s_waitcnt lgkmcnt(7)
	v_mfma_f32_16x16x32_bf16 v[64:67], v[112:115], v[4:7], v[64:67]
	v_mfma_f32_16x16x32_bf16 v[68:71], v[112:115], v[36:39], v[68:71]
	v_xor_b32_e32 v164, 0xc0, v163
	ds_read_b128 v[112:115], v164
	s_waitcnt lgkmcnt(7)
	v_mfma_f32_16x16x32_bf16 v[72:75], v[116:119], v[4:7], v[72:75]
	v_mfma_f32_16x16x32_bf16 v[76:79], v[116:119], v[36:39], v[76:79]
	ds_read_b128 v[116:119], v164 offset:8192
	s_waitcnt lgkmcnt(7)
	v_mfma_f32_16x16x32_bf16 v[80:83], v[120:123], v[4:7], v[80:83]
	v_mfma_f32_16x16x32_bf16 v[84:87], v[120:123], v[36:39], v[84:87]
	ds_read_b128 v[120:123], v164 offset:16384
	s_waitcnt lgkmcnt(7)
	v_mfma_f32_16x16x32_bf16 v[88:91], v[124:127], v[4:7], v[88:91]
	v_mfma_f32_16x16x32_bf16 v[92:95], v[124:127], v[36:39], v[92:95]
	ds_read_b128 v[124:127], v164 offset:24576
	s_waitcnt lgkmcnt(7)
	v_mfma_f32_16x16x32_bf16 v[64:67], v[96:99], v[8:11], v[64:67]
	v_mfma_f32_16x16x32_bf16 v[68:71], v[96:99], v[40:43], v[68:71]
	v_xor_b32_e32 v164, 0x100, v163
	ds_read_b128 v[96:99], v164
	s_waitcnt lgkmcnt(7)
	v_mfma_f32_16x16x32_bf16 v[72:75], v[100:103], v[8:11], v[72:75]
	v_mfma_f32_16x16x32_bf16 v[76:79], v[100:103], v[40:43], v[76:79]
	ds_read_b128 v[100:103], v164 offset:8192
	s_waitcnt lgkmcnt(7)
	v_mfma_f32_16x16x32_bf16 v[80:83], v[104:107], v[8:11], v[80:83]
	v_mfma_f32_16x16x32_bf16 v[84:87], v[104:107], v[40:43], v[84:87]
	ds_read_b128 v[104:107], v164 offset:16384
	s_waitcnt lgkmcnt(7)
	v_mfma_f32_16x16x32_bf16 v[88:91], v[108:111], v[8:11], v[88:91]
	v_mfma_f32_16x16x32_bf16 v[92:95], v[108:111], v[40:43], v[92:95]
	ds_read_b128 v[108:111], v164 offset:24576
	s_waitcnt lgkmcnt(7)
	v_mfma_f32_16x16x32_bf16 v[64:67], v[112:115], v[12:15], v[64:67]
	v_mfma_f32_16x16x32_bf16 v[68:71], v[112:115], v[44:47], v[68:71]
	v_xor_b32_e32 v164, 0x140, v163
	ds_read_b128 v[112:115], v164
	s_waitcnt lgkmcnt(7)
	v_mfma_f32_16x16x32_bf16 v[72:75], v[116:119], v[12:15], v[72:75]
	v_mfma_f32_16x16x32_bf16 v[76:79], v[116:119], v[44:47], v[76:79]
	ds_read_b128 v[116:119], v164 offset:8192
	s_waitcnt lgkmcnt(7)
	v_mfma_f32_16x16x32_bf16 v[80:83], v[120:123], v[12:15], v[80:83]
	v_mfma_f32_16x16x32_bf16 v[84:87], v[120:123], v[44:47], v[84:87]
	ds_read_b128 v[120:123], v164 offset:16384
	s_waitcnt lgkmcnt(7)
	v_mfma_f32_16x16x32_bf16 v[88:91], v[124:127], v[12:15], v[88:91]
	v_mfma_f32_16x16x32_bf16 v[92:95], v[124:127], v[44:47], v[92:95]
	ds_read_b128 v[124:127], v164 offset:24576
	s_waitcnt lgkmcnt(7)
	v_mfma_f32_16x16x32_bf16 v[64:67], v[96:99], v[16:19], v[64:67]
	v_mfma_f32_16x16x32_bf16 v[68:71], v[96:99], v[48:51], v[68:71]
	v_xor_b32_e32 v164, 0x180, v163
	ds_read_b128 v[96:99], v164
	s_waitcnt lgkmcnt(7)
	v_mfma_f32_16x16x32_bf16 v[72:75], v[100:103], v[16:19], v[72:75]
	v_mfma_f32_16x16x32_bf16 v[76:79], v[100:103], v[48:51], v[76:79]
	ds_read_b128 v[100:103], v164 offset:8192
	s_waitcnt lgkmcnt(7)
	v_mfma_f32_16x16x32_bf16 v[80:83], v[104:107], v[16:19], v[80:83]
	v_mfma_f32_16x16x32_bf16 v[84:87], v[104:107], v[48:51], v[84:87]
	ds_read_b128 v[104:107], v164 offset:16384
	s_waitcnt lgkmcnt(7)
	v_mfma_f32_16x16x32_bf16 v[88:91], v[108:111], v[16:19], v[88:91]
	v_mfma_f32_16x16x32_bf16 v[92:95], v[108:111], v[48:51], v[92:95]
	ds_read_b128 v[108:111], v164 offset:24576
	s_waitcnt lgkmcnt(7)
	v_mfma_f32_16x16x32_bf16 v[64:67], v[112:115], v[20:23], v[64:67]
	v_mfma_f32_16x16x32_bf16 v[68:71], v[112:115], v[52:55], v[68:71]
	v_xor_b32_e32 v164, 0x1c0, v163
	ds_read_b128 v[112:115], v164
	s_waitcnt lgkmcnt(7)
	v_mfma_f32_16x16x32_bf16 v[72:75], v[116:119], v[20:23], v[72:75]
	v_mfma_f32_16x16x32_bf16 v[76:79], v[116:119], v[52:55], v[76:79]
	ds_read_b128 v[116:119], v164 offset:8192
	s_waitcnt lgkmcnt(7)
	v_mfma_f32_16x16x32_bf16 v[80:83], v[120:123], v[20:23], v[80:83]
	v_mfma_f32_16x16x32_bf16 v[84:87], v[120:123], v[52:55], v[84:87]
	ds_read_b128 v[120:123], v164 offset:16384
	s_waitcnt lgkmcnt(7)
	v_mfma_f32_16x16x32_bf16 v[88:91], v[124:127], v[20:23], v[88:91]
	v_mfma_f32_16x16x32_bf16 v[92:95], v[124:127], v[52:55], v[92:95]
	ds_read_b128 v[124:127], v164 offset:24576
	s_waitcnt lgkmcnt(7)
	v_mfma_f32_16x16x32_bf16 v[64:67], v[96:99], v[24:27], v[64:67]
	v_mfma_f32_16x16x32_bf16 v[68:71], v[96:99], v[56:59], v[68:71]
	s_waitcnt lgkmcnt(6)
	v_mfma_f32_16x16x32_bf16 v[72:75], v[100:103], v[24:27], v[72:75]
	v_mfma_f32_16x16x32_bf16 v[76:79], v[100:103], v[56:59], v[76:79]
	s_waitcnt lgkmcnt(5)
	v_mfma_f32_16x16x32_bf16 v[80:83], v[104:107], v[24:27], v[80:83]
	v_mfma_f32_16x16x32_bf16 v[84:87], v[104:107], v[56:59], v[84:87]
	s_waitcnt lgkmcnt(4)
	v_mfma_f32_16x16x32_bf16 v[88:91], v[108:111], v[24:27], v[88:91]
	v_mfma_f32_16x16x32_bf16 v[92:95], v[108:111], v[56:59], v[92:95]
	s_waitcnt lgkmcnt(3)
	v_mfma_f32_16x16x32_bf16 v[64:67], v[112:115], v[28:31], v[64:67]
	v_mfma_f32_16x16x32_bf16 v[68:71], v[112:115], v[60:63], v[68:71]
	s_waitcnt lgkmcnt(2)
	v_mfma_f32_16x16x32_bf16 v[72:75], v[116:119], v[28:31], v[72:75]
	v_mfma_f32_16x16x32_bf16 v[76:79], v[116:119], v[60:63], v[76:79]
	s_waitcnt lgkmcnt(1)
	v_mfma_f32_16x16x32_bf16 v[80:83], v[120:123], v[28:31], v[80:83]
	v_mfma_f32_16x16x32_bf16 v[84:87], v[120:123], v[60:63], v[84:87]
	s_waitcnt lgkmcnt(0)
	v_mfma_f32_16x16x32_bf16 v[88:91], v[124:127], v[28:31], v[88:91]
	v_mfma_f32_16x16x32_bf16 v[92:95], v[124:127], v[60:63], v[92:95]
	v_mov_b32_e32 v169, v165
	v_mov_b32_e32 v170, v166
	v_mov_b32_e32 v171, v167
	v_mov_b32_e32 v172, v168
	ds_read_u16 v144, v169
	ds_read_u16 v145, v170
	ds_read_u16 v146, v171
	ds_read_u16 v147, v172
	ds_read_u16 v148, v169 offset:8192
	ds_read_u16 v149, v170 offset:8192
	ds_read_u16 v150, v171 offset:8192
	ds_read_u16 v151, v172 offset:8192
	ds_read_u16 v152, v169 offset:16384
	ds_read_u16 v153, v170 offset:16384
	ds_read_u16 v154, v171 offset:16384
	ds_read_u16 v155, v172 offset:16384
	ds_read_u16 v156, v169 offset:24576
	ds_read_u16 v157, v170 offset:24576
	ds_read_u16 v158, v171 offset:24576
	ds_read_u16 v159, v172 offset:24576
	s_nop 7
	v_fma_f32 v178, v64, s53, v173
	v_fma_f32 v179, v65, s53, v173
	v_fma_f32 v180, v66, s53, v173
	v_fma_f32 v181, v67, s53, v173
	v_fma_f32 v182, v72, s53, v173
	v_fma_f32 v183, v73, s53, v173
	v_fma_f32 v184, v74, s53, v173
	v_fma_f32 v185, v75, s53, v173
	v_fma_f32 v186, v68, s53, v174
	v_fma_f32 v187, v69, s53, v174
	v_fma_f32 v188, v70, s53, v174
	v_fma_f32 v189, v71, s53, v174
	v_fma_f32 v190, v76, s53, v174
	v_fma_f32 v191, v77, s53, v174
	v_fma_f32 v192, v78, s53, v174
	v_fma_f32 v193, v79, s53, v174
	v_exp_f32_e32 v178, v178
	v_exp_f32_e32 v179, v179
	v_exp_f32_e32 v180, v180
	v_exp_f32_e32 v181, v181
	v_exp_f32_e32 v182, v182
	v_exp_f32_e32 v183, v183
	v_exp_f32_e32 v184, v184
	v_exp_f32_e32 v185, v185
	v_exp_f32_e32 v186, v186
	v_exp_f32_e32 v187, v187
	v_exp_f32_e32 v188, v188
	v_exp_f32_e32 v189, v189
	v_exp_f32_e32 v190, v190
	v_exp_f32_e32 v191, v191
	v_exp_f32_e32 v192, v192
	v_exp_f32_e32 v193, v193
	v_add_f32_e32 v178, 1.0, v178
	v_add_f32_e32 v179, 1.0, v179
	v_add_f32_e32 v180, 1.0, v180
	v_add_f32_e32 v181, 1.0, v181
	v_add_f32_e32 v182, 1.0, v182
	v_add_f32_e32 v183, 1.0, v183
	v_add_f32_e32 v184, 1.0, v184
	v_add_f32_e32 v185, 1.0, v185
	v_add_f32_e32 v186, 1.0, v186
	v_add_f32_e32 v187, 1.0, v187
	v_add_f32_e32 v188, 1.0, v188
	v_add_f32_e32 v189, 1.0, v189
	v_add_f32_e32 v190, 1.0, v190
	v_add_f32_e32 v191, 1.0, v191
	v_add_f32_e32 v192, 1.0, v192
	v_add_f32_e32 v193, 1.0, v193
	v_rcp_f32_e32 v178, v178
	v_rcp_f32_e32 v179, v179
	v_rcp_f32_e32 v180, v180
	v_rcp_f32_e32 v181, v181
	v_rcp_f32_e32 v182, v182
	v_rcp_f32_e32 v183, v183
	v_rcp_f32_e32 v184, v184
	v_rcp_f32_e32 v185, v185
	v_rcp_f32_e32 v186, v186
	v_rcp_f32_e32 v187, v187
	v_rcp_f32_e32 v188, v188
	v_rcp_f32_e32 v189, v189
	v_rcp_f32_e32 v190, v190
	v_rcp_f32_e32 v191, v191
	v_rcp_f32_e32 v192, v192
	v_rcp_f32_e32 v193, v193
	v_mul_f32_e32 v178, v175, v178
	v_mul_f32_e32 v179, v175, v179
	v_mul_f32_e32 v180, v175, v180
	v_mul_f32_e32 v181, v175, v181
	v_mul_f32_e32 v182, v175, v182
	v_mul_f32_e32 v183, v175, v183
	v_mul_f32_e32 v184, v175, v184
	v_mul_f32_e32 v185, v175, v185
	v_exp_f32_e32 v96, v178
	v_exp_f32_e32 v97, v179
	v_exp_f32_e32 v98, v180
	v_exp_f32_e32 v99, v181
	v_exp_f32_e32 v100, v182
	v_exp_f32_e32 v101, v183
	v_exp_f32_e32 v102, v184
	v_exp_f32_e32 v103, v185
	s_nop 0
	v_fma_f32 v194, -v96, v96, 1.0
	v_fma_f32 v195, -v97, v97, 1.0
	v_fma_f32 v196, -v98, v98, 1.0
	v_fma_f32 v197, -v99, v99, 1.0
	v_fma_f32 v198, -v100, v100, 1.0
	v_fma_f32 v199, -v101, v101, 1.0
	v_fma_f32 v200, -v102, v102, 1.0
	v_fma_f32 v201, -v103, v103, 1.0
	v_max_f32_e32 v194, 0, v194
	v_max_f32_e32 v195, 0, v195
	v_max_f32_e32 v196, 0, v196
	v_max_f32_e32 v197, 0, v197
	v_max_f32_e32 v198, 0, v198
	v_max_f32_e32 v199, 0, v199
	v_max_f32_e32 v200, 0, v200
	v_max_f32_e32 v201, 0, v201
	v_sqrt_f32_e32 v194, v194
	v_sqrt_f32_e32 v195, v195
	v_sqrt_f32_e32 v196, v196
	v_sqrt_f32_e32 v197, v197
	v_sqrt_f32_e32 v198, v198
	v_sqrt_f32_e32 v199, v199
	v_sqrt_f32_e32 v200, v200
	v_sqrt_f32_e32 v201, v201
	s_waitcnt lgkmcnt(8)
	v_lshlrev_b32_e32 v144, 16, v144
	v_lshlrev_b32_e32 v145, 16, v145
	v_lshlrev_b32_e32 v146, 16, v146
	v_lshlrev_b32_e32 v147, 16, v147
	v_lshlrev_b32_e32 v148, 16, v148
	v_lshlrev_b32_e32 v149, 16, v149
	v_lshlrev_b32_e32 v150, 16, v150
	v_lshlrev_b32_e32 v151, 16, v151
	v_mul_f32_e32 v194, v194, v186
	v_mul_f32_e32 v195, v195, v187
	v_mul_f32_e32 v196, v196, v188
	v_mul_f32_e32 v197, v197, v189
	v_mul_f32_e32 v198, v198, v190
	v_mul_f32_e32 v199, v199, v191
	v_mul_f32_e32 v200, v200, v192
	v_mul_f32_e32 v201, v201, v193
	v_mul_f32_e32 v144, v194, v144
	v_mul_f32_e32 v145, v195, v145
	v_mul_f32_e32 v146, v196, v146
	v_mul_f32_e32 v147, v197, v147
	v_mul_f32_e32 v148, v198, v148
	v_mul_f32_e32 v149, v199, v149
	v_mul_f32_e32 v150, v200, v150
	v_mul_f32_e32 v151, v201, v151
	v_fma_f32 v178, v80, s53, v173
	v_fma_f32 v179, v81, s53, v173
	v_fma_f32 v180, v82, s53, v173
	v_fma_f32 v181, v83, s53, v173
	v_fma_f32 v182, v88, s53, v173
	v_fma_f32 v183, v89, s53, v173
	v_fma_f32 v184, v90, s53, v173
	v_fma_f32 v185, v91, s53, v173
	v_fma_f32 v186, v84, s53, v174
	v_fma_f32 v187, v85, s53, v174
	v_fma_f32 v188, v86, s53, v174
	v_fma_f32 v189, v87, s53, v174
	v_fma_f32 v190, v92, s53, v174
	v_fma_f32 v191, v93, s53, v174
	v_fma_f32 v192, v94, s53, v174
	v_fma_f32 v193, v95, s53, v174
	v_exp_f32_e32 v178, v178
	v_exp_f32_e32 v179, v179
	v_exp_f32_e32 v180, v180
	v_exp_f32_e32 v181, v181
	v_exp_f32_e32 v182, v182
	v_exp_f32_e32 v183, v183
	v_exp_f32_e32 v184, v184
	v_exp_f32_e32 v185, v185
	v_exp_f32_e32 v186, v186
	v_exp_f32_e32 v187, v187
	v_exp_f32_e32 v188, v188
	v_exp_f32_e32 v189, v189
	v_exp_f32_e32 v190, v190
	v_exp_f32_e32 v191, v191
	v_exp_f32_e32 v192, v192
	v_exp_f32_e32 v193, v193
	v_add_f32_e32 v178, 1.0, v178
	v_add_f32_e32 v179, 1.0, v179
	v_add_f32_e32 v180, 1.0, v180
	v_add_f32_e32 v181, 1.0, v181
	v_add_f32_e32 v182, 1.0, v182
	v_add_f32_e32 v183, 1.0, v183
	v_add_f32_e32 v184, 1.0, v184
	v_add_f32_e32 v185, 1.0, v185
	v_add_f32_e32 v186, 1.0, v186
	v_add_f32_e32 v187, 1.0, v187
	v_add_f32_e32 v188, 1.0, v188
	v_add_f32_e32 v189, 1.0, v189
	v_add_f32_e32 v190, 1.0, v190
	v_add_f32_e32 v191, 1.0, v191
	v_add_f32_e32 v192, 1.0, v192
	v_add_f32_e32 v193, 1.0, v193
	v_rcp_f32_e32 v178, v178
	v_rcp_f32_e32 v179, v179
	v_rcp_f32_e32 v180, v180
	v_rcp_f32_e32 v181, v181
	v_rcp_f32_e32 v182, v182
	v_rcp_f32_e32 v183, v183
	v_rcp_f32_e32 v184, v184
	v_rcp_f32_e32 v185, v185
	v_rcp_f32_e32 v186, v186
	v_rcp_f32_e32 v187, v187
	v_rcp_f32_e32 v188, v188
	v_rcp_f32_e32 v189, v189
	v_rcp_f32_e32 v190, v190
	v_rcp_f32_e32 v191, v191
	v_rcp_f32_e32 v192, v192
	v_rcp_f32_e32 v193, v193
	v_mul_f32_e32 v178, v175, v178
	v_mul_f32_e32 v179, v175, v179
	v_mul_f32_e32 v180, v175, v180
	v_mul_f32_e32 v181, v175, v181
	v_mul_f32_e32 v182, v175, v182
	v_mul_f32_e32 v183, v175, v183
	v_mul_f32_e32 v184, v175, v184
	v_mul_f32_e32 v185, v175, v185
	v_exp_f32_e32 v104, v178
	v_exp_f32_e32 v105, v179
	v_exp_f32_e32 v106, v180
	v_exp_f32_e32 v107, v181
	v_exp_f32_e32 v108, v182
	v_exp_f32_e32 v109, v183
	v_exp_f32_e32 v110, v184
	v_exp_f32_e32 v111, v185
	s_nop 0
	v_fma_f32 v194, -v104, v104, 1.0
	v_fma_f32 v195, -v105, v105, 1.0
	v_fma_f32 v196, -v106, v106, 1.0
	v_fma_f32 v197, -v107, v107, 1.0
	v_fma_f32 v198, -v108, v108, 1.0
	v_fma_f32 v199, -v109, v109, 1.0
	v_fma_f32 v200, -v110, v110, 1.0
	v_fma_f32 v201, -v111, v111, 1.0
	v_max_f32_e32 v194, 0, v194
	v_max_f32_e32 v195, 0, v195
	v_max_f32_e32 v196, 0, v196
	v_max_f32_e32 v197, 0, v197
	v_max_f32_e32 v198, 0, v198
	v_max_f32_e32 v199, 0, v199
	v_max_f32_e32 v200, 0, v200
	v_max_f32_e32 v201, 0, v201
	v_sqrt_f32_e32 v194, v194
	v_sqrt_f32_e32 v195, v195
	v_sqrt_f32_e32 v196, v196
	v_sqrt_f32_e32 v197, v197
	v_sqrt_f32_e32 v198, v198
	v_sqrt_f32_e32 v199, v199
	v_sqrt_f32_e32 v200, v200
	v_sqrt_f32_e32 v201, v201
	s_waitcnt lgkmcnt(0)
	v_lshlrev_b32_e32 v152, 16, v152
	v_lshlrev_b32_e32 v153, 16, v153
	v_lshlrev_b32_e32 v154, 16, v154
	v_lshlrev_b32_e32 v155, 16, v155
	v_lshlrev_b32_e32 v156, 16, v156
	v_lshlrev_b32_e32 v157, 16, v157
	v_lshlrev_b32_e32 v158, 16, v158
	v_lshlrev_b32_e32 v159, 16, v159
	v_mul_f32_e32 v194, v194, v186
	v_mul_f32_e32 v195, v195, v187
	v_mul_f32_e32 v196, v196, v188
	v_mul_f32_e32 v197, v197, v189
	v_mul_f32_e32 v198, v198, v190
	v_mul_f32_e32 v199, v199, v191
	v_mul_f32_e32 v200, v200, v192
	v_mul_f32_e32 v201, v201, v193
	v_mul_f32_e32 v152, v194, v152
	v_mul_f32_e32 v153, v195, v153
	v_mul_f32_e32 v154, v196, v154
	v_mul_f32_e32 v155, v197, v155
	v_mul_f32_e32 v156, v198, v156
	v_mul_f32_e32 v157, v199, v157
	v_mul_f32_e32 v158, v200, v158
	v_mul_f32_e32 v159, v201, v159
	v_fma_f32 v146, v98, v147, v146
	v_fma_f32 v150, v102, v151, v150
	v_fma_f32 v154, v106, v155, v154
	v_fma_f32 v158, v110, v159, v158
	v_mul_f32_e32 v98, v98, v99
	v_mul_f32_e32 v102, v102, v103
	v_mul_f32_e32 v106, v106, v107
	v_mul_f32_e32 v110, v110, v111
	v_fma_f32 v145, v97, v146, v145
	v_fma_f32 v149, v101, v150, v149
	v_fma_f32 v153, v105, v154, v153
	v_fma_f32 v157, v109, v158, v157
	v_mul_f32_e32 v97, v97, v98
	v_mul_f32_e32 v101, v101, v102
	v_mul_f32_e32 v105, v105, v106
	v_mul_f32_e32 v109, v109, v110
	v_fma_f32 v144, v96, v145, v144
	v_fma_f32 v148, v100, v149, v148
	v_fma_f32 v152, v104, v153, v152
	v_fma_f32 v156, v108, v157, v156
	v_mul_f32_e32 v96, v96, v97
	v_mul_f32_e32 v100, v100, v101
	v_mul_f32_e32 v104, v104, v105
	v_mul_f32_e32 v108, v108, v109
	ds_bpermute_b32 v178, v204, v96
	ds_bpermute_b32 v182, v204, v144
	ds_bpermute_b32 v179, v204, v100
	ds_bpermute_b32 v183, v204, v148
	ds_bpermute_b32 v180, v204, v104
	ds_bpermute_b32 v184, v204, v152
	ds_bpermute_b32 v181, v204, v108
	ds_bpermute_b32 v185, v204, v156
	s_waitcnt lgkmcnt(0)
	v_fma_f32 v186, v182, v96, v144
	v_cndmask_b32_e64 v178, 1.0, v178, s[34:35]
	v_fma_f32 v187, v183, v100, v148
	v_cndmask_b32_e64 v179, 1.0, v179, s[34:35]
	v_fma_f32 v188, v184, v104, v152
	v_cndmask_b32_e64 v180, 1.0, v180, s[34:35]
	v_fma_f32 v189, v185, v108, v156
	v_cndmask_b32_e64 v181, 1.0, v181, s[34:35]
	v_cndmask_b32_e64 v223, v144, v186, s[34:35]
	v_mul_f32_e32 v219, v96, v178
	v_cndmask_b32_e64 v224, v148, v187, s[34:35]
	v_mul_f32_e32 v220, v100, v179
	v_cndmask_b32_e64 v225, v152, v188, s[34:35]
	v_mul_f32_e32 v221, v104, v180
	v_cndmask_b32_e64 v226, v156, v189, s[34:35]
	v_mul_f32_e32 v222, v108, v181
	ds_bpermute_b32 v178, v205, v219
	ds_bpermute_b32 v182, v205, v223
	ds_bpermute_b32 v179, v205, v220
	ds_bpermute_b32 v183, v205, v224
	ds_bpermute_b32 v180, v205, v221
	ds_bpermute_b32 v184, v205, v225
	ds_bpermute_b32 v181, v205, v222
	ds_bpermute_b32 v185, v205, v226
	s_waitcnt lgkmcnt(0)
	v_fma_f32 v186, v182, v219, v223
	v_cndmask_b32_e64 v178, 1.0, v178, s[36:37]
	v_fma_f32 v187, v183, v220, v224
	v_cndmask_b32_e64 v179, 1.0, v179, s[36:37]
	v_fma_f32 v188, v184, v221, v225
	v_cndmask_b32_e64 v180, 1.0, v180, s[36:37]
	v_fma_f32 v189, v185, v222, v226
	v_cndmask_b32_e64 v181, 1.0, v181, s[36:37]
	v_cndmask_b32_e64 v223, v223, v186, s[36:37]
	v_mul_f32_e32 v219, v219, v178
	v_cndmask_b32_e64 v224, v224, v187, s[36:37]
	v_mul_f32_e32 v220, v220, v179
	v_cndmask_b32_e64 v225, v225, v188, s[36:37]
	v_mul_f32_e32 v221, v221, v180
	v_cndmask_b32_e64 v226, v226, v189, s[36:37]
	v_mul_f32_e32 v222, v222, v181
	ds_bpermute_b32 v227, v204, v219
	ds_bpermute_b32 v231, v204, v223
	ds_bpermute_b32 v235, v206, v219
	ds_bpermute_b32 v239, v206, v223
	ds_bpermute_b32 v228, v204, v220
	ds_bpermute_b32 v232, v204, v224
	ds_bpermute_b32 v236, v206, v220
	ds_bpermute_b32 v244, v206, v224
	ds_bpermute_b32 v229, v204, v221
	ds_bpermute_b32 v233, v204, v225
	ds_bpermute_b32 v237, v206, v221
	ds_bpermute_b32 v245, v206, v225
	ds_bpermute_b32 v230, v204, v222
	ds_bpermute_b32 v234, v204, v226
	ds_bpermute_b32 v238, v206, v222
	ds_bpermute_b32 v246, v206, v226
	s_waitcnt lgkmcnt(0)
	v_cndmask_b32_e64 v227, 1.0, v227, s[34:35]
	v_cndmask_b32_e64 v231, 0, v231, s[34:35]
	v_cndmask_b32_e64 v228, 1.0, v228, s[34:35]
	v_cndmask_b32_e64 v232, 0, v232, s[34:35]
	v_cndmask_b32_e64 v229, 1.0, v229, s[34:35]
	v_cndmask_b32_e64 v233, 0, v233, s[34:35]
	v_cndmask_b32_e64 v230, 1.0, v230, s[34:35]
	v_cndmask_b32_e64 v234, 0, v234, s[34:35]
	v_mov_b32_e32 v190, v238
	v_mov_b32_e32 v194, v246
	v_mov_b32_e32 v198, v190
	v_mov_b32_e32 v201, v194
	v_fma_f32 v194, v194, v237, v245
	v_mul_f32_e32 v190, v190, v237
	v_mov_b32_e32 v199, v190
	v_mov_b32_e32 v177, v194
	v_fma_f32 v194, v194, v236, v244
	v_mul_f32_e32 v190, v190, v236
	v_mov_b32_e32 v200, v190
	v_mov_b32_e32 v203, v194
	v_fma_f32 v194, v194, v235, v239
	v_mul_f32_e32 v190, v190, v235
	v_mov_b32_e32 v191, v194
	ds_write_b64 v207, v[190:191]
	s_waitcnt lgkmcnt(0)
	s_barrier
	ds_read_b64 v[178:179], v208 offset:512
	ds_read_b64 v[180:181], v208
	s_waitcnt lgkmcnt(0)
	v_fma_f32 v182, v176, v178, v179
	v_cndmask_b32_e64 v183, v176, v182, s[38:39]
	v_fma_f32 v176, v182, v180, v181
	v_fma_f32 v184, v183, v200, v203
	v_fma_f32 v185, v183, v199, v177
	v_fma_f32 v186, v183, v198, v201
	v_mov_b32_e32 v187, v183
	v_fma_f32 v184, v184, v227, v231
	v_fma_f32 v185, v185, v228, v232
	v_fma_f32 v186, v186, v229, v233
	v_fma_f32 v187, v187, v230, v234
	v_fma_f32 v144, v184, v96, v144
	v_fma_f32 v148, v185, v100, v148
	v_fma_f32 v152, v186, v104, v152
	v_fma_f32 v156, v187, v108, v156
	v_fma_f32 v145, v184, v97, v145
	v_fma_f32 v149, v185, v101, v149
	v_fma_f32 v153, v186, v105, v153
	v_fma_f32 v157, v187, v109, v157
	v_fma_f32 v146, v184, v98, v146
	v_fma_f32 v150, v185, v102, v150
	v_fma_f32 v154, v186, v106, v154
	v_fma_f32 v158, v187, v110, v158
	v_fma_f32 v147, v184, v99, v147
	v_fma_f32 v151, v185, v103, v151
	v_fma_f32 v155, v186, v107, v155
	v_fma_f32 v159, v187, v111, v159
	s_cmp_eq_u32 s13, 17
	s_cbranch_scc1 .Lmylru_w0_7
	s_waitcnt vmcnt(8)
	s_branch .Lmylru_w1_7

.Lmylru_w1_7:
	v_lshlrev_b32_e32 v178, 16, v247
	v_add_f32_e32 v144, v144, v178
	v_lshlrev_b32_e32 v128, 16, v128
	v_mul_f32_e32 v144, v144, v128
	v_cvt_pk_bf16_f32 v144, v144, v144
	v_and_b32_e32 v179, 0xffff0000, v247
	v_add_f32_e32 v145, v145, v179
	v_lshlrev_b32_e32 v129, 16, v129
	v_mul_f32_e32 v145, v145, v129
	v_cvt_pk_bf16_f32 v145, v145, v145
	v_lshlrev_b32_e32 v180, 16, v248
	v_add_f32_e32 v146, v146, v180
	v_lshlrev_b32_e32 v130, 16, v130
	v_mul_f32_e32 v146, v146, v130
	v_cvt_pk_bf16_f32 v146, v146, v146
	v_and_b32_e32 v181, 0xffff0000, v248
	v_add_f32_e32 v147, v147, v181
	v_lshlrev_b32_e32 v131, 16, v131
	v_mul_f32_e32 v147, v147, v131
	v_cvt_pk_bf16_f32 v147, v147, v147
	v_lshlrev_b32_e32 v178, 16, v249
	v_add_f32_e32 v148, v148, v178
	v_lshlrev_b32_e32 v132, 16, v132
	v_mul_f32_e32 v148, v148, v132
	v_cvt_pk_bf16_f32 v148, v148, v148
	v_and_b32_e32 v179, 0xffff0000, v249
	v_add_f32_e32 v149, v149, v179
	v_lshlrev_b32_e32 v133, 16, v133
	v_mul_f32_e32 v149, v149, v133
	v_cvt_pk_bf16_f32 v149, v149, v149
	v_lshlrev_b32_e32 v180, 16, v250
	v_add_f32_e32 v150, v150, v180
	v_lshlrev_b32_e32 v134, 16, v134
	v_mul_f32_e32 v150, v150, v134
	v_cvt_pk_bf16_f32 v150, v150, v150
	v_and_b32_e32 v181, 0xffff0000, v250
	v_add_f32_e32 v151, v151, v181
	v_lshlrev_b32_e32 v135, 16, v135
	v_mul_f32_e32 v151, v151, v135
	v_cvt_pk_bf16_f32 v151, v151, v151
	v_lshlrev_b32_e32 v178, 16, v251
	v_add_f32_e32 v152, v152, v178
	v_lshlrev_b32_e32 v136, 16, v136
	v_mul_f32_e32 v152, v152, v136
	v_cvt_pk_bf16_f32 v152, v152, v152
	v_and_b32_e32 v179, 0xffff0000, v251
	v_add_f32_e32 v153, v153, v179
	v_lshlrev_b32_e32 v137, 16, v137
	v_mul_f32_e32 v153, v153, v137
	v_cvt_pk_bf16_f32 v153, v153, v153
	v_lshlrev_b32_e32 v180, 16, v252
	v_add_f32_e32 v154, v154, v180
	v_lshlrev_b32_e32 v138, 16, v138
	v_mul_f32_e32 v154, v154, v138
	v_cvt_pk_bf16_f32 v154, v154, v154
	v_and_b32_e32 v181, 0xffff0000, v252
	v_add_f32_e32 v155, v155, v181
	v_lshlrev_b32_e32 v139, 16, v139
	v_mul_f32_e32 v155, v155, v139
	v_cvt_pk_bf16_f32 v155, v155, v155
	v_lshlrev_b32_e32 v178, 16, v253
	v_add_f32_e32 v156, v156, v178
	v_lshlrev_b32_e32 v140, 16, v140
	v_mul_f32_e32 v156, v156, v140
	v_cvt_pk_bf16_f32 v156, v156, v156
	v_and_b32_e32 v179, 0xffff0000, v253
	v_add_f32_e32 v157, v157, v179
	v_lshlrev_b32_e32 v141, 16, v141
	v_mul_f32_e32 v157, v157, v141
	v_cvt_pk_bf16_f32 v157, v157, v157
	v_lshlrev_b32_e32 v180, 16, v254
	v_add_f32_e32 v158, v158, v180
	v_lshlrev_b32_e32 v142, 16, v142
	v_mul_f32_e32 v158, v158, v142
	v_cvt_pk_bf16_f32 v158, v158, v158
	v_and_b32_e32 v181, 0xffff0000, v254
	v_add_f32_e32 v159, v159, v181
	v_lshlrev_b32_e32 v143, 16, v143
	v_mul_f32_e32 v159, v159, v143
	v_cvt_pk_bf16_f32 v159, v159, v159
	v_add_u32_e32 v182, 0x0, v210
	v_add_u32_e32 v183, 0x1000, v182
	global_store_short v182, v144, s[42:43]
	global_store_short v182, v145, s[42:43] offset:2048
	global_store_short v183, v146, s[42:43]
	global_store_short v183, v147, s[42:43] offset:2048
	v_add_u32_e32 v182, 0x8000, v210
	v_add_u32_e32 v183, 0x1000, v182
	global_store_short v182, v148, s[42:43]
	global_store_short v182, v149, s[42:43] offset:2048
	global_store_short v183, v150, s[42:43]
	global_store_short v183, v151, s[42:43] offset:2048
	v_add_u32_e32 v182, 0x10000, v210
	v_add_u32_e32 v183, 0x1000, v182
	global_store_short v182, v152, s[42:43]
	global_store_short v182, v153, s[42:43] offset:2048
	global_store_short v183, v154, s[42:43]
	global_store_short v183, v155, s[42:43] offset:2048
	v_add_u32_e32 v182, 0x18000, v210
	v_add_u32_e32 v183, 0x1000, v182
	global_store_short v182, v156, s[42:43]
	global_store_short v182, v157, s[42:43] offset:2048
	global_store_short v183, v158, s[42:43]
	global_store_short v183, v159, s[42:43] offset:2048
	s_add_i32 s13, s13, 1
	s_cmp_eq_u32 s13, 2
	s_cbranch_scc1 .Lmylru_t0_8
	s_waitcnt vmcnt(16)
	s_branch .Lmylru_t1_8

.Lmylru_t1_8:
	s_barrier
	s_sub_i32 s54, 17, s13
	s_lshl_b32 s55, s54, 14
	s_lshl_b32 s56, s6, 11
	s_add_i32 s55, s55, s56
	s_add_u32 s44, s22, s55
	s_addc_u32 s45, s23, 0
	s_cmp_lt_u32 s13, 2
	s_sub_i32 s50, 1, s13
	s_lshl_b32 s50, s50, 7
	s_lshl_b32 s51, s9, 8
	s_add_i32 s51, s51, 0x8000
	s_add_i32 s51, s51, s50
	s_sub_i32 s50, 17, s13
	s_lshl_b32 s50, s50, 7
	s_lshl_b32 s57, s9, 11
	s_add_i32 s57, s57, s50
	s_cmp_lt_u32 s13, 2
	s_cselect_b32 s57, s51, s57
	s_lshl_b32 s57, s57, 11
	s_add_u32 s40, s18, s57
	s_addc_u32 s41, s19, 0
	s_add_u32 s42, s20, s57
	s_addc_u32 s43, s21, 0
	global_load_dword v247, v209, s[44:45]
	global_load_dword v248, v209, s[44:45] offset:256
	global_load_dword v249, v209, s[44:45] offset:512
	global_load_dword v250, v209, s[44:45] offset:768
	global_load_dword v251, v209, s[44:45] offset:1024
	global_load_dword v252, v209, s[44:45] offset:1280
	global_load_dword v253, v209, s[44:45] offset:1536
	global_load_dword v254, v209, s[44:45] offset:1792
	v_add_u32_e32 v182, 0x0, v210
	v_add_u32_e32 v183, 0x1000, v182
	global_load_ushort v128, v182, s[40:41]
	global_load_ushort v129, v182, s[40:41] offset:2048
	global_load_ushort v130, v183, s[40:41]
	global_load_ushort v131, v183, s[40:41] offset:2048
	v_add_u32_e32 v182, 0x8000, v210
	v_add_u32_e32 v183, 0x1000, v182
	global_load_ushort v132, v182, s[40:41]
	global_load_ushort v133, v182, s[40:41] offset:2048
	global_load_ushort v134, v183, s[40:41]
	global_load_ushort v135, v183, s[40:41] offset:2048
	v_add_u32_e32 v182, 0x10000, v210
	v_add_u32_e32 v183, 0x1000, v182
	global_load_ushort v136, v182, s[40:41]
	global_load_ushort v137, v182, s[40:41] offset:2048
	global_load_ushort v138, v183, s[40:41]
	global_load_ushort v139, v183, s[40:41] offset:2048
	v_add_u32_e32 v182, 0x18000, v210
	v_add_u32_e32 v183, 0x1000, v182
	global_load_ushort v140, v182, s[40:41]
	global_load_ushort v141, v182, s[40:41] offset:2048
	global_load_ushort v142, v183, s[40:41]
	global_load_ushort v143, v183, s[40:41] offset:2048
	s_cmp_eq_u32 s13, 17
	s_cbranch_scc1 .Lmylru_nodma_8
	s_add_i32 s58, s13, 1
	s_cmp_lt_u32 s58, 2
	s_sub_i32 s50, 1, s58
	s_lshl_b32 s50, s50, 7
	s_lshl_b32 s51, s9, 8
	s_add_i32 s51, s51, 0x8000
	s_add_i32 s51, s51, s50
	s_sub_i32 s50, 17, s58
	s_lshl_b32 s50, s50, 7
	s_lshl_b32 s59, s9, 11
	s_add_i32 s59, s59, s50
	s_cmp_lt_u32 s58, 2
	s_cselect_b32 s59, s51, s59
	s_lshl_b32 s52, s59, 11
	s_add_u32 s46, s16, s52
	s_addc_u32 s47, s17, 0
	s_lshl_b32 s52, s6, 13
	s_mov_b32 m0, s52
	s_add_i32 s52, s52, 0x400
	global_load_lds_dwordx4 v211, s[46:47]
	s_mov_b32 m0, s52
	s_add_i32 s52, s52, 0x400
	global_load_lds_dwordx4 v212, s[46:47]
	s_mov_b32 m0, s52
	s_add_i32 s52, s52, 0x400
	global_load_lds_dwordx4 v213, s[46:47]
	s_mov_b32 m0, s52
	s_add_i32 s52, s52, 0x400
	global_load_lds_dwordx4 v214, s[46:47]
	s_mov_b32 m0, s52
	s_add_i32 s52, s52, 0x400
	global_load_lds_dwordx4 v215, s[46:47]
	s_mov_b32 m0, s52
	s_add_i32 s52, s52, 0x400
	global_load_lds_dwordx4 v216, s[46:47]
	s_mov_b32 m0, s52
	s_add_i32 s52, s52, 0x400
	global_load_lds_dwordx4 v217, s[46:47]
	s_mov_b32 m0, s52
	s_nop 0
	global_load_lds_dwordx4 v218, s[46:47]
.Lmylru_nodma_8:
	v_or_b32_e32 v163, 0x10000, v162
	ds_read_b128 v[96:99], v163
	ds_read_b128 v[100:103], v163 offset:8192
	ds_read_b128 v[104:107], v163 offset:16384
	ds_read_b128 v[108:111], v163 offset:24576
	v_xor_b32_e32 v164, 0x40, v163
	ds_read_b128 v[112:115], v164
	ds_read_b128 v[116:119], v164 offset:8192
	ds_read_b128 v[120:123], v164 offset:16384
	ds_read_b128 v[124:127], v164 offset:24576
	s_waitcnt lgkmcnt(7)
	v_mfma_f32_16x16x32_bf16 v[64:67], v[96:99], v[0:3], 0
	v_mfma_f32_16x16x32_bf16 v[68:71], v[96:99], v[32:35], 0
	v_xor_b32_e32 v164, 0x80, v163
	ds_read_b128 v[96:99], v164
	s_waitcnt lgkmcnt(7)
	v_mfma_f32_16x16x32_bf16 v[72:75], v[100:103], v[0:3], 0
	v_mfma_f32_16x16x32_bf16 v[76:79], v[100:103], v[32:35], 0
	ds_read_b128 v[100:103], v164 offset:8192
	s_waitcnt lgkmcnt(7)
	v_mfma_f32_16x16x32_bf16 v[80:83], v[104:107], v[0:3], 0
	v_mfma_f32_16x16x32_bf16 v[84:87], v[104:107], v[32:35], 0
	ds_read_b128 v[104:107], v164 offset:16384
	s_waitcnt lgkmcnt(7)
	v_mfma_f32_16x16x32_bf16 v[88:91], v[108:111], v[0:3], 0
	v_mfma_f32_16x16x32_bf16 v[92:95], v[108:111], v[32:35], 0
	ds_read_b128 v[108:111], v164 offset:24576
	s_waitcnt lgkmcnt(7)
	v_mfma_f32_16x16x32_bf16 v[64:67], v[112:115], v[4:7], v[64:67]
	v_mfma_f32_16x16x32_bf16 v[68:71], v[112:115], v[36:39], v[68:71]
	v_xor_b32_e32 v164, 0xc0, v163
	ds_read_b128 v[112:115], v164
	s_waitcnt lgkmcnt(7)
	v_mfma_f32_16x16x32_bf16 v[72:75], v[116:119], v[4:7], v[72:75]
	v_mfma_f32_16x16x32_bf16 v[76:79], v[116:119], v[36:39], v[76:79]
	ds_read_b128 v[116:119], v164 offset:8192
	s_waitcnt lgkmcnt(7)
	v_mfma_f32_16x16x32_bf16 v[80:83], v[120:123], v[4:7], v[80:83]
	v_mfma_f32_16x16x32_bf16 v[84:87], v[120:123], v[36:39], v[84:87]
	ds_read_b128 v[120:123], v164 offset:16384
	s_waitcnt lgkmcnt(7)
	v_mfma_f32_16x16x32_bf16 v[88:91], v[124:127], v[4:7], v[88:91]
	v_mfma_f32_16x16x32_bf16 v[92:95], v[124:127], v[36:39], v[92:95]
	ds_read_b128 v[124:127], v164 offset:24576
	s_waitcnt lgkmcnt(7)
	v_mfma_f32_16x16x32_bf16 v[64:67], v[96:99], v[8:11], v[64:67]
	v_mfma_f32_16x16x32_bf16 v[68:71], v[96:99], v[40:43], v[68:71]
	v_xor_b32_e32 v164, 0x100, v163
	ds_read_b128 v[96:99], v164
	s_waitcnt lgkmcnt(7)
	v_mfma_f32_16x16x32_bf16 v[72:75], v[100:103], v[8:11], v[72:75]
	v_mfma_f32_16x16x32_bf16 v[76:79], v[100:103], v[40:43], v[76:79]
	ds_read_b128 v[100:103], v164 offset:8192
	s_waitcnt lgkmcnt(7)
	v_mfma_f32_16x16x32_bf16 v[80:83], v[104:107], v[8:11], v[80:83]
	v_mfma_f32_16x16x32_bf16 v[84:87], v[104:107], v[40:43], v[84:87]
	ds_read_b128 v[104:107], v164 offset:16384
	s_waitcnt lgkmcnt(7)
	v_mfma_f32_16x16x32_bf16 v[88:91], v[108:111], v[8:11], v[88:91]
	v_mfma_f32_16x16x32_bf16 v[92:95], v[108:111], v[40:43], v[92:95]
	ds_read_b128 v[108:111], v164 offset:24576
	s_waitcnt lgkmcnt(7)
	v_mfma_f32_16x16x32_bf16 v[64:67], v[112:115], v[12:15], v[64:67]
	v_mfma_f32_16x16x32_bf16 v[68:71], v[112:115], v[44:47], v[68:71]
	v_xor_b32_e32 v164, 0x140, v163
	ds_read_b128 v[112:115], v164
	s_waitcnt lgkmcnt(7)
	v_mfma_f32_16x16x32_bf16 v[72:75], v[116:119], v[12:15], v[72:75]
	v_mfma_f32_16x16x32_bf16 v[76:79], v[116:119], v[44:47], v[76:79]
	ds_read_b128 v[116:119], v164 offset:8192
	s_waitcnt lgkmcnt(7)
	v_mfma_f32_16x16x32_bf16 v[80:83], v[120:123], v[12:15], v[80:83]
	v_mfma_f32_16x16x32_bf16 v[84:87], v[120:123], v[44:47], v[84:87]
	ds_read_b128 v[120:123], v164 offset:16384
	s_waitcnt lgkmcnt(7)
	v_mfma_f32_16x16x32_bf16 v[88:91], v[124:127], v[12:15], v[88:91]
	v_mfma_f32_16x16x32_bf16 v[92:95], v[124:127], v[44:47], v[92:95]
	ds_read_b128 v[124:127], v164 offset:24576
	s_waitcnt lgkmcnt(7)
	v_mfma_f32_16x16x32_bf16 v[64:67], v[96:99], v[16:19], v[64:67]
	v_mfma_f32_16x16x32_bf16 v[68:71], v[96:99], v[48:51], v[68:71]
	v_xor_b32_e32 v164, 0x180, v163
	ds_read_b128 v[96:99], v164
	s_waitcnt lgkmcnt(7)
	v_mfma_f32_16x16x32_bf16 v[72:75], v[100:103], v[16:19], v[72:75]
	v_mfma_f32_16x16x32_bf16 v[76:79], v[100:103], v[48:51], v[76:79]
	ds_read_b128 v[100:103], v164 offset:8192
	s_waitcnt lgkmcnt(7)
	v_mfma_f32_16x16x32_bf16 v[80:83], v[104:107], v[16:19], v[80:83]
	v_mfma_f32_16x16x32_bf16 v[84:87], v[104:107], v[48:51], v[84:87]
	ds_read_b128 v[104:107], v164 offset:16384
	s_waitcnt lgkmcnt(7)
	v_mfma_f32_16x16x32_bf16 v[88:91], v[108:111], v[16:19], v[88:91]
	v_mfma_f32_16x16x32_bf16 v[92:95], v[108:111], v[48:51], v[92:95]
	ds_read_b128 v[108:111], v164 offset:24576
	s_waitcnt lgkmcnt(7)
	v_mfma_f32_16x16x32_bf16 v[64:67], v[112:115], v[20:23], v[64:67]
	v_mfma_f32_16x16x32_bf16 v[68:71], v[112:115], v[52:55], v[68:71]
	v_xor_b32_e32 v164, 0x1c0, v163
	ds_read_b128 v[112:115], v164
	s_waitcnt lgkmcnt(7)
	v_mfma_f32_16x16x32_bf16 v[72:75], v[116:119], v[20:23], v[72:75]
	v_mfma_f32_16x16x32_bf16 v[76:79], v[116:119], v[52:55], v[76:79]
	ds_read_b128 v[116:119], v164 offset:8192
	s_waitcnt lgkmcnt(7)
	v_mfma_f32_16x16x32_bf16 v[80:83], v[120:123], v[20:23], v[80:83]
	v_mfma_f32_16x16x32_bf16 v[84:87], v[120:123], v[52:55], v[84:87]
	ds_read_b128 v[120:123], v164 offset:16384
	s_waitcnt lgkmcnt(7)
	v_mfma_f32_16x16x32_bf16 v[88:91], v[124:127], v[20:23], v[88:91]
	v_mfma_f32_16x16x32_bf16 v[92:95], v[124:127], v[52:55], v[92:95]
	ds_read_b128 v[124:127], v164 offset:24576
	s_waitcnt lgkmcnt(7)
	v_mfma_f32_16x16x32_bf16 v[64:67], v[96:99], v[24:27], v[64:67]
	v_mfma_f32_16x16x32_bf16 v[68:71], v[96:99], v[56:59], v[68:71]
	s_waitcnt lgkmcnt(6)
	v_mfma_f32_16x16x32_bf16 v[72:75], v[100:103], v[24:27], v[72:75]
	v_mfma_f32_16x16x32_bf16 v[76:79], v[100:103], v[56:59], v[76:79]
	s_waitcnt lgkmcnt(5)
	v_mfma_f32_16x16x32_bf16 v[80:83], v[104:107], v[24:27], v[80:83]
	v_mfma_f32_16x16x32_bf16 v[84:87], v[104:107], v[56:59], v[84:87]
	s_waitcnt lgkmcnt(4)
	v_mfma_f32_16x16x32_bf16 v[88:91], v[108:111], v[24:27], v[88:91]
	v_mfma_f32_16x16x32_bf16 v[92:95], v[108:111], v[56:59], v[92:95]
	s_waitcnt lgkmcnt(3)
	v_mfma_f32_16x16x32_bf16 v[64:67], v[112:115], v[28:31], v[64:67]
	v_mfma_f32_16x16x32_bf16 v[68:71], v[112:115], v[60:63], v[68:71]
	s_waitcnt lgkmcnt(2)
	v_mfma_f32_16x16x32_bf16 v[72:75], v[116:119], v[28:31], v[72:75]
	v_mfma_f32_16x16x32_bf16 v[76:79], v[116:119], v[60:63], v[76:79]
	s_waitcnt lgkmcnt(1)
	v_mfma_f32_16x16x32_bf16 v[80:83], v[120:123], v[28:31], v[80:83]
	v_mfma_f32_16x16x32_bf16 v[84:87], v[120:123], v[60:63], v[84:87]
	s_waitcnt lgkmcnt(0)
	v_mfma_f32_16x16x32_bf16 v[88:91], v[124:127], v[28:31], v[88:91]
	v_mfma_f32_16x16x32_bf16 v[92:95], v[124:127], v[60:63], v[92:95]
	v_or_b32_e32 v169, 0x10000, v165
	v_or_b32_e32 v170, 0x10000, v166
	v_or_b32_e32 v171, 0x10000, v167
	v_or_b32_e32 v172, 0x10000, v168
	ds_read_u16 v144, v169
	ds_read_u16 v145, v170
	ds_read_u16 v146, v171
	ds_read_u16 v147, v172
	ds_read_u16 v148, v169 offset:8192
	ds_read_u16 v149, v170 offset:8192
	ds_read_u16 v150, v171 offset:8192
	ds_read_u16 v151, v172 offset:8192
	ds_read_u16 v152, v169 offset:16384
	ds_read_u16 v153, v170 offset:16384
	ds_read_u16 v154, v171 offset:16384
	ds_read_u16 v155, v172 offset:16384
	ds_read_u16 v156, v169 offset:24576
	ds_read_u16 v157, v170 offset:24576
	ds_read_u16 v158, v171 offset:24576
	ds_read_u16 v159, v172 offset:24576
	s_nop 7
	v_fma_f32 v178, v64, s53, v173
	v_fma_f32 v179, v65, s53, v173
	v_fma_f32 v180, v66, s53, v173
	v_fma_f32 v181, v67, s53, v173
	v_fma_f32 v182, v72, s53, v173
	v_fma_f32 v183, v73, s53, v173
	v_fma_f32 v184, v74, s53, v173
	v_fma_f32 v185, v75, s53, v173
	v_fma_f32 v186, v68, s53, v174
	v_fma_f32 v187, v69, s53, v174
	v_fma_f32 v188, v70, s53, v174
	v_fma_f32 v189, v71, s53, v174
	v_fma_f32 v190, v76, s53, v174
	v_fma_f32 v191, v77, s53, v174
	v_fma_f32 v192, v78, s53, v174
	v_fma_f32 v193, v79, s53, v174
	v_exp_f32_e32 v178, v178
	v_exp_f32_e32 v179, v179
	v_exp_f32_e32 v180, v180
	v_exp_f32_e32 v181, v181
	v_exp_f32_e32 v182, v182
	v_exp_f32_e32 v183, v183
	v_exp_f32_e32 v184, v184
	v_exp_f32_e32 v185, v185
	v_exp_f32_e32 v186, v186
	v_exp_f32_e32 v187, v187
	v_exp_f32_e32 v188, v188
	v_exp_f32_e32 v189, v189
	v_exp_f32_e32 v190, v190
	v_exp_f32_e32 v191, v191
	v_exp_f32_e32 v192, v192
	v_exp_f32_e32 v193, v193
	v_add_f32_e32 v178, 1.0, v178
	v_add_f32_e32 v179, 1.0, v179
	v_add_f32_e32 v180, 1.0, v180
	v_add_f32_e32 v181, 1.0, v181
	v_add_f32_e32 v182, 1.0, v182
	v_add_f32_e32 v183, 1.0, v183
	v_add_f32_e32 v184, 1.0, v184
	v_add_f32_e32 v185, 1.0, v185
	v_add_f32_e32 v186, 1.0, v186
	v_add_f32_e32 v187, 1.0, v187
	v_add_f32_e32 v188, 1.0, v188
	v_add_f32_e32 v189, 1.0, v189
	v_add_f32_e32 v190, 1.0, v190
	v_add_f32_e32 v191, 1.0, v191
	v_add_f32_e32 v192, 1.0, v192
	v_add_f32_e32 v193, 1.0, v193
	v_rcp_f32_e32 v178, v178
	v_rcp_f32_e32 v179, v179
	v_rcp_f32_e32 v180, v180
	v_rcp_f32_e32 v181, v181
	v_rcp_f32_e32 v182, v182
	v_rcp_f32_e32 v183, v183
	v_rcp_f32_e32 v184, v184
	v_rcp_f32_e32 v185, v185
	v_rcp_f32_e32 v186, v186
	v_rcp_f32_e32 v187, v187
	v_rcp_f32_e32 v188, v188
	v_rcp_f32_e32 v189, v189
	v_rcp_f32_e32 v190, v190
	v_rcp_f32_e32 v191, v191
	v_rcp_f32_e32 v192, v192
	v_rcp_f32_e32 v193, v193
	v_mul_f32_e32 v178, v175, v178
	v_mul_f32_e32 v179, v175, v179
	v_mul_f32_e32 v180, v175, v180
	v_mul_f32_e32 v181, v175, v181
	v_mul_f32_e32 v182, v175, v182
	v_mul_f32_e32 v183, v175, v183
	v_mul_f32_e32 v184, v175, v184
	v_mul_f32_e32 v185, v175, v185
	v_exp_f32_e32 v96, v178
	v_exp_f32_e32 v97, v179
	v_exp_f32_e32 v98, v180
	v_exp_f32_e32 v99, v181
	v_exp_f32_e32 v100, v182
	v_exp_f32_e32 v101, v183
	v_exp_f32_e32 v102, v184
	v_exp_f32_e32 v103, v185
	s_nop 0
	v_fma_f32 v194, -v96, v96, 1.0
	v_fma_f32 v195, -v97, v97, 1.0
	v_fma_f32 v196, -v98, v98, 1.0
	v_fma_f32 v197, -v99, v99, 1.0
	v_fma_f32 v198, -v100, v100, 1.0
	v_fma_f32 v199, -v101, v101, 1.0
	v_fma_f32 v200, -v102, v102, 1.0
	v_fma_f32 v201, -v103, v103, 1.0
	v_max_f32_e32 v194, 0, v194
	v_max_f32_e32 v195, 0, v195
	v_max_f32_e32 v196, 0, v196
	v_max_f32_e32 v197, 0, v197
	v_max_f32_e32 v198, 0, v198
	v_max_f32_e32 v199, 0, v199
	v_max_f32_e32 v200, 0, v200
	v_max_f32_e32 v201, 0, v201
	v_sqrt_f32_e32 v194, v194
	v_sqrt_f32_e32 v195, v195
	v_sqrt_f32_e32 v196, v196
	v_sqrt_f32_e32 v197, v197
	v_sqrt_f32_e32 v198, v198
	v_sqrt_f32_e32 v199, v199
	v_sqrt_f32_e32 v200, v200
	v_sqrt_f32_e32 v201, v201
	s_waitcnt lgkmcnt(8)
	v_lshlrev_b32_e32 v144, 16, v144
	v_lshlrev_b32_e32 v145, 16, v145
	v_lshlrev_b32_e32 v146, 16, v146
	v_lshlrev_b32_e32 v147, 16, v147
	v_lshlrev_b32_e32 v148, 16, v148
	v_lshlrev_b32_e32 v149, 16, v149
	v_lshlrev_b32_e32 v150, 16, v150
	v_lshlrev_b32_e32 v151, 16, v151
	v_mul_f32_e32 v194, v194, v186
	v_mul_f32_e32 v195, v195, v187
	v_mul_f32_e32 v196, v196, v188
	v_mul_f32_e32 v197, v197, v189
	v_mul_f32_e32 v198, v198, v190
	v_mul_f32_e32 v199, v199, v191
	v_mul_f32_e32 v200, v200, v192
	v_mul_f32_e32 v201, v201, v193
	v_mul_f32_e32 v144, v194, v144
	v_mul_f32_e32 v145, v195, v145
	v_mul_f32_e32 v146, v196, v146
	v_mul_f32_e32 v147, v197, v147
	v_mul_f32_e32 v148, v198, v148
	v_mul_f32_e32 v149, v199, v149
	v_mul_f32_e32 v150, v200, v150
	v_mul_f32_e32 v151, v201, v151
	v_fma_f32 v178, v80, s53, v173
	v_fma_f32 v179, v81, s53, v173
	v_fma_f32 v180, v82, s53, v173
	v_fma_f32 v181, v83, s53, v173
	v_fma_f32 v182, v88, s53, v173
	v_fma_f32 v183, v89, s53, v173
	v_fma_f32 v184, v90, s53, v173
	v_fma_f32 v185, v91, s53, v173
	v_fma_f32 v186, v84, s53, v174
	v_fma_f32 v187, v85, s53, v174
	v_fma_f32 v188, v86, s53, v174
	v_fma_f32 v189, v87, s53, v174
	v_fma_f32 v190, v92, s53, v174
	v_fma_f32 v191, v93, s53, v174
	v_fma_f32 v192, v94, s53, v174
	v_fma_f32 v193, v95, s53, v174
	v_exp_f32_e32 v178, v178
	v_exp_f32_e32 v179, v179
	v_exp_f32_e32 v180, v180
	v_exp_f32_e32 v181, v181
	v_exp_f32_e32 v182, v182
	v_exp_f32_e32 v183, v183
	v_exp_f32_e32 v184, v184
	v_exp_f32_e32 v185, v185
	v_exp_f32_e32 v186, v186
	v_exp_f32_e32 v187, v187
	v_exp_f32_e32 v188, v188
	v_exp_f32_e32 v189, v189
	v_exp_f32_e32 v190, v190
	v_exp_f32_e32 v191, v191
	v_exp_f32_e32 v192, v192
	v_exp_f32_e32 v193, v193
	v_add_f32_e32 v178, 1.0, v178
	v_add_f32_e32 v179, 1.0, v179
	v_add_f32_e32 v180, 1.0, v180
	v_add_f32_e32 v181, 1.0, v181
	v_add_f32_e32 v182, 1.0, v182
	v_add_f32_e32 v183, 1.0, v183
	v_add_f32_e32 v184, 1.0, v184
	v_add_f32_e32 v185, 1.0, v185
	v_add_f32_e32 v186, 1.0, v186
	v_add_f32_e32 v187, 1.0, v187
	v_add_f32_e32 v188, 1.0, v188
	v_add_f32_e32 v189, 1.0, v189
	v_add_f32_e32 v190, 1.0, v190
	v_add_f32_e32 v191, 1.0, v191
	v_add_f32_e32 v192, 1.0, v192
	v_add_f32_e32 v193, 1.0, v193
	v_rcp_f32_e32 v178, v178
	v_rcp_f32_e32 v179, v179
	v_rcp_f32_e32 v180, v180
	v_rcp_f32_e32 v181, v181
	v_rcp_f32_e32 v182, v182
	v_rcp_f32_e32 v183, v183
	v_rcp_f32_e32 v184, v184
	v_rcp_f32_e32 v185, v185
	v_rcp_f32_e32 v186, v186
	v_rcp_f32_e32 v187, v187
	v_rcp_f32_e32 v188, v188
	v_rcp_f32_e32 v189, v189
	v_rcp_f32_e32 v190, v190
	v_rcp_f32_e32 v191, v191
	v_rcp_f32_e32 v192, v192
	v_rcp_f32_e32 v193, v193
	v_mul_f32_e32 v178, v175, v178
	v_mul_f32_e32 v179, v175, v179
	v_mul_f32_e32 v180, v175, v180
	v_mul_f32_e32 v181, v175, v181
	v_mul_f32_e32 v182, v175, v182
	v_mul_f32_e32 v183, v175, v183
	v_mul_f32_e32 v184, v175, v184
	v_mul_f32_e32 v185, v175, v185
	v_exp_f32_e32 v104, v178
	v_exp_f32_e32 v105, v179
	v_exp_f32_e32 v106, v180
	v_exp_f32_e32 v107, v181
	v_exp_f32_e32 v108, v182
	v_exp_f32_e32 v109, v183
	v_exp_f32_e32 v110, v184
	v_exp_f32_e32 v111, v185
	s_nop 0
	v_fma_f32 v194, -v104, v104, 1.0
	v_fma_f32 v195, -v105, v105, 1.0
	v_fma_f32 v196, -v106, v106, 1.0
	v_fma_f32 v197, -v107, v107, 1.0
	v_fma_f32 v198, -v108, v108, 1.0
	v_fma_f32 v199, -v109, v109, 1.0
	v_fma_f32 v200, -v110, v110, 1.0
	v_fma_f32 v201, -v111, v111, 1.0
	v_max_f32_e32 v194, 0, v194
	v_max_f32_e32 v195, 0, v195
	v_max_f32_e32 v196, 0, v196
	v_max_f32_e32 v197, 0, v197
	v_max_f32_e32 v198, 0, v198
	v_max_f32_e32 v199, 0, v199
	v_max_f32_e32 v200, 0, v200
	v_max_f32_e32 v201, 0, v201
	v_sqrt_f32_e32 v194, v194
	v_sqrt_f32_e32 v195, v195
	v_sqrt_f32_e32 v196, v196
	v_sqrt_f32_e32 v197, v197
	v_sqrt_f32_e32 v198, v198
	v_sqrt_f32_e32 v199, v199
	v_sqrt_f32_e32 v200, v200
	v_sqrt_f32_e32 v201, v201
	s_waitcnt lgkmcnt(0)
	v_lshlrev_b32_e32 v152, 16, v152
	v_lshlrev_b32_e32 v153, 16, v153
	v_lshlrev_b32_e32 v154, 16, v154
	v_lshlrev_b32_e32 v155, 16, v155
	v_lshlrev_b32_e32 v156, 16, v156
	v_lshlrev_b32_e32 v157, 16, v157
	v_lshlrev_b32_e32 v158, 16, v158
	v_lshlrev_b32_e32 v159, 16, v159
	v_mul_f32_e32 v194, v194, v186
	v_mul_f32_e32 v195, v195, v187
	v_mul_f32_e32 v196, v196, v188
	v_mul_f32_e32 v197, v197, v189
	v_mul_f32_e32 v198, v198, v190
	v_mul_f32_e32 v199, v199, v191
	v_mul_f32_e32 v200, v200, v192
	v_mul_f32_e32 v201, v201, v193
	v_mul_f32_e32 v152, v194, v152
	v_mul_f32_e32 v153, v195, v153
	v_mul_f32_e32 v154, v196, v154
	v_mul_f32_e32 v155, v197, v155
	v_mul_f32_e32 v156, v198, v156
	v_mul_f32_e32 v157, v199, v157
	v_mul_f32_e32 v158, v200, v158
	v_mul_f32_e32 v159, v201, v159
	v_fma_f32 v146, v98, v147, v146
	v_fma_f32 v150, v102, v151, v150
	v_fma_f32 v154, v106, v155, v154
	v_fma_f32 v158, v110, v159, v158
	v_mul_f32_e32 v98, v98, v99
	v_mul_f32_e32 v102, v102, v103
	v_mul_f32_e32 v106, v106, v107
	v_mul_f32_e32 v110, v110, v111
	v_fma_f32 v145, v97, v146, v145
	v_fma_f32 v149, v101, v150, v149
	v_fma_f32 v153, v105, v154, v153
	v_fma_f32 v157, v109, v158, v157
	v_mul_f32_e32 v97, v97, v98
	v_mul_f32_e32 v101, v101, v102
	v_mul_f32_e32 v105, v105, v106
	v_mul_f32_e32 v109, v109, v110
	v_fma_f32 v144, v96, v145, v144
	v_fma_f32 v148, v100, v149, v148
	v_fma_f32 v152, v104, v153, v152
	v_fma_f32 v156, v108, v157, v156
	v_mul_f32_e32 v96, v96, v97
	v_mul_f32_e32 v100, v100, v101
	v_mul_f32_e32 v104, v104, v105
	v_mul_f32_e32 v108, v108, v109
	ds_bpermute_b32 v178, v204, v96
	ds_bpermute_b32 v182, v204, v144
	ds_bpermute_b32 v179, v204, v100
	ds_bpermute_b32 v183, v204, v148
	ds_bpermute_b32 v180, v204, v104
	ds_bpermute_b32 v184, v204, v152
	ds_bpermute_b32 v181, v204, v108
	ds_bpermute_b32 v185, v204, v156
	s_waitcnt lgkmcnt(0)
	v_fma_f32 v186, v182, v96, v144
	v_cndmask_b32_e64 v178, 1.0, v178, s[34:35]
	v_fma_f32 v187, v183, v100, v148
	v_cndmask_b32_e64 v179, 1.0, v179, s[34:35]
	v_fma_f32 v188, v184, v104, v152
	v_cndmask_b32_e64 v180, 1.0, v180, s[34:35]
	v_fma_f32 v189, v185, v108, v156
	v_cndmask_b32_e64 v181, 1.0, v181, s[34:35]
	v_cndmask_b32_e64 v223, v144, v186, s[34:35]
	v_mul_f32_e32 v219, v96, v178
	v_cndmask_b32_e64 v224, v148, v187, s[34:35]
	v_mul_f32_e32 v220, v100, v179
	v_cndmask_b32_e64 v225, v152, v188, s[34:35]
	v_mul_f32_e32 v221, v104, v180
	v_cndmask_b32_e64 v226, v156, v189, s[34:35]
	v_mul_f32_e32 v222, v108, v181
	ds_bpermute_b32 v178, v205, v219
	ds_bpermute_b32 v182, v205, v223
	ds_bpermute_b32 v179, v205, v220
	ds_bpermute_b32 v183, v205, v224
	ds_bpermute_b32 v180, v205, v221
	ds_bpermute_b32 v184, v205, v225
	ds_bpermute_b32 v181, v205, v222
	ds_bpermute_b32 v185, v205, v226
	s_waitcnt lgkmcnt(0)
	v_fma_f32 v186, v182, v219, v223
	v_cndmask_b32_e64 v178, 1.0, v178, s[36:37]
	v_fma_f32 v187, v183, v220, v224
	v_cndmask_b32_e64 v179, 1.0, v179, s[36:37]
	v_fma_f32 v188, v184, v221, v225
	v_cndmask_b32_e64 v180, 1.0, v180, s[36:37]
	v_fma_f32 v189, v185, v222, v226
	v_cndmask_b32_e64 v181, 1.0, v181, s[36:37]
	v_cndmask_b32_e64 v223, v223, v186, s[36:37]
	v_mul_f32_e32 v219, v219, v178
	v_cndmask_b32_e64 v224, v224, v187, s[36:37]
	v_mul_f32_e32 v220, v220, v179
	v_cndmask_b32_e64 v225, v225, v188, s[36:37]
	v_mul_f32_e32 v221, v221, v180
	v_cndmask_b32_e64 v226, v226, v189, s[36:37]
	v_mul_f32_e32 v222, v222, v181
	ds_bpermute_b32 v227, v204, v219
	ds_bpermute_b32 v231, v204, v223
	ds_bpermute_b32 v235, v206, v219
	ds_bpermute_b32 v239, v206, v223
	ds_bpermute_b32 v228, v204, v220
	ds_bpermute_b32 v232, v204, v224
	ds_bpermute_b32 v236, v206, v220
	ds_bpermute_b32 v244, v206, v224
	ds_bpermute_b32 v229, v204, v221
	ds_bpermute_b32 v233, v204, v225
	ds_bpermute_b32 v237, v206, v221
	ds_bpermute_b32 v245, v206, v225
	ds_bpermute_b32 v230, v204, v222
	ds_bpermute_b32 v234, v204, v226
	ds_bpermute_b32 v238, v206, v222
	ds_bpermute_b32 v246, v206, v226
	s_waitcnt lgkmcnt(0)
	v_cndmask_b32_e64 v227, 1.0, v227, s[34:35]
	v_cndmask_b32_e64 v231, 0, v231, s[34:35]
	v_cndmask_b32_e64 v228, 1.0, v228, s[34:35]
	v_cndmask_b32_e64 v232, 0, v232, s[34:35]
	v_cndmask_b32_e64 v229, 1.0, v229, s[34:35]
	v_cndmask_b32_e64 v233, 0, v233, s[34:35]
	v_cndmask_b32_e64 v230, 1.0, v230, s[34:35]
	v_cndmask_b32_e64 v234, 0, v234, s[34:35]
	v_mov_b32_e32 v190, v238
	v_mov_b32_e32 v194, v246
	v_mov_b32_e32 v198, v190
	v_mov_b32_e32 v201, v194
	v_fma_f32 v194, v194, v237, v245
	v_mul_f32_e32 v190, v190, v237
	v_mov_b32_e32 v199, v190
	v_mov_b32_e32 v177, v194
	v_fma_f32 v194, v194, v236, v244
	v_mul_f32_e32 v190, v190, v236
	v_mov_b32_e32 v200, v190
	v_mov_b32_e32 v203, v194
	v_fma_f32 v194, v194, v235, v239
	v_mul_f32_e32 v190, v190, v235
	v_mov_b32_e32 v191, v194
	ds_write_b64 v207, v[190:191] offset:1024
	s_waitcnt lgkmcnt(0)
	s_barrier
	ds_read_b64 v[178:179], v208 offset:1536
	ds_read_b64 v[180:181], v208 offset:1024
	s_waitcnt lgkmcnt(0)
	v_fma_f32 v182, v176, v178, v179
	v_cndmask_b32_e64 v183, v176, v182, s[38:39]
	v_fma_f32 v176, v182, v180, v181
	v_fma_f32 v184, v183, v200, v203
	v_fma_f32 v185, v183, v199, v177
	v_fma_f32 v186, v183, v198, v201
	v_mov_b32_e32 v187, v183
	v_fma_f32 v184, v184, v227, v231
	v_fma_f32 v185, v185, v228, v232
	v_fma_f32 v186, v186, v229, v233
	v_fma_f32 v187, v187, v230, v234
	v_fma_f32 v144, v184, v96, v144
	v_fma_f32 v148, v185, v100, v148
	v_fma_f32 v152, v186, v104, v152
	v_fma_f32 v156, v187, v108, v156
	v_fma_f32 v145, v184, v97, v145
	v_fma_f32 v149, v185, v101, v149
	v_fma_f32 v153, v186, v105, v153
	v_fma_f32 v157, v187, v109, v157
	v_fma_f32 v146, v184, v98, v146
	v_fma_f32 v150, v185, v102, v150
	v_fma_f32 v154, v186, v106, v154
	v_fma_f32 v158, v187, v110, v158
	v_fma_f32 v147, v184, v99, v147
	v_fma_f32 v151, v185, v103, v151
	v_fma_f32 v155, v186, v107, v155
	v_fma_f32 v159, v187, v111, v159
	s_cmp_eq_u32 s13, 17
	s_cbranch_scc1 .Lmylru_w0_8
	s_waitcnt vmcnt(8)
	s_branch .Lmylru_w1_8

.Lmylru_w1_8:
	v_lshlrev_b32_e32 v178, 16, v247
	v_add_f32_e32 v144, v144, v178
	v_lshlrev_b32_e32 v128, 16, v128
	v_mul_f32_e32 v144, v144, v128
	v_cvt_pk_bf16_f32 v144, v144, v144
	v_and_b32_e32 v179, 0xffff0000, v247
	v_add_f32_e32 v145, v145, v179
	v_lshlrev_b32_e32 v129, 16, v129
	v_mul_f32_e32 v145, v145, v129
	v_cvt_pk_bf16_f32 v145, v145, v145
	v_lshlrev_b32_e32 v180, 16, v248
	v_add_f32_e32 v146, v146, v180
	v_lshlrev_b32_e32 v130, 16, v130
	v_mul_f32_e32 v146, v146, v130
	v_cvt_pk_bf16_f32 v146, v146, v146
	v_and_b32_e32 v181, 0xffff0000, v248
	v_add_f32_e32 v147, v147, v181
	v_lshlrev_b32_e32 v131, 16, v131
	v_mul_f32_e32 v147, v147, v131
	v_cvt_pk_bf16_f32 v147, v147, v147
	v_lshlrev_b32_e32 v178, 16, v249
	v_add_f32_e32 v148, v148, v178
	v_lshlrev_b32_e32 v132, 16, v132
	v_mul_f32_e32 v148, v148, v132
	v_cvt_pk_bf16_f32 v148, v148, v148
	v_and_b32_e32 v179, 0xffff0000, v249
	v_add_f32_e32 v149, v149, v179
	v_lshlrev_b32_e32 v133, 16, v133
	v_mul_f32_e32 v149, v149, v133
	v_cvt_pk_bf16_f32 v149, v149, v149
	v_lshlrev_b32_e32 v180, 16, v250
	v_add_f32_e32 v150, v150, v180
	v_lshlrev_b32_e32 v134, 16, v134
	v_mul_f32_e32 v150, v150, v134
	v_cvt_pk_bf16_f32 v150, v150, v150
	v_and_b32_e32 v181, 0xffff0000, v250
	v_add_f32_e32 v151, v151, v181
	v_lshlrev_b32_e32 v135, 16, v135
	v_mul_f32_e32 v151, v151, v135
	v_cvt_pk_bf16_f32 v151, v151, v151
	v_lshlrev_b32_e32 v178, 16, v251
	v_add_f32_e32 v152, v152, v178
	v_lshlrev_b32_e32 v136, 16, v136
	v_mul_f32_e32 v152, v152, v136
	v_cvt_pk_bf16_f32 v152, v152, v152
	v_and_b32_e32 v179, 0xffff0000, v251
	v_add_f32_e32 v153, v153, v179
	v_lshlrev_b32_e32 v137, 16, v137
	v_mul_f32_e32 v153, v153, v137
	v_cvt_pk_bf16_f32 v153, v153, v153
	v_lshlrev_b32_e32 v180, 16, v252
	v_add_f32_e32 v154, v154, v180
	v_lshlrev_b32_e32 v138, 16, v138
	v_mul_f32_e32 v154, v154, v138
	v_cvt_pk_bf16_f32 v154, v154, v154
	v_and_b32_e32 v181, 0xffff0000, v252
	v_add_f32_e32 v155, v155, v181
	v_lshlrev_b32_e32 v139, 16, v139
	v_mul_f32_e32 v155, v155, v139
	v_cvt_pk_bf16_f32 v155, v155, v155
	v_lshlrev_b32_e32 v178, 16, v253
	v_add_f32_e32 v156, v156, v178
	v_lshlrev_b32_e32 v140, 16, v140
	v_mul_f32_e32 v156, v156, v140
	v_cvt_pk_bf16_f32 v156, v156, v156
	v_and_b32_e32 v179, 0xffff0000, v253
	v_add_f32_e32 v157, v157, v179
	v_lshlrev_b32_e32 v141, 16, v141
	v_mul_f32_e32 v157, v157, v141
	v_cvt_pk_bf16_f32 v157, v157, v157
	v_lshlrev_b32_e32 v180, 16, v254
	v_add_f32_e32 v158, v158, v180
	v_lshlrev_b32_e32 v142, 16, v142
	v_mul_f32_e32 v158, v158, v142
	v_cvt_pk_bf16_f32 v158, v158, v158
	v_and_b32_e32 v181, 0xffff0000, v254
	v_add_f32_e32 v159, v159, v181
	v_lshlrev_b32_e32 v143, 16, v143
	v_mul_f32_e32 v159, v159, v143
	v_cvt_pk_bf16_f32 v159, v159, v159
	v_add_u32_e32 v182, 0x0, v210
	v_add_u32_e32 v183, 0x1000, v182
	global_store_short v182, v144, s[42:43]
	global_store_short v182, v145, s[42:43] offset:2048
	global_store_short v183, v146, s[42:43]
	global_store_short v183, v147, s[42:43] offset:2048
	v_add_u32_e32 v182, 0x8000, v210
	v_add_u32_e32 v183, 0x1000, v182
	global_store_short v182, v148, s[42:43]
	global_store_short v182, v149, s[42:43] offset:2048
	global_store_short v183, v150, s[42:43]
	global_store_short v183, v151, s[42:43] offset:2048
	v_add_u32_e32 v182, 0x10000, v210
	v_add_u32_e32 v183, 0x1000, v182
	global_store_short v182, v152, s[42:43]
	global_store_short v182, v153, s[42:43] offset:2048
	global_store_short v183, v154, s[42:43]
	global_store_short v183, v155, s[42:43] offset:2048
	v_add_u32_e32 v182, 0x18000, v210
	v_add_u32_e32 v183, 0x1000, v182
	global_store_short v182, v156, s[42:43]
	global_store_short v182, v157, s[42:43] offset:2048
	global_store_short v183, v158, s[42:43]
	global_store_short v183, v159, s[42:43] offset:2048
	s_add_i32 s13, s13, 1
	s_add_i32 s60, s60, -1
	s_cmp_lg_u32 s60, 0
	s_cbranch_scc1 .Lmylru_loop_1
	s_waitcnt vmcnt(0) lgkmcnt(0)
